# speedup vs baseline: 1.1276x; 1.0117x over previous
.LBB8_27:
	ds_read_b128 v[72:75], v231
	ds_read_b128 v[80:83], v231 offset:1024
	ds_read_b128 v[88:91], v231 offset:2048
	ds_read_b128 v[92:95], v231 offset:3072
	s_add_u32 s40, s38, 0xfffd0080
	s_addc_u32 s41, s39, -1
	s_cmp_eq_u32 s87, 8
	s_cselect_b32 s43, s9, s41
	s_cselect_b32 s42, s8, s40
	s_cselect_b32 s41, s1, s86
	s_cselect_b32 s40, s0, s85
	v_lshl_add_u64 v[190:191], s[38:39], 0, v[184:185]
	s_add_i32 m0, s51, 0xc000
	ds_read_b128 v[136:139], v232
	ds_read_b128 v[148:151], v232 offset:1024
	ds_read_b128 v[152:155], v232 offset:2048
	ds_read_b128 v[156:159], v232 offset:3072
	ds_read_b128 v[160:163], v232 offset:4096
	ds_read_b128 v[164:167], v232 offset:5120
	ds_read_b128 v[168:171], v232 offset:6144
	ds_read_b128 v[172:175], v232 offset:7168
	global_load_lds_dwordx4 v[190:191], off
	v_lshl_add_u64 v[190:191], s[38:39], 0, v[186:187]
	s_add_i32 m0, s51, 0xe000
	s_nop 0
	global_load_lds_dwordx4 v[190:191], off
	s_waitcnt lgkmcnt(8)
	s_barrier
	s_waitcnt lgkmcnt(0)
	s_setprio 1
	s_waitcnt lgkmcnt(0)
	v_mfma_f32_16x16x32_f16 v[144:147], v[72:75], v[136:139], v[144:147]
	v_mfma_f32_16x16x32_f16 v[140:143], v[88:91], v[136:139], v[140:143]
	v_mfma_f32_16x16x32_f16 v[124:127], v[72:75], v[152:155], v[124:127]
	v_mfma_f32_16x16x32_f16 v[120:123], v[88:91], v[152:155], v[120:123]
	v_mfma_f32_16x16x32_f16 v[108:111], v[72:75], v[160:163], v[108:111]
	v_mfma_f32_16x16x32_f16 v[104:107], v[88:91], v[160:163], v[104:107]
	v_mfma_f32_16x16x32_f16 v[84:87], v[72:75], v[168:171], v[84:87]
	v_mfma_f32_16x16x32_f16 v[76:79], v[88:91], v[168:171], v[76:79]
	v_mfma_f32_16x16x32_f16 v[144:147], v[80:83], v[148:151], v[144:147]
	v_mfma_f32_16x16x32_f16 v[140:143], v[92:95], v[148:151], v[140:143]
	v_mfma_f32_16x16x32_f16 v[124:127], v[80:83], v[156:159], v[124:127]
	v_mfma_f32_16x16x32_f16 v[120:123], v[92:95], v[156:159], v[120:123]
	v_mfma_f32_16x16x32_f16 v[108:111], v[80:83], v[164:167], v[108:111]
	v_mfma_f32_16x16x32_f16 v[104:107], v[92:95], v[164:167], v[104:107]
	v_mfma_f32_16x16x32_f16 v[84:87], v[80:83], v[172:175], v[84:87]
	v_mfma_f32_16x16x32_f16 v[76:79], v[92:95], v[172:175], v[76:79]
	s_setprio 0
	s_barrier
	s_add_i32 s88, s70, s50
	v_lshl_add_u64 v[206:207], s[40:41], 0, v[178:179]
	s_mov_b32 m0, s88
	ds_read_b128 v[190:193], v233
	ds_read_b128 v[194:197], v233 offset:1024
	ds_read_b128 v[198:201], v233 offset:2048
	ds_read_b128 v[202:205], v233 offset:3072
	global_load_lds_dwordx4 v[206:207], off
	v_lshl_add_u64 v[208:209], s[40:41], 0, v[182:183]
	s_add_i32 m0, s88, 0x2000
	s_nop 0
	global_load_lds_dwordx4 v[208:209], off
	s_barrier
	s_waitcnt lgkmcnt(0)
	s_setprio 1
	s_waitcnt lgkmcnt(0)
	v_mfma_f32_16x16x32_f16 v[132:135], v[190:193], v[136:139], v[132:135]
	v_mfma_f32_16x16x32_f16 v[128:131], v[198:201], v[136:139], v[128:131]
	v_mfma_f32_16x16x32_f16 v[116:119], v[190:193], v[152:155], v[116:119]
	v_mfma_f32_16x16x32_f16 v[112:115], v[198:201], v[152:155], v[112:115]
	v_mfma_f32_16x16x32_f16 v[100:103], v[190:193], v[160:163], v[100:103]
	v_mfma_f32_16x16x32_f16 v[96:99], v[198:201], v[160:163], v[96:99]
	v_mfma_f32_16x16x32_f16 v[68:71], v[190:193], v[168:171], v[68:71]
	v_mfma_f32_16x16x32_f16 v[64:67], v[198:201], v[168:171], v[64:67]
	v_mfma_f32_16x16x32_f16 v[132:135], v[194:197], v[148:151], v[132:135]
	v_mfma_f32_16x16x32_f16 v[128:131], v[202:205], v[148:151], v[128:131]
	v_mfma_f32_16x16x32_f16 v[116:119], v[194:197], v[156:159], v[116:119]
	v_mfma_f32_16x16x32_f16 v[112:115], v[202:205], v[156:159], v[112:115]
	v_mfma_f32_16x16x32_f16 v[100:103], v[194:197], v[164:167], v[100:103]
	v_mfma_f32_16x16x32_f16 v[96:99], v[202:205], v[164:167], v[96:99]
	v_mfma_f32_16x16x32_f16 v[68:71], v[194:197], v[172:175], v[68:71]
	v_mfma_f32_16x16x32_f16 v[64:67], v[202:205], v[172:175], v[64:67]
	s_setprio 0
	s_mov_b32 m0, s51
	v_lshl_add_u64 v[210:211], s[42:43], 0, v[176:177]
	s_barrier
	ds_read_b128 v[136:139], v232 offset:16384
	ds_read_b128 v[148:151], v232 offset:17408
	ds_read_b128 v[152:155], v232 offset:18432
	ds_read_b128 v[156:159], v232 offset:19456
	ds_read_b128 v[160:163], v232 offset:20480
	ds_read_b128 v[164:167], v232 offset:21504
	ds_read_b128 v[168:171], v232 offset:22528
	ds_read_b128 v[172:175], v232 offset:23552
	global_load_lds_dwordx4 v[210:211], off
	v_lshl_add_u64 v[212:213], s[42:43], 0, v[180:181]
	s_mov_b32 m0, s52
	s_nop 0
	global_load_lds_dwordx4 v[212:213], off
	s_barrier
	s_waitcnt lgkmcnt(0)
	s_setprio 1
	s_waitcnt lgkmcnt(0)
	v_mfma_f32_16x16x32_f16 v[60:63], v[72:75], v[136:139], v[60:63]
	v_mfma_f32_16x16x32_f16 v[56:59], v[88:91], v[136:139], v[56:59]
	v_mfma_f32_16x16x32_f16 v[44:47], v[72:75], v[152:155], v[44:47]
	v_mfma_f32_16x16x32_f16 v[40:43], v[88:91], v[152:155], v[40:43]
	v_mfma_f32_16x16x32_f16 v[28:31], v[72:75], v[160:163], v[28:31]
	v_mfma_f32_16x16x32_f16 v[24:27], v[88:91], v[160:163], v[24:27]
	v_mfma_f32_16x16x32_f16 v[12:15], v[72:75], v[168:171], v[12:15]
	v_mfma_f32_16x16x32_f16 v[8:11], v[88:91], v[168:171], v[8:11]
	v_mfma_f32_16x16x32_f16 v[60:63], v[80:83], v[148:151], v[60:63]
	v_mfma_f32_16x16x32_f16 v[56:59], v[92:95], v[148:151], v[56:59]
	v_mfma_f32_16x16x32_f16 v[44:47], v[80:83], v[156:159], v[44:47]
	v_mfma_f32_16x16x32_f16 v[40:43], v[92:95], v[156:159], v[40:43]
	v_mfma_f32_16x16x32_f16 v[28:31], v[80:83], v[164:167], v[28:31]
	v_mfma_f32_16x16x32_f16 v[24:27], v[92:95], v[164:167], v[24:27]
	v_mfma_f32_16x16x32_f16 v[12:15], v[80:83], v[172:175], v[12:15]
	v_mfma_f32_16x16x32_f16 v[8:11], v[92:95], v[172:175], v[8:11]
	s_setprio 0
	s_barrier
	s_add_u32 s88, s40, 0xc000
	s_addc_u32 s89, s41, 0
	s_add_i32 s90, s71, s50
	v_lshl_add_u64 v[72:73], s[88:89], 0, v[178:179]
	s_mov_b32 m0, s90
	s_nop 0
	global_load_lds_dwordx4 v[72:73], off
	v_lshl_add_u64 v[72:73], s[88:89], 0, v[182:183]
	s_add_i32 m0, s90, 0x2000
	s_nop 0
	global_load_lds_dwordx4 v[72:73], off
	s_waitcnt vmcnt(6)
	s_barrier
	s_setprio 1
	v_mfma_f32_16x16x32_f16 v[52:55], v[190:193], v[136:139], v[52:55]
	v_mfma_f32_16x16x32_f16 v[48:51], v[198:201], v[136:139], v[48:51]
	v_mfma_f32_16x16x32_f16 v[36:39], v[190:193], v[152:155], v[36:39]
	v_mfma_f32_16x16x32_f16 v[32:35], v[198:201], v[152:155], v[32:35]
	v_mfma_f32_16x16x32_f16 v[20:23], v[190:193], v[160:163], v[20:23]
	v_mfma_f32_16x16x32_f16 v[16:19], v[198:201], v[160:163], v[16:19]
	v_mfma_f32_16x16x32_f16 v[4:7], v[190:193], v[168:171], v[4:7]
	v_mfma_f32_16x16x32_f16 v[0:3], v[198:201], v[168:171], v[0:3]
	v_mfma_f32_16x16x32_f16 v[52:55], v[194:197], v[148:151], v[52:55]
	v_mfma_f32_16x16x32_f16 v[48:51], v[202:205], v[148:151], v[48:51]
	v_mfma_f32_16x16x32_f16 v[36:39], v[194:197], v[156:159], v[36:39]
	v_mfma_f32_16x16x32_f16 v[32:35], v[202:205], v[156:159], v[32:35]
	v_mfma_f32_16x16x32_f16 v[20:23], v[194:197], v[164:167], v[20:23]
	v_mfma_f32_16x16x32_f16 v[16:19], v[202:205], v[164:167], v[16:19]
	v_mfma_f32_16x16x32_f16 v[4:7], v[194:197], v[172:175], v[4:7]
	v_mfma_f32_16x16x32_f16 v[0:3], v[202:205], v[172:175], v[0:3]
	s_setprio 0
	s_add_i32 s88, 0, 0x18000
	v_add_u32_e32 v92, s88, v228
	s_barrier
	ds_read_b128 v[72:75], v92
	ds_read_b128 v[80:83], v92 offset:1024
	ds_read_b128 v[88:91], v92 offset:2048
	ds_read_b128 v[92:95], v92 offset:3072
	s_add_u32 s42, s42, 0x30000
	s_addc_u32 s43, s43, 0
	s_mov_b32 m0, s53
	v_lshl_add_u64 v[190:191], s[42:43], 0, v[176:177]
	ds_read_b128 v[136:139], v232 offset:32768
	ds_read_b128 v[148:151], v232 offset:33792
	ds_read_b128 v[152:155], v232 offset:34816
	ds_read_b128 v[156:159], v232 offset:35840
	ds_read_b128 v[160:163], v232 offset:36864
	ds_read_b128 v[164:167], v232 offset:37888
	ds_read_b128 v[168:171], v232 offset:38912
	ds_read_b128 v[172:175], v232 offset:39936
	global_load_lds_dwordx4 v[190:191], off
	v_lshl_add_u64 v[190:191], s[42:43], 0, v[180:181]
	s_mov_b32 m0, s54
	s_nop 0
	global_load_lds_dwordx4 v[190:191], off
	s_waitcnt lgkmcnt(8)
	s_barrier
	s_waitcnt lgkmcnt(0)
	s_setprio 1
	s_waitcnt lgkmcnt(0)
	v_mfma_f32_16x16x32_f16 v[144:147], v[72:75], v[136:139], v[144:147]
	v_mfma_f32_16x16x32_f16 v[140:143], v[88:91], v[136:139], v[140:143]
	v_mfma_f32_16x16x32_f16 v[124:127], v[72:75], v[152:155], v[124:127]
	v_mfma_f32_16x16x32_f16 v[120:123], v[88:91], v[152:155], v[120:123]
	v_mfma_f32_16x16x32_f16 v[108:111], v[72:75], v[160:163], v[108:111]
	v_mfma_f32_16x16x32_f16 v[104:107], v[88:91], v[160:163], v[104:107]
	v_mfma_f32_16x16x32_f16 v[84:87], v[72:75], v[168:171], v[84:87]
	v_mfma_f32_16x16x32_f16 v[76:79], v[88:91], v[168:171], v[76:79]
	v_mfma_f32_16x16x32_f16 v[144:147], v[80:83], v[148:151], v[144:147]
	v_mfma_f32_16x16x32_f16 v[140:143], v[92:95], v[148:151], v[140:143]
	v_mfma_f32_16x16x32_f16 v[124:127], v[80:83], v[156:159], v[124:127]
	v_mfma_f32_16x16x32_f16 v[120:123], v[92:95], v[156:159], v[120:123]
	v_mfma_f32_16x16x32_f16 v[108:111], v[80:83], v[164:167], v[108:111]
	v_mfma_f32_16x16x32_f16 v[104:107], v[92:95], v[164:167], v[104:107]
	v_mfma_f32_16x16x32_f16 v[84:87], v[80:83], v[172:175], v[84:87]
	v_mfma_f32_16x16x32_f16 v[76:79], v[92:95], v[172:175], v[76:79]
	s_setprio 0
	s_barrier
	s_add_i32 s42, 0, 0x1c000
	s_add_i32 s43, s88, s50
	v_add_u32_e32 v202, s42, v228
	v_lshl_add_u64 v[206:207], v[206:207], 0, s[36:37]
	s_mov_b32 m0, s43
	ds_read_b128 v[190:193], v202
	ds_read_b128 v[194:197], v202 offset:1024
	ds_read_b128 v[198:201], v202 offset:2048
	ds_read_b128 v[202:205], v202 offset:3072
	global_load_lds_dwordx4 v[206:207], off
	v_lshl_add_u64 v[206:207], v[208:209], 0, s[36:37]
	s_add_i32 m0, s43, 0x2000
	s_nop 0
	global_load_lds_dwordx4 v[206:207], off
	s_barrier
	s_waitcnt lgkmcnt(0)
	s_setprio 1
	s_waitcnt lgkmcnt(0)
	v_mfma_f32_16x16x32_f16 v[132:135], v[190:193], v[136:139], v[132:135]
	v_mfma_f32_16x16x32_f16 v[128:131], v[198:201], v[136:139], v[128:131]
	v_mfma_f32_16x16x32_f16 v[116:119], v[190:193], v[152:155], v[116:119]
	v_mfma_f32_16x16x32_f16 v[112:115], v[198:201], v[152:155], v[112:115]
	v_mfma_f32_16x16x32_f16 v[100:103], v[190:193], v[160:163], v[100:103]
	v_mfma_f32_16x16x32_f16 v[96:99], v[198:201], v[160:163], v[96:99]
	v_mfma_f32_16x16x32_f16 v[68:71], v[190:193], v[168:171], v[68:71]
	v_mfma_f32_16x16x32_f16 v[64:67], v[198:201], v[168:171], v[64:67]
	v_mfma_f32_16x16x32_f16 v[132:135], v[194:197], v[148:151], v[132:135]
	v_mfma_f32_16x16x32_f16 v[128:131], v[202:205], v[148:151], v[128:131]
	v_mfma_f32_16x16x32_f16 v[116:119], v[194:197], v[156:159], v[116:119]
	v_mfma_f32_16x16x32_f16 v[112:115], v[202:205], v[156:159], v[112:115]
	v_mfma_f32_16x16x32_f16 v[100:103], v[194:197], v[164:167], v[100:103]
	v_mfma_f32_16x16x32_f16 v[96:99], v[202:205], v[164:167], v[96:99]
	v_mfma_f32_16x16x32_f16 v[68:71], v[194:197], v[172:175], v[68:71]
	v_mfma_f32_16x16x32_f16 v[64:67], v[202:205], v[172:175], v[64:67]
	s_setprio 0
	s_mov_b32 m0, s59
	v_lshl_add_u64 v[206:207], v[210:211], 0, s[36:37]
	s_barrier
	ds_read_b128 v[136:139], v232 offset:49152
	ds_read_b128 v[148:151], v232 offset:50176
	ds_read_b128 v[152:155], v232 offset:51200
	ds_read_b128 v[156:159], v232 offset:52224
	ds_read_b128 v[160:163], v232 offset:53248
	ds_read_b128 v[164:167], v232 offset:54272
	ds_read_b128 v[168:171], v232 offset:55296
	ds_read_b128 v[172:175], v232 offset:56320
	global_load_lds_dwordx4 v[206:207], off
	v_lshl_add_u64 v[206:207], v[212:213], 0, s[36:37]
	s_mov_b32 m0, s60
	s_nop 0
	global_load_lds_dwordx4 v[206:207], off
	s_barrier
	s_waitcnt lgkmcnt(0)
	s_setprio 1
	s_waitcnt lgkmcnt(0)
	v_mfma_f32_16x16x32_f16 v[60:63], v[72:75], v[136:139], v[60:63]
	v_mfma_f32_16x16x32_f16 v[56:59], v[88:91], v[136:139], v[56:59]
	v_mfma_f32_16x16x32_f16 v[44:47], v[72:75], v[152:155], v[44:47]
	v_mfma_f32_16x16x32_f16 v[40:43], v[88:91], v[152:155], v[40:43]
	v_mfma_f32_16x16x32_f16 v[28:31], v[72:75], v[160:163], v[28:31]
	v_mfma_f32_16x16x32_f16 v[24:27], v[88:91], v[160:163], v[24:27]
	v_mfma_f32_16x16x32_f16 v[12:15], v[72:75], v[168:171], v[12:15]
	v_mfma_f32_16x16x32_f16 v[8:11], v[88:91], v[168:171], v[8:11]
	v_mfma_f32_16x16x32_f16 v[60:63], v[80:83], v[148:151], v[60:63]
	v_mfma_f32_16x16x32_f16 v[56:59], v[92:95], v[148:151], v[56:59]
	v_mfma_f32_16x16x32_f16 v[44:47], v[80:83], v[156:159], v[44:47]
	v_mfma_f32_16x16x32_f16 v[40:43], v[92:95], v[156:159], v[40:43]
	v_mfma_f32_16x16x32_f16 v[28:31], v[80:83], v[164:167], v[28:31]
	v_mfma_f32_16x16x32_f16 v[24:27], v[92:95], v[164:167], v[24:27]
	v_mfma_f32_16x16x32_f16 v[12:15], v[80:83], v[172:175], v[12:15]
	v_mfma_f32_16x16x32_f16 v[8:11], v[92:95], v[172:175], v[8:11]
	s_setprio 0
	s_barrier
	s_add_u32 s40, s40, 0xc080
	s_addc_u32 s41, s41, 0
	s_add_i32 s42, s42, s50
	v_lshl_add_u64 v[72:73], s[40:41], 0, v[178:179]
	s_mov_b32 m0, s42
	s_nop 0
	global_load_lds_dwordx4 v[72:73], off
	v_lshl_add_u64 v[72:73], s[40:41], 0, v[182:183]
	s_add_i32 m0, s42, 0x2000
	s_nop 0
	global_load_lds_dwordx4 v[72:73], off
	s_waitcnt vmcnt(6)
	s_barrier
	s_setprio 1
	v_mfma_f32_16x16x32_f16 v[52:55], v[190:193], v[136:139], v[52:55]
	v_mfma_f32_16x16x32_f16 v[48:51], v[198:201], v[136:139], v[48:51]
	v_mfma_f32_16x16x32_f16 v[36:39], v[190:193], v[152:155], v[36:39]
	v_mfma_f32_16x16x32_f16 v[32:35], v[198:201], v[152:155], v[32:35]
	v_mfma_f32_16x16x32_f16 v[20:23], v[190:193], v[160:163], v[20:23]
	v_mfma_f32_16x16x32_f16 v[16:19], v[198:201], v[160:163], v[16:19]
	v_mfma_f32_16x16x32_f16 v[4:7], v[190:193], v[168:171], v[4:7]
	v_mfma_f32_16x16x32_f16 v[0:3], v[198:201], v[168:171], v[0:3]
	v_mfma_f32_16x16x32_f16 v[52:55], v[194:197], v[148:151], v[52:55]
	v_mfma_f32_16x16x32_f16 v[48:51], v[202:205], v[148:151], v[48:51]
	v_mfma_f32_16x16x32_f16 v[36:39], v[194:197], v[156:159], v[36:39]
	v_mfma_f32_16x16x32_f16 v[32:35], v[202:205], v[156:159], v[32:35]
	v_mfma_f32_16x16x32_f16 v[20:23], v[194:197], v[164:167], v[20:23]
	v_mfma_f32_16x16x32_f16 v[16:19], v[202:205], v[164:167], v[16:19]
	v_mfma_f32_16x16x32_f16 v[4:7], v[194:197], v[172:175], v[4:7]
	v_mfma_f32_16x16x32_f16 v[0:3], v[202:205], v[172:175], v[0:3]
	s_setprio 0
	s_add_i32 s87, s87, 2
	s_add_u32 s38, s38, 0x100
	s_addc_u32 s39, s39, 0
	s_add_u32 s85, s85, 0x100
	s_addc_u32 s86, s86, 0
	s_cmp_gt_u32 s87, 9
	s_barrier
	s_cbranch_scc0 .LBB8_27
	s_lshl_b32 s92, s84, 8
	s_add_i32 s92, s92, s58
	s_lshl_b32 s93, s83, 8
	s_or_b32 s93, s93, s61
	v_lshlrev_b32_e32 v237, 2, v226
	s_lshl_b32 s96, s93, 2
	s_add_u32 s94, s16, s96
	s_addc_u32 s95, s17, 0
	global_load_dwordx4 v[72:75], v237, s[94:95] offset:0
	global_load_dwordx4 v[80:83], v237, s[94:95] offset:16
	global_load_dwordx4 v[88:91], v237, s[94:95] offset:128
	global_load_dwordx4 v[92:95], v237, s[94:95] offset:144
	s_add_u32 s94, s18, s96
	s_addc_u32 s95, s19, 0
	global_load_dwordx4 v[136:139], v237, s[94:95] offset:0
	global_load_dwordx4 v[148:151], v237, s[94:95] offset:16
	global_load_dwordx4 v[152:155], v237, s[94:95] offset:128
	global_load_dwordx4 v[156:159], v237, s[94:95] offset:144
	s_add_u32 s94, s14, s96
	s_addc_u32 s95, s15, 0
	global_load_dwordx4 v[160:163], v237, s[94:95] offset:0
	global_load_dwordx4 v[164:167], v237, s[94:95] offset:16
	global_load_dwordx4 v[168:171], v237, s[94:95] offset:128
	global_load_dwordx4 v[172:175], v237, s[94:95] offset:144
	v_lshlrev_b32_e32 v190, 3, v227
	s_lshl_b32 s96, s92, 3
	s_add_u32 s94, s12, s96
	s_addc_u32 s95, s13, 0
	global_load_dwordx2 v[238:239], v190, s[94:95] offset:0
	global_load_dwordx2 v[192:193], v190, s[94:95] offset:128
	global_load_dwordx2 v[194:195], v190, s[94:95] offset:256
	global_load_dwordx2 v[196:197], v190, s[94:95] offset:384
	global_load_dwordx2 v[198:199], v190, s[94:95] offset:1024
	global_load_dwordx2 v[200:201], v190, s[94:95] offset:1152
	global_load_dwordx2 v[202:203], v190, s[94:95] offset:1280
	global_load_dwordx2 v[204:205], v190, s[94:95] offset:1408
	v_mul_u32_u24_e32 v191, 0x600, v227
	v_lshl_add_u32 v191, v226, 1, v191
	s_mul_i32 s96, s92, 0x600
	s_lshl_b32 s97, s93, 1
	s_add_u32 s96, s96, s97
	s_add_u32 s98, s10, s96
	s_addc_u32 s99, s11, 0
	s_add_u32 s94, s98, 0x0
	s_addc_u32 s95, s99, 0
	global_load_dwordx4 v[208:211], v191, s[94:95] offset:0 nt
	global_load_dwordx4 v[212:215], v191, s[94:95] offset:64 nt
	s_add_u32 s94, s98, 0x6000
	s_addc_u32 s95, s99, 0
	global_load_dwordx4 v[216:219], v191, s[94:95] offset:0 nt
	global_load_dwordx4 v[220:223], v191, s[94:95] offset:64 nt
	v_add_u32_e32 v225, s92, v229
	v_mul_u32_u24_e32 v225, 0x600, v225
	s_lshl_b32 s97, s93, 1
	v_add3_u32 v225, v225, v230, s97
	v_mul_u32_u24_e32 v224, 0x60, v227
	s_mul_i32 s96, s92, 0x60
	s_lshl_b32 s97, s83, 5
	s_add_u32 s96, s96, s97
	s_lshr_b32 s97, s61, 3
	s_add_u32 s96, s96, s97
	s_add_u32 s96, s96, 0x800
	s_add_u32 s100, s28, s96
	s_addc_u32 s101, s29, 0
	s_waitcnt vmcnt(19)
	v_pk_add_f32 v[72:73], v[72:73], v[136:137]
	v_pk_add_f32 v[74:75], v[74:75], v[138:139]
	s_waitcnt vmcnt(18)
	v_pk_add_f32 v[80:81], v[80:81], v[148:149]
	v_pk_add_f32 v[82:83], v[82:83], v[150:151]
	s_waitcnt vmcnt(17)
	v_pk_add_f32 v[88:89], v[88:89], v[152:153]
	v_pk_add_f32 v[90:91], v[90:91], v[154:155]
	s_waitcnt vmcnt(16)
	v_pk_add_f32 v[92:93], v[92:93], v[156:157]
	v_pk_add_f32 v[94:95], v[94:95], v[158:159]
	v_pk_add_f32 v[144:145], v[144:145], v[72:73]
	v_pk_add_f32 v[146:147], v[146:147], v[74:75]
	v_pk_add_f32 v[124:125], v[124:125], v[72:73]
	v_pk_add_f32 v[126:127], v[126:127], v[74:75]
	v_pk_add_f32 v[108:109], v[108:109], v[72:73]
	v_pk_add_f32 v[110:111], v[110:111], v[74:75]
	v_pk_add_f32 v[84:85], v[84:85], v[72:73]
	v_pk_add_f32 v[86:87], v[86:87], v[74:75]
	v_pk_add_f32 v[60:61], v[60:61], v[72:73]
	v_pk_add_f32 v[62:63], v[62:63], v[74:75]
	v_pk_add_f32 v[44:45], v[44:45], v[72:73]
	v_pk_add_f32 v[46:47], v[46:47], v[74:75]
	v_pk_add_f32 v[28:29], v[28:29], v[72:73]
	v_pk_add_f32 v[30:31], v[30:31], v[74:75]
	v_pk_add_f32 v[12:13], v[12:13], v[72:73]
	v_pk_add_f32 v[14:15], v[14:15], v[74:75]
	v_pk_add_f32 v[140:141], v[140:141], v[80:81]
	v_pk_add_f32 v[142:143], v[142:143], v[82:83]
	v_pk_add_f32 v[120:121], v[120:121], v[80:81]
	v_pk_add_f32 v[122:123], v[122:123], v[82:83]
	v_pk_add_f32 v[104:105], v[104:105], v[80:81]
	v_pk_add_f32 v[106:107], v[106:107], v[82:83]
	v_pk_add_f32 v[76:77], v[76:77], v[80:81]
	v_pk_add_f32 v[78:79], v[78:79], v[82:83]
	v_pk_add_f32 v[56:57], v[56:57], v[80:81]
	v_pk_add_f32 v[58:59], v[58:59], v[82:83]
	v_pk_add_f32 v[40:41], v[40:41], v[80:81]
	v_pk_add_f32 v[42:43], v[42:43], v[82:83]
	v_pk_add_f32 v[24:25], v[24:25], v[80:81]
	v_pk_add_f32 v[26:27], v[26:27], v[82:83]
	v_pk_add_f32 v[8:9], v[8:9], v[80:81]
	v_pk_add_f32 v[10:11], v[10:11], v[82:83]
	v_pk_add_f32 v[132:133], v[132:133], v[88:89]
	v_pk_add_f32 v[134:135], v[134:135], v[90:91]
	v_pk_add_f32 v[116:117], v[116:117], v[88:89]
	v_pk_add_f32 v[118:119], v[118:119], v[90:91]
	v_pk_add_f32 v[100:101], v[100:101], v[88:89]
	v_pk_add_f32 v[102:103], v[102:103], v[90:91]
	v_pk_add_f32 v[68:69], v[68:69], v[88:89]
	v_pk_add_f32 v[70:71], v[70:71], v[90:91]
	v_pk_add_f32 v[52:53], v[52:53], v[88:89]
	v_pk_add_f32 v[54:55], v[54:55], v[90:91]
	v_pk_add_f32 v[36:37], v[36:37], v[88:89]
	v_pk_add_f32 v[38:39], v[38:39], v[90:91]
	v_pk_add_f32 v[20:21], v[20:21], v[88:89]
	v_pk_add_f32 v[22:23], v[22:23], v[90:91]
	v_pk_add_f32 v[4:5], v[4:5], v[88:89]
	v_pk_add_f32 v[6:7], v[6:7], v[90:91]
	v_pk_add_f32 v[128:129], v[128:129], v[92:93]
	v_pk_add_f32 v[130:131], v[130:131], v[94:95]
	v_pk_add_f32 v[112:113], v[112:113], v[92:93]
	v_pk_add_f32 v[114:115], v[114:115], v[94:95]
	v_pk_add_f32 v[96:97], v[96:97], v[92:93]
	v_pk_add_f32 v[98:99], v[98:99], v[94:95]
	v_pk_add_f32 v[64:65], v[64:65], v[92:93]
	v_pk_add_f32 v[66:67], v[66:67], v[94:95]
	v_pk_add_f32 v[48:49], v[48:49], v[92:93]
	v_pk_add_f32 v[50:51], v[50:51], v[94:95]
	v_pk_add_f32 v[32:33], v[32:33], v[92:93]
	v_pk_add_f32 v[34:35], v[34:35], v[94:95]
	v_pk_add_f32 v[16:17], v[16:17], v[92:93]
	v_pk_add_f32 v[18:19], v[18:19], v[94:95]
	v_pk_add_f32 v[0:1], v[0:1], v[92:93]
	v_pk_add_f32 v[2:3], v[2:3], v[94:95]
	s_add_u32 s94, s98, 0xc000
	s_addc_u32 s95, s99, 0
	global_load_dwordx4 v[240:243], v191, s[94:95] offset:0 nt
	global_load_dwordx4 v[244:247], v191, s[94:95] offset:64 nt
	s_add_u32 s94, s98, 0x12000
	s_addc_u32 s95, s99, 0
	global_load_dwordx4 v[248:251], v191, s[94:95] offset:0 nt
	global_load_dwordx4 v[252:255], v191, s[94:95] offset:64 nt
	s_add_u32 s94, s98, 0x30000
	s_addc_u32 s95, s99, 0
	global_load_dwordx4 v[136:139], v191, s[94:95] offset:0 nt
	global_load_dwordx4 v[148:151], v191, s[94:95] offset:64 nt
	s_add_u32 s94, s98, 0x36000
	s_addc_u32 s95, s99, 0
	global_load_dwordx4 v[152:155], v191, s[94:95] offset:0 nt
	global_load_dwordx4 v[156:159], v191, s[94:95] offset:64 nt
	s_waitcnt vmcnt(19)
	s_waitcnt vmcnt(11)
	v_cvt_f32_f16_e32 v72, v208
	v_cvt_f32_f16_sdwa v73, v208 dst_sel:DWORD dst_unused:UNUSED_PAD src0_sel:WORD_1
	v_cvt_f32_f16_e32 v74, v209
	v_cvt_f32_f16_sdwa v75, v209 dst_sel:DWORD dst_unused:UNUSED_PAD src0_sel:WORD_1
	v_cvt_f32_f16_e32 v80, v210
	v_cvt_f32_f16_sdwa v81, v210 dst_sel:DWORD dst_unused:UNUSED_PAD src0_sel:WORD_1
	v_cvt_f32_f16_e32 v82, v211
	v_cvt_f32_f16_sdwa v83, v211 dst_sel:DWORD dst_unused:UNUSED_PAD src0_sel:WORD_1
	v_sub_f32_e32 v72, v72, v238
	v_sub_f32_e32 v73, v73, v238
	v_sub_f32_e32 v74, v74, v238
	v_sub_f32_e32 v75, v75, v238
	v_sub_f32_e32 v80, v80, v238
	v_sub_f32_e32 v81, v81, v238
	v_sub_f32_e32 v82, v82, v238
	v_sub_f32_e32 v83, v83, v238
	v_pk_mul_f32 v[72:73], v[238:239], v[72:73] op_sel:[1,0]
	v_pk_mul_f32 v[74:75], v[238:239], v[74:75] op_sel:[1,0]
	v_pk_mul_f32 v[80:81], v[238:239], v[80:81] op_sel:[1,0]
	v_pk_mul_f32 v[82:83], v[238:239], v[82:83] op_sel:[1,0]
	v_pk_fma_f32 v[144:145], v[72:73], v[160:161], v[144:145]
	v_pk_fma_f32 v[146:147], v[74:75], v[162:163], v[146:147]
	v_pk_fma_f32 v[140:141], v[80:81], v[164:165], v[140:141]
	v_pk_fma_f32 v[142:143], v[82:83], v[166:167], v[142:143]
	v_cvt_pk_f16_f32 v144, v144, v145
	v_cvt_pk_f16_f32 v145, v146, v147
	v_cvt_pk_f16_f32 v146, v140, v141
	v_cvt_pk_f16_f32 v147, v142, v143
	ds_write_b128 v235, v[144:147]
	v_fma_mix_f32 v206, v144, 1.0, 0 op_sel_hi:[1,0,0]
	v_fma_mix_f32 v207, v144, v144, 0 op_sel_hi:[1,1,0]
	v_fma_mix_f32 v206, v144, 1.0, v206 op_sel:[1,0,0] op_sel_hi:[1,0,0]
	v_fma_mix_f32 v207, v144, v144, v207 op_sel:[1,1,0] op_sel_hi:[1,1,0]
	v_fma_mix_f32 v206, v145, 1.0, v206 op_sel_hi:[1,0,0]
	v_fma_mix_f32 v207, v145, v145, v207 op_sel_hi:[1,1,0]
	v_fma_mix_f32 v206, v145, 1.0, v206 op_sel:[1,0,0] op_sel_hi:[1,0,0]
	v_fma_mix_f32 v207, v145, v145, v207 op_sel:[1,1,0] op_sel_hi:[1,1,0]
	v_fma_mix_f32 v206, v146, 1.0, v206 op_sel_hi:[1,0,0]
	v_fma_mix_f32 v207, v146, v146, v207 op_sel_hi:[1,1,0]
	v_fma_mix_f32 v206, v146, 1.0, v206 op_sel:[1,0,0] op_sel_hi:[1,0,0]
	v_fma_mix_f32 v207, v146, v146, v207 op_sel:[1,1,0] op_sel_hi:[1,1,0]
	v_fma_mix_f32 v206, v147, 1.0, v206 op_sel_hi:[1,0,0]
	v_fma_mix_f32 v207, v147, v147, v207 op_sel_hi:[1,1,0]
	v_fma_mix_f32 v206, v147, 1.0, v206 op_sel:[1,0,0] op_sel_hi:[1,0,0]
	v_fma_mix_f32 v207, v147, v147, v207 op_sel:[1,1,0] op_sel_hi:[1,1,0]
	s_waitcnt vmcnt(10)
	v_cvt_f32_f16_e32 v72, v212
	v_cvt_f32_f16_sdwa v73, v212 dst_sel:DWORD dst_unused:UNUSED_PAD src0_sel:WORD_1
	v_cvt_f32_f16_e32 v74, v213
	v_cvt_f32_f16_sdwa v75, v213 dst_sel:DWORD dst_unused:UNUSED_PAD src0_sel:WORD_1
	v_cvt_f32_f16_e32 v80, v214
	v_cvt_f32_f16_sdwa v81, v214 dst_sel:DWORD dst_unused:UNUSED_PAD src0_sel:WORD_1
	v_cvt_f32_f16_e32 v82, v215
	v_cvt_f32_f16_sdwa v83, v215 dst_sel:DWORD dst_unused:UNUSED_PAD src0_sel:WORD_1
	v_sub_f32_e32 v72, v72, v238
	v_sub_f32_e32 v73, v73, v238
	v_sub_f32_e32 v74, v74, v238
	v_sub_f32_e32 v75, v75, v238
	v_sub_f32_e32 v80, v80, v238
	v_sub_f32_e32 v81, v81, v238
	v_sub_f32_e32 v82, v82, v238
	v_sub_f32_e32 v83, v83, v238
	v_pk_mul_f32 v[72:73], v[238:239], v[72:73] op_sel:[1,0]
	v_pk_mul_f32 v[74:75], v[238:239], v[74:75] op_sel:[1,0]
	v_pk_mul_f32 v[80:81], v[238:239], v[80:81] op_sel:[1,0]
	v_pk_mul_f32 v[82:83], v[238:239], v[82:83] op_sel:[1,0]
	v_pk_fma_f32 v[132:133], v[72:73], v[168:169], v[132:133]
	v_pk_fma_f32 v[134:135], v[74:75], v[170:171], v[134:135]
	v_pk_fma_f32 v[128:129], v[80:81], v[172:173], v[128:129]
	v_pk_fma_f32 v[130:131], v[82:83], v[174:175], v[130:131]
	v_cvt_pk_f16_f32 v132, v132, v133
	v_cvt_pk_f16_f32 v133, v134, v135
	v_cvt_pk_f16_f32 v134, v128, v129
	v_cvt_pk_f16_f32 v135, v130, v131
	ds_write_b128 v235, v[132:135] offset:64
	v_fma_mix_f32 v206, v132, 1.0, v206 op_sel_hi:[1,0,0]
	v_fma_mix_f32 v207, v132, v132, v207 op_sel_hi:[1,1,0]
	v_fma_mix_f32 v206, v132, 1.0, v206 op_sel:[1,0,0] op_sel_hi:[1,0,0]
	v_fma_mix_f32 v207, v132, v132, v207 op_sel:[1,1,0] op_sel_hi:[1,1,0]
	v_fma_mix_f32 v206, v133, 1.0, v206 op_sel_hi:[1,0,0]
	v_fma_mix_f32 v207, v133, v133, v207 op_sel_hi:[1,1,0]
	v_fma_mix_f32 v206, v133, 1.0, v206 op_sel:[1,0,0] op_sel_hi:[1,0,0]
	v_fma_mix_f32 v207, v133, v133, v207 op_sel:[1,1,0] op_sel_hi:[1,1,0]
	v_fma_mix_f32 v206, v134, 1.0, v206 op_sel_hi:[1,0,0]
	v_fma_mix_f32 v207, v134, v134, v207 op_sel_hi:[1,1,0]
	v_fma_mix_f32 v206, v134, 1.0, v206 op_sel:[1,0,0] op_sel_hi:[1,0,0]
	v_fma_mix_f32 v207, v134, v134, v207 op_sel:[1,1,0] op_sel_hi:[1,1,0]
	v_fma_mix_f32 v206, v135, 1.0, v206 op_sel_hi:[1,0,0]
	v_fma_mix_f32 v207, v135, v135, v207 op_sel_hi:[1,1,0]
	v_fma_mix_f32 v206, v135, 1.0, v206 op_sel:[1,0,0] op_sel_hi:[1,0,0]
	v_fma_mix_f32 v207, v135, v135, v207 op_sel:[1,1,0] op_sel_hi:[1,1,0]
	ds_read_b128 v[88:91], v236
	ds_read_b128 v[92:95], v236 offset:1152
	s_waitcnt vmcnt(9)
	v_cvt_f32_f16_e32 v72, v216
	v_cvt_f32_f16_sdwa v73, v216 dst_sel:DWORD dst_unused:UNUSED_PAD src0_sel:WORD_1
	v_cvt_f32_f16_e32 v74, v217
	v_cvt_f32_f16_sdwa v75, v217 dst_sel:DWORD dst_unused:UNUSED_PAD src0_sel:WORD_1
	v_cvt_f32_f16_e32 v80, v218
	v_cvt_f32_f16_sdwa v81, v218 dst_sel:DWORD dst_unused:UNUSED_PAD src0_sel:WORD_1
	v_cvt_f32_f16_e32 v82, v219
	v_cvt_f32_f16_sdwa v83, v219 dst_sel:DWORD dst_unused:UNUSED_PAD src0_sel:WORD_1
	v_sub_f32_e32 v72, v72, v192
	v_sub_f32_e32 v73, v73, v192
	v_sub_f32_e32 v74, v74, v192
	v_sub_f32_e32 v75, v75, v192
	v_sub_f32_e32 v80, v80, v192
	v_sub_f32_e32 v81, v81, v192
	v_sub_f32_e32 v82, v82, v192
	v_sub_f32_e32 v83, v83, v192
	v_pk_mul_f32 v[72:73], v[192:193], v[72:73] op_sel:[1,0]
	v_pk_mul_f32 v[74:75], v[192:193], v[74:75] op_sel:[1,0]
	v_pk_mul_f32 v[80:81], v[192:193], v[80:81] op_sel:[1,0]
	v_pk_mul_f32 v[82:83], v[192:193], v[82:83] op_sel:[1,0]
	v_pk_fma_f32 v[124:125], v[72:73], v[160:161], v[124:125]
	v_pk_fma_f32 v[126:127], v[74:75], v[162:163], v[126:127]
	v_pk_fma_f32 v[120:121], v[80:81], v[164:165], v[120:121]
	v_pk_fma_f32 v[122:123], v[82:83], v[166:167], v[122:123]
	v_cvt_pk_f16_f32 v124, v124, v125
	v_cvt_pk_f16_f32 v125, v126, v127
	v_cvt_pk_f16_f32 v126, v120, v121
	v_cvt_pk_f16_f32 v127, v122, v123
	s_waitcnt lgkmcnt(0)
	buffer_store_dwordx4 v[88:91], v225, s[24:27], 0 offen nt
	v_add_u32_e32 v82, 0x3000, v225
	buffer_store_dwordx4 v[92:95], v82, s[24:27], 0 offen nt
	ds_write_b128 v235, v[124:127]
	v_fma_mix_f32 v140, v124, 1.0, 0 op_sel_hi:[1,0,0]
	v_fma_mix_f32 v141, v124, v124, 0 op_sel_hi:[1,1,0]
	v_fma_mix_f32 v140, v124, 1.0, v140 op_sel:[1,0,0] op_sel_hi:[1,0,0]
	v_fma_mix_f32 v141, v124, v124, v141 op_sel:[1,1,0] op_sel_hi:[1,1,0]
	v_fma_mix_f32 v140, v125, 1.0, v140 op_sel_hi:[1,0,0]
	v_fma_mix_f32 v141, v125, v125, v141 op_sel_hi:[1,1,0]
	v_fma_mix_f32 v140, v125, 1.0, v140 op_sel:[1,0,0] op_sel_hi:[1,0,0]
	v_fma_mix_f32 v141, v125, v125, v141 op_sel:[1,1,0] op_sel_hi:[1,1,0]
	v_fma_mix_f32 v140, v126, 1.0, v140 op_sel_hi:[1,0,0]
	v_fma_mix_f32 v141, v126, v126, v141 op_sel_hi:[1,1,0]
	v_fma_mix_f32 v140, v126, 1.0, v140 op_sel:[1,0,0] op_sel_hi:[1,0,0]
	v_fma_mix_f32 v141, v126, v126, v141 op_sel:[1,1,0] op_sel_hi:[1,1,0]
	v_fma_mix_f32 v140, v127, 1.0, v140 op_sel_hi:[1,0,0]
	v_fma_mix_f32 v141, v127, v127, v141 op_sel_hi:[1,1,0]
	v_fma_mix_f32 v140, v127, 1.0, v140 op_sel:[1,0,0] op_sel_hi:[1,0,0]
	v_fma_mix_f32 v141, v127, v127, v141 op_sel:[1,1,0] op_sel_hi:[1,1,0]
	s_waitcnt vmcnt(10)
	v_cvt_f32_f16_e32 v72, v220
	v_cvt_f32_f16_sdwa v73, v220 dst_sel:DWORD dst_unused:UNUSED_PAD src0_sel:WORD_1
	v_cvt_f32_f16_e32 v74, v221
	v_cvt_f32_f16_sdwa v75, v221 dst_sel:DWORD dst_unused:UNUSED_PAD src0_sel:WORD_1
	v_cvt_f32_f16_e32 v80, v222
	v_cvt_f32_f16_sdwa v81, v222 dst_sel:DWORD dst_unused:UNUSED_PAD src0_sel:WORD_1
	v_cvt_f32_f16_e32 v82, v223
	v_cvt_f32_f16_sdwa v83, v223 dst_sel:DWORD dst_unused:UNUSED_PAD src0_sel:WORD_1
	v_sub_f32_e32 v72, v72, v192
	v_sub_f32_e32 v73, v73, v192
	v_sub_f32_e32 v74, v74, v192
	v_sub_f32_e32 v75, v75, v192
	v_sub_f32_e32 v80, v80, v192
	v_sub_f32_e32 v81, v81, v192
	v_sub_f32_e32 v82, v82, v192
	v_sub_f32_e32 v83, v83, v192
	v_pk_mul_f32 v[72:73], v[192:193], v[72:73] op_sel:[1,0]
	v_pk_mul_f32 v[74:75], v[192:193], v[74:75] op_sel:[1,0]
	v_pk_mul_f32 v[80:81], v[192:193], v[80:81] op_sel:[1,0]
	v_pk_mul_f32 v[82:83], v[192:193], v[82:83] op_sel:[1,0]
	v_pk_fma_f32 v[116:117], v[72:73], v[168:169], v[116:117]
	v_pk_fma_f32 v[118:119], v[74:75], v[170:171], v[118:119]
	v_pk_fma_f32 v[112:113], v[80:81], v[172:173], v[112:113]
	v_pk_fma_f32 v[114:115], v[82:83], v[174:175], v[114:115]
	v_cvt_pk_f16_f32 v116, v116, v117
	v_cvt_pk_f16_f32 v117, v118, v119
	v_cvt_pk_f16_f32 v118, v112, v113
	v_cvt_pk_f16_f32 v119, v114, v115
	ds_write_b128 v235, v[116:119] offset:64
	v_fma_mix_f32 v140, v116, 1.0, v140 op_sel_hi:[1,0,0]
	v_fma_mix_f32 v141, v116, v116, v141 op_sel_hi:[1,1,0]
	v_fma_mix_f32 v140, v116, 1.0, v140 op_sel:[1,0,0] op_sel_hi:[1,0,0]
	v_fma_mix_f32 v141, v116, v116, v141 op_sel:[1,1,0] op_sel_hi:[1,1,0]
	v_fma_mix_f32 v140, v117, 1.0, v140 op_sel_hi:[1,0,0]
	v_fma_mix_f32 v141, v117, v117, v141 op_sel_hi:[1,1,0]
	v_fma_mix_f32 v140, v117, 1.0, v140 op_sel:[1,0,0] op_sel_hi:[1,0,0]
	v_fma_mix_f32 v141, v117, v117, v141 op_sel:[1,1,0] op_sel_hi:[1,1,0]
	v_fma_mix_f32 v140, v118, 1.0, v140 op_sel_hi:[1,0,0]
	v_fma_mix_f32 v141, v118, v118, v141 op_sel_hi:[1,1,0]
	v_fma_mix_f32 v140, v118, 1.0, v140 op_sel:[1,0,0] op_sel_hi:[1,0,0]
	v_fma_mix_f32 v141, v118, v118, v141 op_sel:[1,1,0] op_sel_hi:[1,1,0]
	v_fma_mix_f32 v140, v119, 1.0, v140 op_sel_hi:[1,0,0]
	v_fma_mix_f32 v141, v119, v119, v141 op_sel_hi:[1,1,0]
	v_fma_mix_f32 v140, v119, 1.0, v140 op_sel:[1,0,0] op_sel_hi:[1,0,0]
	v_fma_mix_f32 v141, v119, v119, v141 op_sel:[1,1,0] op_sel_hi:[1,1,0]
	ds_read_b128 v[208:211], v236
	ds_read_b128 v[128:131], v236 offset:1152
	s_add_u32 s94, s98, 0x3c000
	s_addc_u32 s95, s99, 0
	global_load_dwordx4 v[212:215], v191, s[94:95] offset:0 nt
	global_load_dwordx4 v[144:147], v191, s[94:95] offset:64 nt
	s_add_u32 s94, s98, 0x42000
	s_addc_u32 s95, s99, 0
	global_load_dwordx4 v[132:135], v191, s[94:95] offset:0 nt
	global_load_dwordx4 v[88:91], v191, s[94:95] offset:64 nt
	s_waitcnt vmcnt(13)
	v_cvt_f32_f16_e32 v72, v240
	v_cvt_f32_f16_sdwa v73, v240 dst_sel:DWORD dst_unused:UNUSED_PAD src0_sel:WORD_1
	v_cvt_f32_f16_e32 v74, v241
	v_cvt_f32_f16_sdwa v75, v241 dst_sel:DWORD dst_unused:UNUSED_PAD src0_sel:WORD_1
	v_cvt_f32_f16_e32 v80, v242
	v_cvt_f32_f16_sdwa v81, v242 dst_sel:DWORD dst_unused:UNUSED_PAD src0_sel:WORD_1
	v_cvt_f32_f16_e32 v82, v243
	v_cvt_f32_f16_sdwa v83, v243 dst_sel:DWORD dst_unused:UNUSED_PAD src0_sel:WORD_1
	v_sub_f32_e32 v72, v72, v194
	v_sub_f32_e32 v73, v73, v194
	v_sub_f32_e32 v74, v74, v194
	v_sub_f32_e32 v75, v75, v194
	v_sub_f32_e32 v80, v80, v194
	v_sub_f32_e32 v81, v81, v194
	v_sub_f32_e32 v82, v82, v194
	v_sub_f32_e32 v83, v83, v194
	v_pk_mul_f32 v[72:73], v[194:195], v[72:73] op_sel:[1,0]
	v_pk_mul_f32 v[74:75], v[194:195], v[74:75] op_sel:[1,0]
	v_pk_mul_f32 v[80:81], v[194:195], v[80:81] op_sel:[1,0]
	v_pk_mul_f32 v[82:83], v[194:195], v[82:83] op_sel:[1,0]
	v_pk_fma_f32 v[108:109], v[72:73], v[160:161], v[108:109]
	v_pk_fma_f32 v[110:111], v[74:75], v[162:163], v[110:111]
	v_pk_fma_f32 v[104:105], v[80:81], v[164:165], v[104:105]
	v_pk_fma_f32 v[106:107], v[82:83], v[166:167], v[106:107]
	v_cvt_pk_f16_f32 v108, v108, v109
	v_cvt_pk_f16_f32 v109, v110, v111
	v_cvt_pk_f16_f32 v110, v104, v105
	v_cvt_pk_f16_f32 v111, v106, v107
	s_waitcnt lgkmcnt(0)
	v_add_u32_e32 v83, 0x6000, v225
	buffer_store_dwordx4 v[208:211], v83, s[24:27], 0 offen nt
	v_add_u32_e32 v82, 0x9000, v225
	buffer_store_dwordx4 v[128:131], v82, s[24:27], 0 offen nt
	ds_write_b128 v235, v[108:111]
	v_fma_mix_f32 v142, v108, 1.0, 0 op_sel_hi:[1,0,0]
	v_fma_mix_f32 v143, v108, v108, 0 op_sel_hi:[1,1,0]
	v_fma_mix_f32 v142, v108, 1.0, v142 op_sel:[1,0,0] op_sel_hi:[1,0,0]
	v_fma_mix_f32 v143, v108, v108, v143 op_sel:[1,1,0] op_sel_hi:[1,1,0]
	v_fma_mix_f32 v142, v109, 1.0, v142 op_sel_hi:[1,0,0]
	v_fma_mix_f32 v143, v109, v109, v143 op_sel_hi:[1,1,0]
	v_fma_mix_f32 v142, v109, 1.0, v142 op_sel:[1,0,0] op_sel_hi:[1,0,0]
	v_fma_mix_f32 v143, v109, v109, v143 op_sel:[1,1,0] op_sel_hi:[1,1,0]
	v_fma_mix_f32 v142, v110, 1.0, v142 op_sel_hi:[1,0,0]
	v_fma_mix_f32 v143, v110, v110, v143 op_sel_hi:[1,1,0]
	v_fma_mix_f32 v142, v110, 1.0, v142 op_sel:[1,0,0] op_sel_hi:[1,0,0]
	v_fma_mix_f32 v143, v110, v110, v143 op_sel:[1,1,0] op_sel_hi:[1,1,0]
	v_fma_mix_f32 v142, v111, 1.0, v142 op_sel_hi:[1,0,0]
	v_fma_mix_f32 v143, v111, v111, v143 op_sel_hi:[1,1,0]
	v_fma_mix_f32 v142, v111, 1.0, v142 op_sel:[1,0,0] op_sel_hi:[1,0,0]
	v_fma_mix_f32 v143, v111, v111, v143 op_sel:[1,1,0] op_sel_hi:[1,1,0]
	s_waitcnt vmcnt(14)
	v_cvt_f32_f16_e32 v72, v244
	v_cvt_f32_f16_sdwa v73, v244 dst_sel:DWORD dst_unused:UNUSED_PAD src0_sel:WORD_1
	v_cvt_f32_f16_e32 v74, v245
	v_cvt_f32_f16_sdwa v75, v245 dst_sel:DWORD dst_unused:UNUSED_PAD src0_sel:WORD_1
	v_cvt_f32_f16_e32 v80, v246
	v_cvt_f32_f16_sdwa v81, v246 dst_sel:DWORD dst_unused:UNUSED_PAD src0_sel:WORD_1
	v_cvt_f32_f16_e32 v82, v247
	v_cvt_f32_f16_sdwa v83, v247 dst_sel:DWORD dst_unused:UNUSED_PAD src0_sel:WORD_1
	v_sub_f32_e32 v72, v72, v194
	v_sub_f32_e32 v73, v73, v194
	v_sub_f32_e32 v74, v74, v194
	v_sub_f32_e32 v75, v75, v194
	v_sub_f32_e32 v80, v80, v194
	v_sub_f32_e32 v81, v81, v194
	v_sub_f32_e32 v82, v82, v194
	v_sub_f32_e32 v83, v83, v194
	v_pk_mul_f32 v[72:73], v[194:195], v[72:73] op_sel:[1,0]
	v_pk_mul_f32 v[74:75], v[194:195], v[74:75] op_sel:[1,0]
	v_pk_mul_f32 v[80:81], v[194:195], v[80:81] op_sel:[1,0]
	v_pk_mul_f32 v[82:83], v[194:195], v[82:83] op_sel:[1,0]
	v_pk_fma_f32 v[100:101], v[72:73], v[168:169], v[100:101]
	v_pk_fma_f32 v[102:103], v[74:75], v[170:171], v[102:103]
	v_pk_fma_f32 v[96:97], v[80:81], v[172:173], v[96:97]
	v_pk_fma_f32 v[98:99], v[82:83], v[174:175], v[98:99]
	v_cvt_pk_f16_f32 v100, v100, v101
	v_cvt_pk_f16_f32 v101, v102, v103
	v_cvt_pk_f16_f32 v102, v96, v97
	v_cvt_pk_f16_f32 v103, v98, v99
	ds_write_b128 v235, v[100:103] offset:64
	v_fma_mix_f32 v142, v100, 1.0, v142 op_sel_hi:[1,0,0]
	v_fma_mix_f32 v143, v100, v100, v143 op_sel_hi:[1,1,0]
	v_fma_mix_f32 v142, v100, 1.0, v142 op_sel:[1,0,0] op_sel_hi:[1,0,0]
	v_fma_mix_f32 v143, v100, v100, v143 op_sel:[1,1,0] op_sel_hi:[1,1,0]
	v_fma_mix_f32 v142, v101, 1.0, v142 op_sel_hi:[1,0,0]
	v_fma_mix_f32 v143, v101, v101, v143 op_sel_hi:[1,1,0]
	v_fma_mix_f32 v142, v101, 1.0, v142 op_sel:[1,0,0] op_sel_hi:[1,0,0]
	v_fma_mix_f32 v143, v101, v101, v143 op_sel:[1,1,0] op_sel_hi:[1,1,0]
	v_fma_mix_f32 v142, v102, 1.0, v142 op_sel_hi:[1,0,0]
	v_fma_mix_f32 v143, v102, v102, v143 op_sel_hi:[1,1,0]
	v_fma_mix_f32 v142, v102, 1.0, v142 op_sel:[1,0,0] op_sel_hi:[1,0,0]
	v_fma_mix_f32 v143, v102, v102, v143 op_sel:[1,1,0] op_sel_hi:[1,1,0]
	v_fma_mix_f32 v142, v103, 1.0, v142 op_sel_hi:[1,0,0]
	v_fma_mix_f32 v143, v103, v103, v143 op_sel_hi:[1,1,0]
	v_fma_mix_f32 v142, v103, 1.0, v142 op_sel:[1,0,0] op_sel_hi:[1,0,0]
	v_fma_mix_f32 v143, v103, v103, v143 op_sel:[1,1,0] op_sel_hi:[1,1,0]
	ds_read_b128 v[92:95], v236
	ds_read_b128 v[120:123], v236 offset:1152
	s_waitcnt vmcnt(13)
	v_cvt_f32_f16_e32 v72, v248
	v_cvt_f32_f16_sdwa v73, v248 dst_sel:DWORD dst_unused:UNUSED_PAD src0_sel:WORD_1
	v_cvt_f32_f16_e32 v74, v249
	v_cvt_f32_f16_sdwa v75, v249 dst_sel:DWORD dst_unused:UNUSED_PAD src0_sel:WORD_1
	v_cvt_f32_f16_e32 v80, v250
	v_cvt_f32_f16_sdwa v81, v250 dst_sel:DWORD dst_unused:UNUSED_PAD src0_sel:WORD_1
	v_cvt_f32_f16_e32 v82, v251
	v_cvt_f32_f16_sdwa v83, v251 dst_sel:DWORD dst_unused:UNUSED_PAD src0_sel:WORD_1
	v_sub_f32_e32 v72, v72, v196
	v_sub_f32_e32 v73, v73, v196
	v_sub_f32_e32 v74, v74, v196
	v_sub_f32_e32 v75, v75, v196
	v_sub_f32_e32 v80, v80, v196
	v_sub_f32_e32 v81, v81, v196
	v_sub_f32_e32 v82, v82, v196
	v_sub_f32_e32 v83, v83, v196
	v_pk_mul_f32 v[72:73], v[196:197], v[72:73] op_sel:[1,0]
	v_pk_mul_f32 v[74:75], v[196:197], v[74:75] op_sel:[1,0]
	v_pk_mul_f32 v[80:81], v[196:197], v[80:81] op_sel:[1,0]
	v_pk_mul_f32 v[82:83], v[196:197], v[82:83] op_sel:[1,0]
	v_pk_fma_f32 v[84:85], v[72:73], v[160:161], v[84:85]
	v_pk_fma_f32 v[86:87], v[74:75], v[162:163], v[86:87]
	v_pk_fma_f32 v[76:77], v[80:81], v[164:165], v[76:77]
	v_pk_fma_f32 v[78:79], v[82:83], v[166:167], v[78:79]
	v_cvt_pk_f16_f32 v84, v84, v85
	v_cvt_pk_f16_f32 v85, v86, v87
	v_cvt_pk_f16_f32 v86, v76, v77
	v_cvt_pk_f16_f32 v87, v78, v79
	s_waitcnt lgkmcnt(0)
	v_add_u32_e32 v83, 0xc000, v225
	buffer_store_dwordx4 v[92:95], v83, s[24:27], 0 offen nt
	v_add_u32_e32 v82, 0xf000, v225
	buffer_store_dwordx4 v[120:123], v82, s[24:27], 0 offen nt
	ds_write_b128 v235, v[84:87]
	v_fma_mix_f32 v216, v84, 1.0, 0 op_sel_hi:[1,0,0]
	v_fma_mix_f32 v217, v84, v84, 0 op_sel_hi:[1,1,0]
	v_fma_mix_f32 v216, v84, 1.0, v216 op_sel:[1,0,0] op_sel_hi:[1,0,0]
	v_fma_mix_f32 v217, v84, v84, v217 op_sel:[1,1,0] op_sel_hi:[1,1,0]
	v_fma_mix_f32 v216, v85, 1.0, v216 op_sel_hi:[1,0,0]
	v_fma_mix_f32 v217, v85, v85, v217 op_sel_hi:[1,1,0]
	v_fma_mix_f32 v216, v85, 1.0, v216 op_sel:[1,0,0] op_sel_hi:[1,0,0]
	v_fma_mix_f32 v217, v85, v85, v217 op_sel:[1,1,0] op_sel_hi:[1,1,0]
	v_fma_mix_f32 v216, v86, 1.0, v216 op_sel_hi:[1,0,0]
	v_fma_mix_f32 v217, v86, v86, v217 op_sel_hi:[1,1,0]
	v_fma_mix_f32 v216, v86, 1.0, v216 op_sel:[1,0,0] op_sel_hi:[1,0,0]
	v_fma_mix_f32 v217, v86, v86, v217 op_sel:[1,1,0] op_sel_hi:[1,1,0]
	v_fma_mix_f32 v216, v87, 1.0, v216 op_sel_hi:[1,0,0]
	v_fma_mix_f32 v217, v87, v87, v217 op_sel_hi:[1,1,0]
	v_fma_mix_f32 v216, v87, 1.0, v216 op_sel:[1,0,0] op_sel_hi:[1,0,0]
	v_fma_mix_f32 v217, v87, v87, v217 op_sel:[1,1,0] op_sel_hi:[1,1,0]
	s_waitcnt vmcnt(14)
	v_cvt_f32_f16_e32 v72, v252
	v_cvt_f32_f16_sdwa v73, v252 dst_sel:DWORD dst_unused:UNUSED_PAD src0_sel:WORD_1
	v_cvt_f32_f16_e32 v74, v253
	v_cvt_f32_f16_sdwa v75, v253 dst_sel:DWORD dst_unused:UNUSED_PAD src0_sel:WORD_1
	v_cvt_f32_f16_e32 v80, v254
	v_cvt_f32_f16_sdwa v81, v254 dst_sel:DWORD dst_unused:UNUSED_PAD src0_sel:WORD_1
	v_cvt_f32_f16_e32 v82, v255
	v_cvt_f32_f16_sdwa v83, v255 dst_sel:DWORD dst_unused:UNUSED_PAD src0_sel:WORD_1
	v_sub_f32_e32 v72, v72, v196
	v_sub_f32_e32 v73, v73, v196
	v_sub_f32_e32 v74, v74, v196
	v_sub_f32_e32 v75, v75, v196
	v_sub_f32_e32 v80, v80, v196
	v_sub_f32_e32 v81, v81, v196
	v_sub_f32_e32 v82, v82, v196
	v_sub_f32_e32 v83, v83, v196
	v_pk_mul_f32 v[72:73], v[196:197], v[72:73] op_sel:[1,0]
	v_pk_mul_f32 v[74:75], v[196:197], v[74:75] op_sel:[1,0]
	v_pk_mul_f32 v[80:81], v[196:197], v[80:81] op_sel:[1,0]
	v_pk_mul_f32 v[82:83], v[196:197], v[82:83] op_sel:[1,0]
	v_pk_fma_f32 v[68:69], v[72:73], v[168:169], v[68:69]
	v_pk_fma_f32 v[70:71], v[74:75], v[170:171], v[70:71]
	v_pk_fma_f32 v[64:65], v[80:81], v[172:173], v[64:65]
	v_pk_fma_f32 v[66:67], v[82:83], v[174:175], v[66:67]
	v_cvt_pk_f16_f32 v68, v68, v69
	v_cvt_pk_f16_f32 v69, v70, v71
	v_cvt_pk_f16_f32 v70, v64, v65
	v_cvt_pk_f16_f32 v71, v66, v67
	ds_write_b128 v235, v[68:71] offset:64
	v_fma_mix_f32 v216, v68, 1.0, v216 op_sel_hi:[1,0,0]
	v_fma_mix_f32 v217, v68, v68, v217 op_sel_hi:[1,1,0]
	v_fma_mix_f32 v216, v68, 1.0, v216 op_sel:[1,0,0] op_sel_hi:[1,0,0]
	v_fma_mix_f32 v217, v68, v68, v217 op_sel:[1,1,0] op_sel_hi:[1,1,0]
	v_fma_mix_f32 v216, v69, 1.0, v216 op_sel_hi:[1,0,0]
	v_fma_mix_f32 v217, v69, v69, v217 op_sel_hi:[1,1,0]
	v_fma_mix_f32 v216, v69, 1.0, v216 op_sel:[1,0,0] op_sel_hi:[1,0,0]
	v_fma_mix_f32 v217, v69, v69, v217 op_sel:[1,1,0] op_sel_hi:[1,1,0]
	v_fma_mix_f32 v216, v70, 1.0, v216 op_sel_hi:[1,0,0]
	v_fma_mix_f32 v217, v70, v70, v217 op_sel_hi:[1,1,0]
	v_fma_mix_f32 v216, v70, 1.0, v216 op_sel:[1,0,0] op_sel_hi:[1,0,0]
	v_fma_mix_f32 v217, v70, v70, v217 op_sel:[1,1,0] op_sel_hi:[1,1,0]
	v_fma_mix_f32 v216, v71, 1.0, v216 op_sel_hi:[1,0,0]
	v_fma_mix_f32 v217, v71, v71, v217 op_sel_hi:[1,1,0]
	v_fma_mix_f32 v216, v71, 1.0, v216 op_sel:[1,0,0] op_sel_hi:[1,0,0]
	v_fma_mix_f32 v217, v71, v71, v217 op_sel:[1,1,0] op_sel_hi:[1,1,0]
	ds_read_b128 v[112:115], v236
	ds_read_b128 v[220:223], v236 offset:1152
	s_waitcnt vmcnt(13)
	v_cvt_f32_f16_e32 v72, v136
	v_cvt_f32_f16_sdwa v73, v136 dst_sel:DWORD dst_unused:UNUSED_PAD src0_sel:WORD_1
	v_cvt_f32_f16_e32 v74, v137
	v_cvt_f32_f16_sdwa v75, v137 dst_sel:DWORD dst_unused:UNUSED_PAD src0_sel:WORD_1
	v_cvt_f32_f16_e32 v80, v138
	v_cvt_f32_f16_sdwa v81, v138 dst_sel:DWORD dst_unused:UNUSED_PAD src0_sel:WORD_1
	v_cvt_f32_f16_e32 v82, v139
	v_cvt_f32_f16_sdwa v83, v139 dst_sel:DWORD dst_unused:UNUSED_PAD src0_sel:WORD_1
	v_sub_f32_e32 v72, v72, v198
	v_sub_f32_e32 v73, v73, v198
	v_sub_f32_e32 v74, v74, v198
	v_sub_f32_e32 v75, v75, v198
	v_sub_f32_e32 v80, v80, v198
	v_sub_f32_e32 v81, v81, v198
	v_sub_f32_e32 v82, v82, v198
	v_sub_f32_e32 v83, v83, v198
	v_pk_mul_f32 v[72:73], v[198:199], v[72:73] op_sel:[1,0]
	v_pk_mul_f32 v[74:75], v[198:199], v[74:75] op_sel:[1,0]
	v_pk_mul_f32 v[80:81], v[198:199], v[80:81] op_sel:[1,0]
	v_pk_mul_f32 v[82:83], v[198:199], v[82:83] op_sel:[1,0]
	v_pk_fma_f32 v[60:61], v[72:73], v[160:161], v[60:61]
	v_pk_fma_f32 v[62:63], v[74:75], v[162:163], v[62:63]
	v_pk_fma_f32 v[56:57], v[80:81], v[164:165], v[56:57]
	v_pk_fma_f32 v[58:59], v[82:83], v[166:167], v[58:59]
	v_cvt_pk_f16_f32 v60, v60, v61
	v_cvt_pk_f16_f32 v61, v62, v63
	v_cvt_pk_f16_f32 v62, v56, v57
	v_cvt_pk_f16_f32 v63, v58, v59
	s_waitcnt lgkmcnt(0)
	v_add_u32_e32 v83, 0x12000, v225
	buffer_store_dwordx4 v[112:115], v83, s[24:27], 0 offen nt
	v_add_u32_e32 v82, 0x15000, v225
	buffer_store_dwordx4 v[220:223], v82, s[24:27], 0 offen nt
	ds_write_b128 v235, v[60:63]
	v_fma_mix_f32 v218, v60, 1.0, 0 op_sel_hi:[1,0,0]
	v_fma_mix_f32 v219, v60, v60, 0 op_sel_hi:[1,1,0]
	v_fma_mix_f32 v218, v60, 1.0, v218 op_sel:[1,0,0] op_sel_hi:[1,0,0]
	v_fma_mix_f32 v219, v60, v60, v219 op_sel:[1,1,0] op_sel_hi:[1,1,0]
	v_fma_mix_f32 v218, v61, 1.0, v218 op_sel_hi:[1,0,0]
	v_fma_mix_f32 v219, v61, v61, v219 op_sel_hi:[1,1,0]
	v_fma_mix_f32 v218, v61, 1.0, v218 op_sel:[1,0,0] op_sel_hi:[1,0,0]
	v_fma_mix_f32 v219, v61, v61, v219 op_sel:[1,1,0] op_sel_hi:[1,1,0]
	v_fma_mix_f32 v218, v62, 1.0, v218 op_sel_hi:[1,0,0]
	v_fma_mix_f32 v219, v62, v62, v219 op_sel_hi:[1,1,0]
	v_fma_mix_f32 v218, v62, 1.0, v218 op_sel:[1,0,0] op_sel_hi:[1,0,0]
	v_fma_mix_f32 v219, v62, v62, v219 op_sel:[1,1,0] op_sel_hi:[1,1,0]
	v_fma_mix_f32 v218, v63, 1.0, v218 op_sel_hi:[1,0,0]
	v_fma_mix_f32 v219, v63, v63, v219 op_sel_hi:[1,1,0]
	v_fma_mix_f32 v218, v63, 1.0, v218 op_sel:[1,0,0] op_sel_hi:[1,0,0]
	v_fma_mix_f32 v219, v63, v63, v219 op_sel:[1,1,0] op_sel_hi:[1,1,0]
	s_waitcnt vmcnt(14)
	v_cvt_f32_f16_e32 v72, v148
	v_cvt_f32_f16_sdwa v73, v148 dst_sel:DWORD dst_unused:UNUSED_PAD src0_sel:WORD_1
	v_cvt_f32_f16_e32 v74, v149
	v_cvt_f32_f16_sdwa v75, v149 dst_sel:DWORD dst_unused:UNUSED_PAD src0_sel:WORD_1
	v_cvt_f32_f16_e32 v80, v150
	v_cvt_f32_f16_sdwa v81, v150 dst_sel:DWORD dst_unused:UNUSED_PAD src0_sel:WORD_1
	v_cvt_f32_f16_e32 v82, v151
	v_cvt_f32_f16_sdwa v83, v151 dst_sel:DWORD dst_unused:UNUSED_PAD src0_sel:WORD_1
	v_sub_f32_e32 v72, v72, v198
	v_sub_f32_e32 v73, v73, v198
	v_sub_f32_e32 v74, v74, v198
	v_sub_f32_e32 v75, v75, v198
	v_sub_f32_e32 v80, v80, v198
	v_sub_f32_e32 v81, v81, v198
	v_sub_f32_e32 v82, v82, v198
	v_sub_f32_e32 v83, v83, v198
	v_pk_mul_f32 v[72:73], v[198:199], v[72:73] op_sel:[1,0]
	v_pk_mul_f32 v[74:75], v[198:199], v[74:75] op_sel:[1,0]
	v_pk_mul_f32 v[80:81], v[198:199], v[80:81] op_sel:[1,0]
	v_pk_mul_f32 v[82:83], v[198:199], v[82:83] op_sel:[1,0]
	v_pk_fma_f32 v[52:53], v[72:73], v[168:169], v[52:53]
	v_pk_fma_f32 v[54:55], v[74:75], v[170:171], v[54:55]
	v_pk_fma_f32 v[48:49], v[80:81], v[172:173], v[48:49]
	v_pk_fma_f32 v[50:51], v[82:83], v[174:175], v[50:51]
	v_cvt_pk_f16_f32 v52, v52, v53
	v_cvt_pk_f16_f32 v53, v54, v55
	v_cvt_pk_f16_f32 v54, v48, v49
	v_cvt_pk_f16_f32 v55, v50, v51
	ds_write_b128 v235, v[52:55] offset:64
	v_fma_mix_f32 v218, v52, 1.0, v218 op_sel_hi:[1,0,0]
	v_fma_mix_f32 v219, v52, v52, v219 op_sel_hi:[1,1,0]
	v_fma_mix_f32 v218, v52, 1.0, v218 op_sel:[1,0,0] op_sel_hi:[1,0,0]
	v_fma_mix_f32 v219, v52, v52, v219 op_sel:[1,1,0] op_sel_hi:[1,1,0]
	v_fma_mix_f32 v218, v53, 1.0, v218 op_sel_hi:[1,0,0]
	v_fma_mix_f32 v219, v53, v53, v219 op_sel_hi:[1,1,0]
	v_fma_mix_f32 v218, v53, 1.0, v218 op_sel:[1,0,0] op_sel_hi:[1,0,0]
	v_fma_mix_f32 v219, v53, v53, v219 op_sel:[1,1,0] op_sel_hi:[1,1,0]
	v_fma_mix_f32 v218, v54, 1.0, v218 op_sel_hi:[1,0,0]
	v_fma_mix_f32 v219, v54, v54, v219 op_sel_hi:[1,1,0]
	v_fma_mix_f32 v218, v54, 1.0, v218 op_sel:[1,0,0] op_sel_hi:[1,0,0]
	v_fma_mix_f32 v219, v54, v54, v219 op_sel:[1,1,0] op_sel_hi:[1,1,0]
	v_fma_mix_f32 v218, v55, 1.0, v218 op_sel_hi:[1,0,0]
	v_fma_mix_f32 v219, v55, v55, v219 op_sel_hi:[1,1,0]
	v_fma_mix_f32 v218, v55, 1.0, v218 op_sel:[1,0,0] op_sel_hi:[1,0,0]
	v_fma_mix_f32 v219, v55, v55, v219 op_sel:[1,1,0] op_sel_hi:[1,1,0]
	ds_read_b128 v[124:127], v236
	ds_read_b128 v[116:119], v236 offset:1152
	s_waitcnt vmcnt(13)
	v_cvt_f32_f16_e32 v72, v152
	v_cvt_f32_f16_sdwa v73, v152 dst_sel:DWORD dst_unused:UNUSED_PAD src0_sel:WORD_1
	v_cvt_f32_f16_e32 v74, v153
	v_cvt_f32_f16_sdwa v75, v153 dst_sel:DWORD dst_unused:UNUSED_PAD src0_sel:WORD_1
	v_cvt_f32_f16_e32 v80, v154
	v_cvt_f32_f16_sdwa v81, v154 dst_sel:DWORD dst_unused:UNUSED_PAD src0_sel:WORD_1
	v_cvt_f32_f16_e32 v82, v155
	v_cvt_f32_f16_sdwa v83, v155 dst_sel:DWORD dst_unused:UNUSED_PAD src0_sel:WORD_1
	v_sub_f32_e32 v72, v72, v200
	v_sub_f32_e32 v73, v73, v200
	v_sub_f32_e32 v74, v74, v200
	v_sub_f32_e32 v75, v75, v200
	v_sub_f32_e32 v80, v80, v200
	v_sub_f32_e32 v81, v81, v200
	v_sub_f32_e32 v82, v82, v200
	v_sub_f32_e32 v83, v83, v200
	v_pk_mul_f32 v[72:73], v[200:201], v[72:73] op_sel:[1,0]
	v_pk_mul_f32 v[74:75], v[200:201], v[74:75] op_sel:[1,0]
	v_pk_mul_f32 v[80:81], v[200:201], v[80:81] op_sel:[1,0]
	v_pk_mul_f32 v[82:83], v[200:201], v[82:83] op_sel:[1,0]
	v_pk_fma_f32 v[44:45], v[72:73], v[160:161], v[44:45]
	v_pk_fma_f32 v[46:47], v[74:75], v[162:163], v[46:47]
	v_pk_fma_f32 v[40:41], v[80:81], v[164:165], v[40:41]
	v_pk_fma_f32 v[42:43], v[82:83], v[166:167], v[42:43]
	v_cvt_pk_f16_f32 v44, v44, v45
	v_cvt_pk_f16_f32 v45, v46, v47
	v_cvt_pk_f16_f32 v46, v40, v41
	v_cvt_pk_f16_f32 v47, v42, v43
	s_waitcnt lgkmcnt(0)
	v_add_u32_e32 v83, 0x30000, v225
	buffer_store_dwordx4 v[124:127], v83, s[24:27], 0 offen nt
	v_add_u32_e32 v82, 0x33000, v225
	buffer_store_dwordx4 v[116:119], v82, s[24:27], 0 offen nt
	ds_write_b128 v235, v[44:47]
	v_fma_mix_f32 v208, v44, 1.0, 0 op_sel_hi:[1,0,0]
	v_fma_mix_f32 v209, v44, v44, 0 op_sel_hi:[1,1,0]
	v_fma_mix_f32 v208, v44, 1.0, v208 op_sel:[1,0,0] op_sel_hi:[1,0,0]
	v_fma_mix_f32 v209, v44, v44, v209 op_sel:[1,1,0] op_sel_hi:[1,1,0]
	v_fma_mix_f32 v208, v45, 1.0, v208 op_sel_hi:[1,0,0]
	v_fma_mix_f32 v209, v45, v45, v209 op_sel_hi:[1,1,0]
	v_fma_mix_f32 v208, v45, 1.0, v208 op_sel:[1,0,0] op_sel_hi:[1,0,0]
	v_fma_mix_f32 v209, v45, v45, v209 op_sel:[1,1,0] op_sel_hi:[1,1,0]
	v_fma_mix_f32 v208, v46, 1.0, v208 op_sel_hi:[1,0,0]
	v_fma_mix_f32 v209, v46, v46, v209 op_sel_hi:[1,1,0]
	v_fma_mix_f32 v208, v46, 1.0, v208 op_sel:[1,0,0] op_sel_hi:[1,0,0]
	v_fma_mix_f32 v209, v46, v46, v209 op_sel:[1,1,0] op_sel_hi:[1,1,0]
	v_fma_mix_f32 v208, v47, 1.0, v208 op_sel_hi:[1,0,0]
	v_fma_mix_f32 v209, v47, v47, v209 op_sel_hi:[1,1,0]
	v_fma_mix_f32 v208, v47, 1.0, v208 op_sel:[1,0,0] op_sel_hi:[1,0,0]
	v_fma_mix_f32 v209, v47, v47, v209 op_sel:[1,1,0] op_sel_hi:[1,1,0]
	s_waitcnt vmcnt(14)
	v_cvt_f32_f16_e32 v72, v156
	v_cvt_f32_f16_sdwa v73, v156 dst_sel:DWORD dst_unused:UNUSED_PAD src0_sel:WORD_1
	v_cvt_f32_f16_e32 v74, v157
	v_cvt_f32_f16_sdwa v75, v157 dst_sel:DWORD dst_unused:UNUSED_PAD src0_sel:WORD_1
	v_cvt_f32_f16_e32 v80, v158
	v_cvt_f32_f16_sdwa v81, v158 dst_sel:DWORD dst_unused:UNUSED_PAD src0_sel:WORD_1
	v_cvt_f32_f16_e32 v82, v159
	v_cvt_f32_f16_sdwa v83, v159 dst_sel:DWORD dst_unused:UNUSED_PAD src0_sel:WORD_1
	v_sub_f32_e32 v72, v72, v200
	v_sub_f32_e32 v73, v73, v200
	v_sub_f32_e32 v74, v74, v200
	v_sub_f32_e32 v75, v75, v200
	v_sub_f32_e32 v80, v80, v200
	v_sub_f32_e32 v81, v81, v200
	v_sub_f32_e32 v82, v82, v200
	v_sub_f32_e32 v83, v83, v200
	v_pk_mul_f32 v[72:73], v[200:201], v[72:73] op_sel:[1,0]
	v_pk_mul_f32 v[74:75], v[200:201], v[74:75] op_sel:[1,0]
	v_pk_mul_f32 v[80:81], v[200:201], v[80:81] op_sel:[1,0]
	v_pk_mul_f32 v[82:83], v[200:201], v[82:83] op_sel:[1,0]
	v_pk_fma_f32 v[36:37], v[72:73], v[168:169], v[36:37]
	v_pk_fma_f32 v[38:39], v[74:75], v[170:171], v[38:39]
	v_pk_fma_f32 v[32:33], v[80:81], v[172:173], v[32:33]
	v_pk_fma_f32 v[34:35], v[82:83], v[174:175], v[34:35]
	v_cvt_pk_f16_f32 v36, v36, v37
	v_cvt_pk_f16_f32 v37, v38, v39
	v_cvt_pk_f16_f32 v38, v32, v33
	v_cvt_pk_f16_f32 v39, v34, v35
	ds_write_b128 v235, v[36:39] offset:64
	v_fma_mix_f32 v208, v36, 1.0, v208 op_sel_hi:[1,0,0]
	v_fma_mix_f32 v209, v36, v36, v209 op_sel_hi:[1,1,0]
	v_fma_mix_f32 v208, v36, 1.0, v208 op_sel:[1,0,0] op_sel_hi:[1,0,0]
	v_fma_mix_f32 v209, v36, v36, v209 op_sel:[1,1,0] op_sel_hi:[1,1,0]
	v_fma_mix_f32 v208, v37, 1.0, v208 op_sel_hi:[1,0,0]
	v_fma_mix_f32 v209, v37, v37, v209 op_sel_hi:[1,1,0]
	v_fma_mix_f32 v208, v37, 1.0, v208 op_sel:[1,0,0] op_sel_hi:[1,0,0]
	v_fma_mix_f32 v209, v37, v37, v209 op_sel:[1,1,0] op_sel_hi:[1,1,0]
	v_fma_mix_f32 v208, v38, 1.0, v208 op_sel_hi:[1,0,0]
	v_fma_mix_f32 v209, v38, v38, v209 op_sel_hi:[1,1,0]
	v_fma_mix_f32 v208, v38, 1.0, v208 op_sel:[1,0,0] op_sel_hi:[1,0,0]
	v_fma_mix_f32 v209, v38, v38, v209 op_sel:[1,1,0] op_sel_hi:[1,1,0]
	v_fma_mix_f32 v208, v39, 1.0, v208 op_sel_hi:[1,0,0]
	v_fma_mix_f32 v209, v39, v39, v209 op_sel_hi:[1,1,0]
	v_fma_mix_f32 v208, v39, 1.0, v208 op_sel:[1,0,0] op_sel_hi:[1,0,0]
	v_fma_mix_f32 v209, v39, v39, v209 op_sel:[1,1,0] op_sel_hi:[1,1,0]
	ds_read_b128 v[128:131], v236
	ds_read_b128 v[104:107], v236 offset:1152
	s_waitcnt vmcnt(11)
	v_cvt_f32_f16_e32 v72, v212
	v_cvt_f32_f16_sdwa v73, v212 dst_sel:DWORD dst_unused:UNUSED_PAD src0_sel:WORD_1
	v_cvt_f32_f16_e32 v74, v213
	v_cvt_f32_f16_sdwa v75, v213 dst_sel:DWORD dst_unused:UNUSED_PAD src0_sel:WORD_1
	v_cvt_f32_f16_e32 v80, v214
	v_cvt_f32_f16_sdwa v81, v214 dst_sel:DWORD dst_unused:UNUSED_PAD src0_sel:WORD_1
	v_cvt_f32_f16_e32 v82, v215
	v_cvt_f32_f16_sdwa v83, v215 dst_sel:DWORD dst_unused:UNUSED_PAD src0_sel:WORD_1
	v_sub_f32_e32 v72, v72, v202
	v_sub_f32_e32 v73, v73, v202
	v_sub_f32_e32 v74, v74, v202
	v_sub_f32_e32 v75, v75, v202
	v_sub_f32_e32 v80, v80, v202
	v_sub_f32_e32 v81, v81, v202
	v_sub_f32_e32 v82, v82, v202
	v_sub_f32_e32 v83, v83, v202
	v_pk_mul_f32 v[72:73], v[202:203], v[72:73] op_sel:[1,0]
	v_pk_mul_f32 v[74:75], v[202:203], v[74:75] op_sel:[1,0]
	v_pk_mul_f32 v[80:81], v[202:203], v[80:81] op_sel:[1,0]
	v_pk_mul_f32 v[82:83], v[202:203], v[82:83] op_sel:[1,0]
	v_pk_fma_f32 v[28:29], v[72:73], v[160:161], v[28:29]
	v_pk_fma_f32 v[30:31], v[74:75], v[162:163], v[30:31]
	v_pk_fma_f32 v[24:25], v[80:81], v[164:165], v[24:25]
	v_pk_fma_f32 v[26:27], v[82:83], v[166:167], v[26:27]
	v_cvt_pk_f16_f32 v28, v28, v29
	v_cvt_pk_f16_f32 v29, v30, v31
	v_cvt_pk_f16_f32 v30, v24, v25
	v_cvt_pk_f16_f32 v31, v26, v27
	s_waitcnt lgkmcnt(0)
	v_add_u32_e32 v83, 0x36000, v225
	buffer_store_dwordx4 v[128:131], v83, s[24:27], 0 offen nt
	v_add_u32_e32 v82, 0x39000, v225
	buffer_store_dwordx4 v[104:107], v82, s[24:27], 0 offen nt
	ds_write_b128 v235, v[28:31]
	v_fma_mix_f32 v210, v28, 1.0, 0 op_sel_hi:[1,0,0]
	v_fma_mix_f32 v211, v28, v28, 0 op_sel_hi:[1,1,0]
	v_fma_mix_f32 v210, v28, 1.0, v210 op_sel:[1,0,0] op_sel_hi:[1,0,0]
	v_fma_mix_f32 v211, v28, v28, v211 op_sel:[1,1,0] op_sel_hi:[1,1,0]
	v_fma_mix_f32 v210, v29, 1.0, v210 op_sel_hi:[1,0,0]
	v_fma_mix_f32 v211, v29, v29, v211 op_sel_hi:[1,1,0]
	v_fma_mix_f32 v210, v29, 1.0, v210 op_sel:[1,0,0] op_sel_hi:[1,0,0]
	v_fma_mix_f32 v211, v29, v29, v211 op_sel:[1,1,0] op_sel_hi:[1,1,0]
	v_fma_mix_f32 v210, v30, 1.0, v210 op_sel_hi:[1,0,0]
	v_fma_mix_f32 v211, v30, v30, v211 op_sel_hi:[1,1,0]
	v_fma_mix_f32 v210, v30, 1.0, v210 op_sel:[1,0,0] op_sel_hi:[1,0,0]
	v_fma_mix_f32 v211, v30, v30, v211 op_sel:[1,1,0] op_sel_hi:[1,1,0]
	v_fma_mix_f32 v210, v31, 1.0, v210 op_sel_hi:[1,0,0]
	v_fma_mix_f32 v211, v31, v31, v211 op_sel_hi:[1,1,0]
	v_fma_mix_f32 v210, v31, 1.0, v210 op_sel:[1,0,0] op_sel_hi:[1,0,0]
	v_fma_mix_f32 v211, v31, v31, v211 op_sel:[1,1,0] op_sel_hi:[1,1,0]
	s_waitcnt vmcnt(12)
	v_cvt_f32_f16_e32 v72, v144
	v_cvt_f32_f16_sdwa v73, v144 dst_sel:DWORD dst_unused:UNUSED_PAD src0_sel:WORD_1
	v_cvt_f32_f16_e32 v74, v145
	v_cvt_f32_f16_sdwa v75, v145 dst_sel:DWORD dst_unused:UNUSED_PAD src0_sel:WORD_1
	v_cvt_f32_f16_e32 v80, v146
	v_cvt_f32_f16_sdwa v81, v146 dst_sel:DWORD dst_unused:UNUSED_PAD src0_sel:WORD_1
	v_cvt_f32_f16_e32 v82, v147
	v_cvt_f32_f16_sdwa v83, v147 dst_sel:DWORD dst_unused:UNUSED_PAD src0_sel:WORD_1
	v_sub_f32_e32 v72, v72, v202
	v_sub_f32_e32 v73, v73, v202
	v_sub_f32_e32 v74, v74, v202
	v_sub_f32_e32 v75, v75, v202
	v_sub_f32_e32 v80, v80, v202
	v_sub_f32_e32 v81, v81, v202
	v_sub_f32_e32 v82, v82, v202
	v_sub_f32_e32 v83, v83, v202
	v_pk_mul_f32 v[72:73], v[202:203], v[72:73] op_sel:[1,0]
	v_pk_mul_f32 v[74:75], v[202:203], v[74:75] op_sel:[1,0]
	v_pk_mul_f32 v[80:81], v[202:203], v[80:81] op_sel:[1,0]
	v_pk_mul_f32 v[82:83], v[202:203], v[82:83] op_sel:[1,0]
	v_pk_fma_f32 v[20:21], v[72:73], v[168:169], v[20:21]
	v_pk_fma_f32 v[22:23], v[74:75], v[170:171], v[22:23]
	v_pk_fma_f32 v[16:17], v[80:81], v[172:173], v[16:17]
	v_pk_fma_f32 v[18:19], v[82:83], v[174:175], v[18:19]
	v_cvt_pk_f16_f32 v20, v20, v21
	v_cvt_pk_f16_f32 v21, v22, v23
	v_cvt_pk_f16_f32 v22, v16, v17
	v_cvt_pk_f16_f32 v23, v18, v19
	ds_write_b128 v235, v[20:23] offset:64
	v_fma_mix_f32 v210, v20, 1.0, v210 op_sel_hi:[1,0,0]
	v_fma_mix_f32 v211, v20, v20, v211 op_sel_hi:[1,1,0]
	v_fma_mix_f32 v210, v20, 1.0, v210 op_sel:[1,0,0] op_sel_hi:[1,0,0]
	v_fma_mix_f32 v211, v20, v20, v211 op_sel:[1,1,0] op_sel_hi:[1,1,0]
	v_fma_mix_f32 v210, v21, 1.0, v210 op_sel_hi:[1,0,0]
	v_fma_mix_f32 v211, v21, v21, v211 op_sel_hi:[1,1,0]
	v_fma_mix_f32 v210, v21, 1.0, v210 op_sel:[1,0,0] op_sel_hi:[1,0,0]
	v_fma_mix_f32 v211, v21, v21, v211 op_sel:[1,1,0] op_sel_hi:[1,1,0]
	v_fma_mix_f32 v210, v22, 1.0, v210 op_sel_hi:[1,0,0]
	v_fma_mix_f32 v211, v22, v22, v211 op_sel_hi:[1,1,0]
	v_fma_mix_f32 v210, v22, 1.0, v210 op_sel:[1,0,0] op_sel_hi:[1,0,0]
	v_fma_mix_f32 v211, v22, v22, v211 op_sel:[1,1,0] op_sel_hi:[1,1,0]
	v_fma_mix_f32 v210, v23, 1.0, v210 op_sel_hi:[1,0,0]
	v_fma_mix_f32 v211, v23, v23, v211 op_sel_hi:[1,1,0]
	v_fma_mix_f32 v210, v23, 1.0, v210 op_sel:[1,0,0] op_sel_hi:[1,0,0]
	v_fma_mix_f32 v211, v23, v23, v211 op_sel:[1,1,0] op_sel_hi:[1,1,0]
	ds_read_b128 v[240:243], v236
	ds_read_b128 v[96:99], v236 offset:1152
	s_waitcnt vmcnt(11)
	v_cvt_f32_f16_e32 v72, v132
	v_cvt_f32_f16_sdwa v73, v132 dst_sel:DWORD dst_unused:UNUSED_PAD src0_sel:WORD_1
	v_cvt_f32_f16_e32 v74, v133
	v_cvt_f32_f16_sdwa v75, v133 dst_sel:DWORD dst_unused:UNUSED_PAD src0_sel:WORD_1
	v_cvt_f32_f16_e32 v80, v134
	v_cvt_f32_f16_sdwa v81, v134 dst_sel:DWORD dst_unused:UNUSED_PAD src0_sel:WORD_1
	v_cvt_f32_f16_e32 v82, v135
	v_cvt_f32_f16_sdwa v83, v135 dst_sel:DWORD dst_unused:UNUSED_PAD src0_sel:WORD_1
	v_sub_f32_e32 v72, v72, v204
	v_sub_f32_e32 v73, v73, v204
	v_sub_f32_e32 v74, v74, v204
	v_sub_f32_e32 v75, v75, v204
	v_sub_f32_e32 v80, v80, v204
	v_sub_f32_e32 v81, v81, v204
	v_sub_f32_e32 v82, v82, v204
	v_sub_f32_e32 v83, v83, v204
	v_pk_mul_f32 v[72:73], v[204:205], v[72:73] op_sel:[1,0]
	v_pk_mul_f32 v[74:75], v[204:205], v[74:75] op_sel:[1,0]
	v_pk_mul_f32 v[80:81], v[204:205], v[80:81] op_sel:[1,0]
	v_pk_mul_f32 v[82:83], v[204:205], v[82:83] op_sel:[1,0]
	v_pk_fma_f32 v[12:13], v[72:73], v[160:161], v[12:13]
	v_pk_fma_f32 v[14:15], v[74:75], v[162:163], v[14:15]
	v_pk_fma_f32 v[8:9], v[80:81], v[164:165], v[8:9]
	v_pk_fma_f32 v[10:11], v[82:83], v[166:167], v[10:11]
	v_cvt_pk_f16_f32 v12, v12, v13
	v_cvt_pk_f16_f32 v13, v14, v15
	v_cvt_pk_f16_f32 v14, v8, v9
	v_cvt_pk_f16_f32 v15, v10, v11
	s_waitcnt lgkmcnt(0)
	v_add_u32_e32 v83, 0x3c000, v225
	buffer_store_dwordx4 v[240:243], v83, s[24:27], 0 offen nt
	v_add_u32_e32 v82, 0x3f000, v225
	buffer_store_dwordx4 v[96:99], v82, s[24:27], 0 offen nt
	ds_write_b128 v235, v[12:15]
	v_fma_mix_f32 v244, v12, 1.0, 0 op_sel_hi:[1,0,0]
	v_fma_mix_f32 v245, v12, v12, 0 op_sel_hi:[1,1,0]
	v_fma_mix_f32 v244, v12, 1.0, v244 op_sel:[1,0,0] op_sel_hi:[1,0,0]
	v_fma_mix_f32 v245, v12, v12, v245 op_sel:[1,1,0] op_sel_hi:[1,1,0]
	v_fma_mix_f32 v244, v13, 1.0, v244 op_sel_hi:[1,0,0]
	v_fma_mix_f32 v245, v13, v13, v245 op_sel_hi:[1,1,0]
	v_fma_mix_f32 v244, v13, 1.0, v244 op_sel:[1,0,0] op_sel_hi:[1,0,0]
	v_fma_mix_f32 v245, v13, v13, v245 op_sel:[1,1,0] op_sel_hi:[1,1,0]
	v_fma_mix_f32 v244, v14, 1.0, v244 op_sel_hi:[1,0,0]
	v_fma_mix_f32 v245, v14, v14, v245 op_sel_hi:[1,1,0]
	v_fma_mix_f32 v244, v14, 1.0, v244 op_sel:[1,0,0] op_sel_hi:[1,0,0]
	v_fma_mix_f32 v245, v14, v14, v245 op_sel:[1,1,0] op_sel_hi:[1,1,0]
	v_fma_mix_f32 v244, v15, 1.0, v244 op_sel_hi:[1,0,0]
	v_fma_mix_f32 v245, v15, v15, v245 op_sel_hi:[1,1,0]
	v_fma_mix_f32 v244, v15, 1.0, v244 op_sel:[1,0,0] op_sel_hi:[1,0,0]
	v_fma_mix_f32 v245, v15, v15, v245 op_sel:[1,1,0] op_sel_hi:[1,1,0]
	s_waitcnt vmcnt(12)
	v_cvt_f32_f16_e32 v72, v88
	v_cvt_f32_f16_sdwa v73, v88 dst_sel:DWORD dst_unused:UNUSED_PAD src0_sel:WORD_1
	v_cvt_f32_f16_e32 v74, v89
	v_cvt_f32_f16_sdwa v75, v89 dst_sel:DWORD dst_unused:UNUSED_PAD src0_sel:WORD_1
	v_cvt_f32_f16_e32 v80, v90
	v_cvt_f32_f16_sdwa v81, v90 dst_sel:DWORD dst_unused:UNUSED_PAD src0_sel:WORD_1
	v_cvt_f32_f16_e32 v82, v91
	v_cvt_f32_f16_sdwa v83, v91 dst_sel:DWORD dst_unused:UNUSED_PAD src0_sel:WORD_1
	v_sub_f32_e32 v72, v72, v204
	v_sub_f32_e32 v73, v73, v204
	v_sub_f32_e32 v74, v74, v204
	v_sub_f32_e32 v75, v75, v204
	v_sub_f32_e32 v80, v80, v204
	v_sub_f32_e32 v81, v81, v204
	v_sub_f32_e32 v82, v82, v204
	v_sub_f32_e32 v83, v83, v204
	v_pk_mul_f32 v[72:73], v[204:205], v[72:73] op_sel:[1,0]
	v_pk_mul_f32 v[74:75], v[204:205], v[74:75] op_sel:[1,0]
	v_pk_mul_f32 v[80:81], v[204:205], v[80:81] op_sel:[1,0]
	v_pk_mul_f32 v[82:83], v[204:205], v[82:83] op_sel:[1,0]
	v_pk_fma_f32 v[4:5], v[72:73], v[168:169], v[4:5]
	v_pk_fma_f32 v[6:7], v[74:75], v[170:171], v[6:7]
	v_pk_fma_f32 v[0:1], v[80:81], v[172:173], v[0:1]
	v_pk_fma_f32 v[2:3], v[82:83], v[174:175], v[2:3]
	v_cvt_pk_f16_f32 v4, v4, v5
	v_cvt_pk_f16_f32 v5, v6, v7
	v_cvt_pk_f16_f32 v6, v0, v1
	v_cvt_pk_f16_f32 v7, v2, v3
	ds_write_b128 v235, v[4:7] offset:64
	v_fma_mix_f32 v244, v4, 1.0, v244 op_sel_hi:[1,0,0]
	v_fma_mix_f32 v245, v4, v4, v245 op_sel_hi:[1,1,0]
	v_fma_mix_f32 v244, v4, 1.0, v244 op_sel:[1,0,0] op_sel_hi:[1,0,0]
	v_fma_mix_f32 v245, v4, v4, v245 op_sel:[1,1,0] op_sel_hi:[1,1,0]
	v_fma_mix_f32 v244, v5, 1.0, v244 op_sel_hi:[1,0,0]
	v_fma_mix_f32 v245, v5, v5, v245 op_sel_hi:[1,1,0]
	v_fma_mix_f32 v244, v5, 1.0, v244 op_sel:[1,0,0] op_sel_hi:[1,0,0]
	v_fma_mix_f32 v245, v5, v5, v245 op_sel:[1,1,0] op_sel_hi:[1,1,0]
	v_fma_mix_f32 v244, v6, 1.0, v244 op_sel_hi:[1,0,0]
	v_fma_mix_f32 v245, v6, v6, v245 op_sel_hi:[1,1,0]
	v_fma_mix_f32 v244, v6, 1.0, v244 op_sel:[1,0,0] op_sel_hi:[1,0,0]
	v_fma_mix_f32 v245, v6, v6, v245 op_sel:[1,1,0] op_sel_hi:[1,1,0]
	v_fma_mix_f32 v244, v7, 1.0, v244 op_sel_hi:[1,0,0]
	v_fma_mix_f32 v245, v7, v7, v245 op_sel_hi:[1,1,0]
	v_fma_mix_f32 v244, v7, 1.0, v244 op_sel:[1,0,0] op_sel_hi:[1,0,0]
	v_fma_mix_f32 v245, v7, v7, v245 op_sel:[1,1,0] op_sel_hi:[1,1,0]
	ds_read_b128 v[108:111], v236
	ds_read_b128 v[100:103], v236 offset:1152
	s_waitcnt lgkmcnt(0)
	v_add_u32_e32 v83, 0x42000, v225
	buffer_store_dwordx4 v[108:111], v83, s[24:27], 0 offen nt
	v_add_u32_e32 v82, 0x45000, v225
	buffer_store_dwordx4 v[100:103], v82, s[24:27], 0 offen nt
	v_xor_b32_e32 v246, 16, v234
	v_lshlrev_b32_e32 v246, 2, v246
	v_xor_b32_e32 v247, 32, v234
	v_lshlrev_b32_e32 v247, 2, v247
	ds_bpermute_b32 v92, v246, v206
	ds_bpermute_b32 v93, v246, v207
	ds_bpermute_b32 v94, v246, v140
	ds_bpermute_b32 v95, v246, v141
	ds_bpermute_b32 v120, v246, v142
	ds_bpermute_b32 v121, v246, v143
	ds_bpermute_b32 v122, v246, v216
	ds_bpermute_b32 v123, v246, v217
	s_waitcnt lgkmcnt(0)
	v_pk_add_f32 v[206:207], v[206:207], v[92:93]
	v_pk_add_f32 v[140:141], v[140:141], v[94:95]
	v_pk_add_f32 v[142:143], v[142:143], v[120:121]
	v_pk_add_f32 v[216:217], v[216:217], v[122:123]
	ds_bpermute_b32 v92, v246, v218
	ds_bpermute_b32 v93, v246, v219
	ds_bpermute_b32 v94, v246, v208
	ds_bpermute_b32 v95, v246, v209
	ds_bpermute_b32 v120, v246, v210
	ds_bpermute_b32 v121, v246, v211
	ds_bpermute_b32 v122, v246, v244
	ds_bpermute_b32 v123, v246, v245
	s_waitcnt lgkmcnt(0)
	v_pk_add_f32 v[218:219], v[218:219], v[92:93]
	v_pk_add_f32 v[208:209], v[208:209], v[94:95]
	v_pk_add_f32 v[210:211], v[210:211], v[120:121]
	v_pk_add_f32 v[244:245], v[244:245], v[122:123]
	ds_bpermute_b32 v92, v247, v206
	ds_bpermute_b32 v93, v247, v207
	ds_bpermute_b32 v94, v247, v140
	ds_bpermute_b32 v95, v247, v141
	ds_bpermute_b32 v120, v247, v142
	ds_bpermute_b32 v121, v247, v143
	ds_bpermute_b32 v122, v247, v216
	ds_bpermute_b32 v123, v247, v217
	s_waitcnt lgkmcnt(0)
	v_pk_add_f32 v[206:207], v[206:207], v[92:93]
	v_pk_add_f32 v[140:141], v[140:141], v[94:95]
	v_pk_add_f32 v[142:143], v[142:143], v[120:121]
	v_pk_add_f32 v[216:217], v[216:217], v[122:123]
	ds_bpermute_b32 v92, v247, v218
	ds_bpermute_b32 v93, v247, v219
	ds_bpermute_b32 v94, v247, v208
	ds_bpermute_b32 v95, v247, v209
	ds_bpermute_b32 v120, v247, v210
	ds_bpermute_b32 v121, v247, v211
	ds_bpermute_b32 v122, v247, v244
	ds_bpermute_b32 v123, v247, v245
	s_waitcnt lgkmcnt(0)
	v_pk_add_f32 v[218:219], v[218:219], v[92:93]
	v_pk_add_f32 v[208:209], v[208:209], v[94:95]
	v_pk_add_f32 v[210:211], v[210:211], v[120:121]
	v_pk_add_f32 v[244:245], v[244:245], v[122:123]
	global_store_dwordx2 v224, v[206:207], s[100:101] offset:-2048
	global_store_dwordx2 v224, v[140:141], s[100:101] offset:-512
	global_store_dwordx2 v224, v[142:143], s[100:101] offset:1024
	global_store_dwordx2 v224, v[216:217], s[100:101] offset:2560
	s_add_u32 s100, s100, 0x3000
	s_addc_u32 s101, s101, 0
	global_store_dwordx2 v224, v[218:219], s[100:101] offset:-2048
	global_store_dwordx2 v224, v[208:209], s[100:101] offset:-512
	global_store_dwordx2 v224, v[210:211], s[100:101] offset:1024
	global_store_dwordx2 v224, v[244:245], s[100:101] offset:2560
	s_mov_b32 s83, s81
	s_mov_b32 s84, s82
	s_mov_b64 s[40:41], s[0:1]
	s_mov_b64 s[38:39], s[8:9]
	s_mov_b64 vcc, s[6:7]
	s_cbranch_vccz .LBB8_12
	s_waitcnt vmcnt(0)
	s_cmpk_gt_u32 s44, 0xff
	s_cbranch_scc1 .LBB8_31
	s_barrier

.LBB8_32:
	s_endpgm
	s_endpgm
	s_endpgm
	s_endpgm
	s_endpgm
	s_endpgm
	s_endpgm
	s_endpgm
	s_endpgm
	s_endpgm
	s_endpgm
	s_endpgm
	s_endpgm
	s_endpgm
	s_endpgm
	s_endpgm
	s_endpgm
	s_endpgm
	s_endpgm
	s_endpgm
	s_endpgm
	s_endpgm
	s_endpgm
	s_endpgm
	s_endpgm
	s_endpgm
	s_endpgm
	s_endpgm
	s_endpgm
	s_endpgm
	s_endpgm
	s_endpgm
	s_endpgm
	s_endpgm
	s_endpgm
	s_endpgm
	s_endpgm
	s_endpgm
	s_endpgm
	s_endpgm
	s_endpgm
	s_endpgm
	s_endpgm
	s_endpgm
	s_endpgm
	s_endpgm
	.section	.rodata,"a",@progbits
	.p2align	6, 0x0
	.amdhsa_kernel _Z6k_gemmIN2pg6EpiResELi768EEvNS0_4GemmET_
		.amdhsa_group_segment_fixed_size 0
		.amdhsa_private_segment_fixed_size 0
		.amdhsa_kernarg_size 344
		.amdhsa_user_sgpr_count 2
		.amdhsa_user_sgpr_dispatch_ptr 0
		.amdhsa_user_sgpr_queue_ptr 0
		.amdhsa_user_sgpr_kernarg_segment_ptr 1
		.amdhsa_user_sgpr_dispatch_id 0
		.amdhsa_user_sgpr_kernarg_preload_length 0
		.amdhsa_user_sgpr_kernarg_preload_offset 0
		.amdhsa_user_sgpr_private_segment_size 0
		.amdhsa_uses_dynamic_stack 0
		.amdhsa_enable_private_segment 0
		.amdhsa_system_sgpr_workgroup_id_x 1
		.amdhsa_system_sgpr_workgroup_id_y 0
		.amdhsa_system_sgpr_workgroup_id_z 0
		.amdhsa_system_sgpr_workgroup_info 0
		.amdhsa_system_vgpr_workitem_id 0
		.amdhsa_next_free_vgpr 256
		.amdhsa_next_free_sgpr 102
		.amdhsa_accum_offset 256
		.amdhsa_reserve_vcc 1
		.amdhsa_float_round_mode_32 0
		.amdhsa_float_round_mode_16_64 0
		.amdhsa_float_denorm_mode_32 3
		.amdhsa_float_denorm_mode_16_64 3
		.amdhsa_dx10_clamp 1
		.amdhsa_ieee_mode 1
		.amdhsa_fp16_overflow 0
		.amdhsa_tg_split 0
		.amdhsa_exception_fp_ieee_invalid_op 0
		.amdhsa_exception_fp_denorm_src 0
		.amdhsa_exception_fp_ieee_div_zero 0
		.amdhsa_exception_fp_ieee_overflow 0
		.amdhsa_exception_fp_ieee_underflow 0
		.amdhsa_exception_fp_ieee_inexact 0
		.amdhsa_exception_int_div_zero 0
	.end_amdhsa_kernel

.LBB10_27:
	ds_read_b128 v[72:75], v231
	ds_read_b128 v[80:83], v231 offset:1024
	ds_read_b128 v[88:91], v231 offset:2048
	ds_read_b128 v[92:95], v231 offset:3072
	s_add_u32 s40, s38, 0xfff40080
	s_addc_u32 s41, s39, -1
	s_cmp_eq_u32 s87, 44
	s_cselect_b32 s43, s9, s41
	s_cselect_b32 s42, s8, s40
	s_cselect_b32 s41, s1, s86
	s_cselect_b32 s40, s0, s85
	v_lshl_add_u64 v[190:191], s[38:39], 0, v[184:185]
	s_add_i32 m0, s51, 0xc000
	ds_read_b128 v[136:139], v232
	ds_read_b128 v[148:151], v232 offset:1024
	ds_read_b128 v[152:155], v232 offset:2048
	ds_read_b128 v[156:159], v232 offset:3072
	ds_read_b128 v[160:163], v232 offset:4096
	ds_read_b128 v[164:167], v232 offset:5120
	ds_read_b128 v[168:171], v232 offset:6144
	ds_read_b128 v[172:175], v232 offset:7168
	global_load_lds_dwordx4 v[190:191], off
	v_lshl_add_u64 v[190:191], s[38:39], 0, v[186:187]
	s_add_i32 m0, s51, 0xe000
	s_nop 0
	global_load_lds_dwordx4 v[190:191], off
	s_waitcnt lgkmcnt(8)
	s_barrier
	s_waitcnt lgkmcnt(0)
	s_setprio 1
	s_waitcnt lgkmcnt(0)
	v_mfma_f32_16x16x32_f16 v[144:147], v[72:75], v[136:139], v[144:147]
	v_mfma_f32_16x16x32_f16 v[140:143], v[88:91], v[136:139], v[140:143]
	v_mfma_f32_16x16x32_f16 v[124:127], v[72:75], v[152:155], v[124:127]
	v_mfma_f32_16x16x32_f16 v[120:123], v[88:91], v[152:155], v[120:123]
	v_mfma_f32_16x16x32_f16 v[108:111], v[72:75], v[160:163], v[108:111]
	v_mfma_f32_16x16x32_f16 v[104:107], v[88:91], v[160:163], v[104:107]
	v_mfma_f32_16x16x32_f16 v[84:87], v[72:75], v[168:171], v[84:87]
	v_mfma_f32_16x16x32_f16 v[76:79], v[88:91], v[168:171], v[76:79]
	v_mfma_f32_16x16x32_f16 v[144:147], v[80:83], v[148:151], v[144:147]
	v_mfma_f32_16x16x32_f16 v[140:143], v[92:95], v[148:151], v[140:143]
	v_mfma_f32_16x16x32_f16 v[124:127], v[80:83], v[156:159], v[124:127]
	v_mfma_f32_16x16x32_f16 v[120:123], v[92:95], v[156:159], v[120:123]
	v_mfma_f32_16x16x32_f16 v[108:111], v[80:83], v[164:167], v[108:111]
	v_mfma_f32_16x16x32_f16 v[104:107], v[92:95], v[164:167], v[104:107]
	v_mfma_f32_16x16x32_f16 v[84:87], v[80:83], v[172:175], v[84:87]
	v_mfma_f32_16x16x32_f16 v[76:79], v[92:95], v[172:175], v[76:79]
	s_setprio 0
	s_barrier
	s_add_i32 s88, s69, s50
	v_lshl_add_u64 v[206:207], s[40:41], 0, v[178:179]
	s_mov_b32 m0, s88
	ds_read_b128 v[190:193], v233
	ds_read_b128 v[194:197], v233 offset:1024
	ds_read_b128 v[198:201], v233 offset:2048
	ds_read_b128 v[202:205], v233 offset:3072
	global_load_lds_dwordx4 v[206:207], off
	v_lshl_add_u64 v[208:209], s[40:41], 0, v[182:183]
	s_add_i32 m0, s88, 0x2000
	s_nop 0
	global_load_lds_dwordx4 v[208:209], off
	s_barrier
	s_waitcnt lgkmcnt(0)
	s_setprio 1
	s_waitcnt lgkmcnt(0)
	v_mfma_f32_16x16x32_f16 v[132:135], v[190:193], v[136:139], v[132:135]
	v_mfma_f32_16x16x32_f16 v[128:131], v[198:201], v[136:139], v[128:131]
	v_mfma_f32_16x16x32_f16 v[116:119], v[190:193], v[152:155], v[116:119]
	v_mfma_f32_16x16x32_f16 v[112:115], v[198:201], v[152:155], v[112:115]
	v_mfma_f32_16x16x32_f16 v[100:103], v[190:193], v[160:163], v[100:103]
	v_mfma_f32_16x16x32_f16 v[96:99], v[198:201], v[160:163], v[96:99]
	v_mfma_f32_16x16x32_f16 v[68:71], v[190:193], v[168:171], v[68:71]
	v_mfma_f32_16x16x32_f16 v[64:67], v[198:201], v[168:171], v[64:67]
	v_mfma_f32_16x16x32_f16 v[132:135], v[194:197], v[148:151], v[132:135]
	v_mfma_f32_16x16x32_f16 v[128:131], v[202:205], v[148:151], v[128:131]
	v_mfma_f32_16x16x32_f16 v[116:119], v[194:197], v[156:159], v[116:119]
	v_mfma_f32_16x16x32_f16 v[112:115], v[202:205], v[156:159], v[112:115]
	v_mfma_f32_16x16x32_f16 v[100:103], v[194:197], v[164:167], v[100:103]
	v_mfma_f32_16x16x32_f16 v[96:99], v[202:205], v[164:167], v[96:99]
	v_mfma_f32_16x16x32_f16 v[68:71], v[194:197], v[172:175], v[68:71]
	v_mfma_f32_16x16x32_f16 v[64:67], v[202:205], v[172:175], v[64:67]
	s_setprio 0
	s_mov_b32 m0, s51
	v_lshl_add_u64 v[210:211], s[42:43], 0, v[176:177]
	s_barrier
	ds_read_b128 v[136:139], v232 offset:16384
	ds_read_b128 v[148:151], v232 offset:17408
	ds_read_b128 v[152:155], v232 offset:18432
	ds_read_b128 v[156:159], v232 offset:19456
	ds_read_b128 v[160:163], v232 offset:20480
	ds_read_b128 v[164:167], v232 offset:21504
	ds_read_b128 v[168:171], v232 offset:22528
	ds_read_b128 v[172:175], v232 offset:23552
	global_load_lds_dwordx4 v[210:211], off
	v_lshl_add_u64 v[212:213], s[42:43], 0, v[180:181]
	s_mov_b32 m0, s52
	s_nop 0
	global_load_lds_dwordx4 v[212:213], off
	s_barrier
	s_waitcnt lgkmcnt(0)
	s_setprio 1
	s_waitcnt lgkmcnt(0)
	v_mfma_f32_16x16x32_f16 v[60:63], v[72:75], v[136:139], v[60:63]
	v_mfma_f32_16x16x32_f16 v[56:59], v[88:91], v[136:139], v[56:59]
	v_mfma_f32_16x16x32_f16 v[44:47], v[72:75], v[152:155], v[44:47]
	v_mfma_f32_16x16x32_f16 v[40:43], v[88:91], v[152:155], v[40:43]
	v_mfma_f32_16x16x32_f16 v[28:31], v[72:75], v[160:163], v[28:31]
	v_mfma_f32_16x16x32_f16 v[24:27], v[88:91], v[160:163], v[24:27]
	v_mfma_f32_16x16x32_f16 v[12:15], v[72:75], v[168:171], v[12:15]
	v_mfma_f32_16x16x32_f16 v[8:11], v[88:91], v[168:171], v[8:11]
	v_mfma_f32_16x16x32_f16 v[60:63], v[80:83], v[148:151], v[60:63]
	v_mfma_f32_16x16x32_f16 v[56:59], v[92:95], v[148:151], v[56:59]
	v_mfma_f32_16x16x32_f16 v[44:47], v[80:83], v[156:159], v[44:47]
	v_mfma_f32_16x16x32_f16 v[40:43], v[92:95], v[156:159], v[40:43]
	v_mfma_f32_16x16x32_f16 v[28:31], v[80:83], v[164:167], v[28:31]
	v_mfma_f32_16x16x32_f16 v[24:27], v[92:95], v[164:167], v[24:27]
	v_mfma_f32_16x16x32_f16 v[12:15], v[80:83], v[172:175], v[12:15]
	v_mfma_f32_16x16x32_f16 v[8:11], v[92:95], v[172:175], v[8:11]
	s_setprio 0
	s_barrier
	s_add_u32 s88, s40, 0x30000
	s_addc_u32 s89, s41, 0
	s_add_i32 s90, s70, s50
	v_lshl_add_u64 v[72:73], s[88:89], 0, v[178:179]
	s_mov_b32 m0, s90
	s_nop 0
	global_load_lds_dwordx4 v[72:73], off
	v_lshl_add_u64 v[72:73], s[88:89], 0, v[182:183]
	s_add_i32 m0, s90, 0x2000
	s_nop 0
	global_load_lds_dwordx4 v[72:73], off
	s_waitcnt vmcnt(6)
	s_barrier
	s_setprio 1
	v_mfma_f32_16x16x32_f16 v[52:55], v[190:193], v[136:139], v[52:55]
	v_mfma_f32_16x16x32_f16 v[48:51], v[198:201], v[136:139], v[48:51]
	v_mfma_f32_16x16x32_f16 v[36:39], v[190:193], v[152:155], v[36:39]
	v_mfma_f32_16x16x32_f16 v[32:35], v[198:201], v[152:155], v[32:35]
	v_mfma_f32_16x16x32_f16 v[20:23], v[190:193], v[160:163], v[20:23]
	v_mfma_f32_16x16x32_f16 v[16:19], v[198:201], v[160:163], v[16:19]
	v_mfma_f32_16x16x32_f16 v[4:7], v[190:193], v[168:171], v[4:7]
	v_mfma_f32_16x16x32_f16 v[0:3], v[198:201], v[168:171], v[0:3]
	v_mfma_f32_16x16x32_f16 v[52:55], v[194:197], v[148:151], v[52:55]
	v_mfma_f32_16x16x32_f16 v[48:51], v[202:205], v[148:151], v[48:51]
	v_mfma_f32_16x16x32_f16 v[36:39], v[194:197], v[156:159], v[36:39]
	v_mfma_f32_16x16x32_f16 v[32:35], v[202:205], v[156:159], v[32:35]
	v_mfma_f32_16x16x32_f16 v[20:23], v[194:197], v[164:167], v[20:23]
	v_mfma_f32_16x16x32_f16 v[16:19], v[202:205], v[164:167], v[16:19]
	v_mfma_f32_16x16x32_f16 v[4:7], v[194:197], v[172:175], v[4:7]
	v_mfma_f32_16x16x32_f16 v[0:3], v[202:205], v[172:175], v[0:3]
	s_setprio 0
	s_add_i32 s88, 0, 0x18000
	v_add_u32_e32 v92, s88, v228
	s_barrier
	ds_read_b128 v[72:75], v92
	ds_read_b128 v[80:83], v92 offset:1024
	ds_read_b128 v[88:91], v92 offset:2048
	ds_read_b128 v[92:95], v92 offset:3072
	s_add_u32 s42, s42, 0xc0000
	s_addc_u32 s43, s43, 0
	s_mov_b32 m0, s53
	v_lshl_add_u64 v[190:191], s[42:43], 0, v[176:177]
	ds_read_b128 v[136:139], v232 offset:32768
	ds_read_b128 v[148:151], v232 offset:33792
	ds_read_b128 v[152:155], v232 offset:34816
	ds_read_b128 v[156:159], v232 offset:35840
	ds_read_b128 v[160:163], v232 offset:36864
	ds_read_b128 v[164:167], v232 offset:37888
	ds_read_b128 v[168:171], v232 offset:38912
	ds_read_b128 v[172:175], v232 offset:39936
	global_load_lds_dwordx4 v[190:191], off
	v_lshl_add_u64 v[190:191], s[42:43], 0, v[180:181]
	s_mov_b32 m0, s54
	s_nop 0
	global_load_lds_dwordx4 v[190:191], off
	s_waitcnt lgkmcnt(8)
	s_barrier
	s_waitcnt lgkmcnt(0)
	s_setprio 1
	s_waitcnt lgkmcnt(0)
	v_mfma_f32_16x16x32_f16 v[144:147], v[72:75], v[136:139], v[144:147]
	v_mfma_f32_16x16x32_f16 v[140:143], v[88:91], v[136:139], v[140:143]
	v_mfma_f32_16x16x32_f16 v[124:127], v[72:75], v[152:155], v[124:127]
	v_mfma_f32_16x16x32_f16 v[120:123], v[88:91], v[152:155], v[120:123]
	v_mfma_f32_16x16x32_f16 v[108:111], v[72:75], v[160:163], v[108:111]
	v_mfma_f32_16x16x32_f16 v[104:107], v[88:91], v[160:163], v[104:107]
	v_mfma_f32_16x16x32_f16 v[84:87], v[72:75], v[168:171], v[84:87]
	v_mfma_f32_16x16x32_f16 v[76:79], v[88:91], v[168:171], v[76:79]
	v_mfma_f32_16x16x32_f16 v[144:147], v[80:83], v[148:151], v[144:147]
	v_mfma_f32_16x16x32_f16 v[140:143], v[92:95], v[148:151], v[140:143]
	v_mfma_f32_16x16x32_f16 v[124:127], v[80:83], v[156:159], v[124:127]
	v_mfma_f32_16x16x32_f16 v[120:123], v[92:95], v[156:159], v[120:123]
	v_mfma_f32_16x16x32_f16 v[108:111], v[80:83], v[164:167], v[108:111]
	v_mfma_f32_16x16x32_f16 v[104:107], v[92:95], v[164:167], v[104:107]
	v_mfma_f32_16x16x32_f16 v[84:87], v[80:83], v[172:175], v[84:87]
	v_mfma_f32_16x16x32_f16 v[76:79], v[92:95], v[172:175], v[76:79]
	s_setprio 0
	s_barrier
	s_add_i32 s42, 0, 0x1c000
	s_add_i32 s43, s88, s50
	v_add_u32_e32 v202, s42, v228
	v_lshl_add_u64 v[206:207], v[206:207], 0, s[36:37]
	s_mov_b32 m0, s43
	ds_read_b128 v[190:193], v202
	ds_read_b128 v[194:197], v202 offset:1024
	ds_read_b128 v[198:201], v202 offset:2048
	ds_read_b128 v[202:205], v202 offset:3072
	global_load_lds_dwordx4 v[206:207], off
	v_lshl_add_u64 v[206:207], v[208:209], 0, s[36:37]
	s_add_i32 m0, s43, 0x2000
	s_nop 0
	global_load_lds_dwordx4 v[206:207], off
	s_barrier
	s_waitcnt lgkmcnt(0)
	s_setprio 1
	s_waitcnt lgkmcnt(0)
	v_mfma_f32_16x16x32_f16 v[132:135], v[190:193], v[136:139], v[132:135]
	v_mfma_f32_16x16x32_f16 v[128:131], v[198:201], v[136:139], v[128:131]
	v_mfma_f32_16x16x32_f16 v[116:119], v[190:193], v[152:155], v[116:119]
	v_mfma_f32_16x16x32_f16 v[112:115], v[198:201], v[152:155], v[112:115]
	v_mfma_f32_16x16x32_f16 v[100:103], v[190:193], v[160:163], v[100:103]
	v_mfma_f32_16x16x32_f16 v[96:99], v[198:201], v[160:163], v[96:99]
	v_mfma_f32_16x16x32_f16 v[68:71], v[190:193], v[168:171], v[68:71]
	v_mfma_f32_16x16x32_f16 v[64:67], v[198:201], v[168:171], v[64:67]
	v_mfma_f32_16x16x32_f16 v[132:135], v[194:197], v[148:151], v[132:135]
	v_mfma_f32_16x16x32_f16 v[128:131], v[202:205], v[148:151], v[128:131]
	v_mfma_f32_16x16x32_f16 v[116:119], v[194:197], v[156:159], v[116:119]
	v_mfma_f32_16x16x32_f16 v[112:115], v[202:205], v[156:159], v[112:115]
	v_mfma_f32_16x16x32_f16 v[100:103], v[194:197], v[164:167], v[100:103]
	v_mfma_f32_16x16x32_f16 v[96:99], v[202:205], v[164:167], v[96:99]
	v_mfma_f32_16x16x32_f16 v[68:71], v[194:197], v[172:175], v[68:71]
	v_mfma_f32_16x16x32_f16 v[64:67], v[202:205], v[172:175], v[64:67]
	s_setprio 0
	s_mov_b32 m0, s58
	v_lshl_add_u64 v[206:207], v[210:211], 0, s[36:37]
	s_barrier
	ds_read_b128 v[136:139], v232 offset:49152
	ds_read_b128 v[148:151], v232 offset:50176
	ds_read_b128 v[152:155], v232 offset:51200
	ds_read_b128 v[156:159], v232 offset:52224
	ds_read_b128 v[160:163], v232 offset:53248
	ds_read_b128 v[164:167], v232 offset:54272
	ds_read_b128 v[168:171], v232 offset:55296
	ds_read_b128 v[172:175], v232 offset:56320
	global_load_lds_dwordx4 v[206:207], off
	v_lshl_add_u64 v[206:207], v[212:213], 0, s[36:37]
	s_mov_b32 m0, s59
	s_nop 0
	global_load_lds_dwordx4 v[206:207], off
	s_barrier
	s_waitcnt lgkmcnt(0)
	s_setprio 1
	s_waitcnt lgkmcnt(0)
	v_mfma_f32_16x16x32_f16 v[60:63], v[72:75], v[136:139], v[60:63]
	v_mfma_f32_16x16x32_f16 v[56:59], v[88:91], v[136:139], v[56:59]
	v_mfma_f32_16x16x32_f16 v[44:47], v[72:75], v[152:155], v[44:47]
	v_mfma_f32_16x16x32_f16 v[40:43], v[88:91], v[152:155], v[40:43]
	v_mfma_f32_16x16x32_f16 v[28:31], v[72:75], v[160:163], v[28:31]
	v_mfma_f32_16x16x32_f16 v[24:27], v[88:91], v[160:163], v[24:27]
	v_mfma_f32_16x16x32_f16 v[12:15], v[72:75], v[168:171], v[12:15]
	v_mfma_f32_16x16x32_f16 v[8:11], v[88:91], v[168:171], v[8:11]
	v_mfma_f32_16x16x32_f16 v[60:63], v[80:83], v[148:151], v[60:63]
	v_mfma_f32_16x16x32_f16 v[56:59], v[92:95], v[148:151], v[56:59]
	v_mfma_f32_16x16x32_f16 v[44:47], v[80:83], v[156:159], v[44:47]
	v_mfma_f32_16x16x32_f16 v[40:43], v[92:95], v[156:159], v[40:43]
	v_mfma_f32_16x16x32_f16 v[28:31], v[80:83], v[164:167], v[28:31]
	v_mfma_f32_16x16x32_f16 v[24:27], v[92:95], v[164:167], v[24:27]
	v_mfma_f32_16x16x32_f16 v[12:15], v[80:83], v[172:175], v[12:15]
	v_mfma_f32_16x16x32_f16 v[8:11], v[92:95], v[172:175], v[8:11]
	s_setprio 0
	s_barrier
	s_add_u32 s40, s40, 0x30080
	s_addc_u32 s41, s41, 0
	s_add_i32 s42, s42, s50
	v_lshl_add_u64 v[72:73], s[40:41], 0, v[178:179]
	s_mov_b32 m0, s42
	s_nop 0
	global_load_lds_dwordx4 v[72:73], off
	v_lshl_add_u64 v[72:73], s[40:41], 0, v[182:183]
	s_add_i32 m0, s42, 0x2000
	s_nop 0
	global_load_lds_dwordx4 v[72:73], off
	s_waitcnt vmcnt(6)
	s_barrier
	s_setprio 1
	v_mfma_f32_16x16x32_f16 v[52:55], v[190:193], v[136:139], v[52:55]
	v_mfma_f32_16x16x32_f16 v[48:51], v[198:201], v[136:139], v[48:51]
	v_mfma_f32_16x16x32_f16 v[36:39], v[190:193], v[152:155], v[36:39]
	v_mfma_f32_16x16x32_f16 v[32:35], v[198:201], v[152:155], v[32:35]
	v_mfma_f32_16x16x32_f16 v[20:23], v[190:193], v[160:163], v[20:23]
	v_mfma_f32_16x16x32_f16 v[16:19], v[198:201], v[160:163], v[16:19]
	v_mfma_f32_16x16x32_f16 v[4:7], v[190:193], v[168:171], v[4:7]
	v_mfma_f32_16x16x32_f16 v[0:3], v[198:201], v[168:171], v[0:3]
	v_mfma_f32_16x16x32_f16 v[52:55], v[194:197], v[148:151], v[52:55]
	v_mfma_f32_16x16x32_f16 v[48:51], v[202:205], v[148:151], v[48:51]
	v_mfma_f32_16x16x32_f16 v[36:39], v[194:197], v[156:159], v[36:39]
	v_mfma_f32_16x16x32_f16 v[32:35], v[202:205], v[156:159], v[32:35]
	v_mfma_f32_16x16x32_f16 v[20:23], v[194:197], v[164:167], v[20:23]
	v_mfma_f32_16x16x32_f16 v[16:19], v[202:205], v[164:167], v[16:19]
	v_mfma_f32_16x16x32_f16 v[4:7], v[194:197], v[172:175], v[4:7]
	v_mfma_f32_16x16x32_f16 v[0:3], v[202:205], v[172:175], v[0:3]
	s_setprio 0
	s_add_i32 s87, s87, 2
	s_add_u32 s38, s38, 0x100
	s_addc_u32 s39, s39, 0
	s_add_u32 s85, s85, 0x100
	s_addc_u32 s86, s86, 0
	s_cmp_gt_u32 s87, 45
	s_barrier
	s_cbranch_scc0 .LBB10_27
	s_lshl_b32 s92, s84, 8
	s_add_i32 s92, s92, s57
	s_lshl_b32 s93, s83, 8
	s_or_b32 s93, s93, s60
	v_lshlrev_b32_e32 v237, 2, v226
	s_lshl_b32 s96, s93, 2
	s_add_u32 s94, s16, s96
	s_addc_u32 s95, s17, 0
	global_load_dwordx4 v[72:75], v237, s[94:95] offset:0
	global_load_dwordx4 v[80:83], v237, s[94:95] offset:16
	global_load_dwordx4 v[88:91], v237, s[94:95] offset:128
	global_load_dwordx4 v[92:95], v237, s[94:95] offset:144
	s_add_u32 s94, s18, s96
	s_addc_u32 s95, s19, 0
	global_load_dwordx4 v[136:139], v237, s[94:95] offset:0
	global_load_dwordx4 v[148:151], v237, s[94:95] offset:16
	global_load_dwordx4 v[152:155], v237, s[94:95] offset:128
	global_load_dwordx4 v[156:159], v237, s[94:95] offset:144
	s_add_u32 s94, s14, s96
	s_addc_u32 s95, s15, 0
	global_load_dwordx4 v[160:163], v237, s[94:95] offset:0
	global_load_dwordx4 v[164:167], v237, s[94:95] offset:16
	global_load_dwordx4 v[168:171], v237, s[94:95] offset:128
	global_load_dwordx4 v[172:175], v237, s[94:95] offset:144
	v_lshlrev_b32_e32 v190, 3, v227
	s_lshl_b32 s96, s92, 3
	s_add_u32 s94, s12, s96
	s_addc_u32 s95, s13, 0
	global_load_dwordx2 v[238:239], v190, s[94:95] offset:0
	global_load_dwordx2 v[192:193], v190, s[94:95] offset:128
	global_load_dwordx2 v[194:195], v190, s[94:95] offset:256
	global_load_dwordx2 v[196:197], v190, s[94:95] offset:384
	global_load_dwordx2 v[198:199], v190, s[94:95] offset:1024
	global_load_dwordx2 v[200:201], v190, s[94:95] offset:1152
	global_load_dwordx2 v[202:203], v190, s[94:95] offset:1280
	global_load_dwordx2 v[204:205], v190, s[94:95] offset:1408
	v_mul_u32_u24_e32 v191, 0x600, v227
	v_lshl_add_u32 v191, v226, 1, v191
	s_mul_i32 s96, s92, 0x600
	s_lshl_b32 s97, s93, 1
	s_add_u32 s96, s96, s97
	s_add_u32 s98, s10, s96
	s_addc_u32 s99, s11, 0
	s_add_u32 s94, s98, 0x0
	s_addc_u32 s95, s99, 0
	global_load_dwordx4 v[208:211], v191, s[94:95] offset:0 nt
	global_load_dwordx4 v[212:215], v191, s[94:95] offset:64 nt
	s_add_u32 s94, s98, 0x6000
	s_addc_u32 s95, s99, 0
	global_load_dwordx4 v[216:219], v191, s[94:95] offset:0 nt
	global_load_dwordx4 v[220:223], v191, s[94:95] offset:64 nt
	v_add_u32_e32 v225, s92, v229
	v_mul_u32_u24_e32 v225, 0x600, v225
	s_lshl_b32 s97, s93, 1
	v_add3_u32 v225, v225, v230, s97
	v_mul_u32_u24_e32 v224, 0x60, v227
	s_mul_i32 s96, s92, 0x60
	s_lshl_b32 s97, s83, 5
	s_add_u32 s96, s96, s97
	s_lshr_b32 s97, s60, 3
	s_add_u32 s96, s96, s97
	s_add_u32 s96, s96, 0x800
	s_add_u32 s100, s28, s96
	s_addc_u32 s101, s29, 0
	s_waitcnt vmcnt(19)
	v_pk_add_f32 v[72:73], v[72:73], v[136:137]
	v_pk_add_f32 v[74:75], v[74:75], v[138:139]
	s_waitcnt vmcnt(18)
	v_pk_add_f32 v[80:81], v[80:81], v[148:149]
	v_pk_add_f32 v[82:83], v[82:83], v[150:151]
	s_waitcnt vmcnt(17)
	v_pk_add_f32 v[88:89], v[88:89], v[152:153]
	v_pk_add_f32 v[90:91], v[90:91], v[154:155]
	s_waitcnt vmcnt(16)
	v_pk_add_f32 v[92:93], v[92:93], v[156:157]
	v_pk_add_f32 v[94:95], v[94:95], v[158:159]
	v_pk_add_f32 v[144:145], v[144:145], v[72:73]
	v_pk_add_f32 v[146:147], v[146:147], v[74:75]
	v_pk_add_f32 v[124:125], v[124:125], v[72:73]
	v_pk_add_f32 v[126:127], v[126:127], v[74:75]
	v_pk_add_f32 v[108:109], v[108:109], v[72:73]
	v_pk_add_f32 v[110:111], v[110:111], v[74:75]
	v_pk_add_f32 v[84:85], v[84:85], v[72:73]
	v_pk_add_f32 v[86:87], v[86:87], v[74:75]
	v_pk_add_f32 v[60:61], v[60:61], v[72:73]
	v_pk_add_f32 v[62:63], v[62:63], v[74:75]
	v_pk_add_f32 v[44:45], v[44:45], v[72:73]
	v_pk_add_f32 v[46:47], v[46:47], v[74:75]
	v_pk_add_f32 v[28:29], v[28:29], v[72:73]
	v_pk_add_f32 v[30:31], v[30:31], v[74:75]
	v_pk_add_f32 v[12:13], v[12:13], v[72:73]
	v_pk_add_f32 v[14:15], v[14:15], v[74:75]
	v_pk_add_f32 v[140:141], v[140:141], v[80:81]
	v_pk_add_f32 v[142:143], v[142:143], v[82:83]
	v_pk_add_f32 v[120:121], v[120:121], v[80:81]
	v_pk_add_f32 v[122:123], v[122:123], v[82:83]
	v_pk_add_f32 v[104:105], v[104:105], v[80:81]
	v_pk_add_f32 v[106:107], v[106:107], v[82:83]
	v_pk_add_f32 v[76:77], v[76:77], v[80:81]
	v_pk_add_f32 v[78:79], v[78:79], v[82:83]
	v_pk_add_f32 v[56:57], v[56:57], v[80:81]
	v_pk_add_f32 v[58:59], v[58:59], v[82:83]
	v_pk_add_f32 v[40:41], v[40:41], v[80:81]
	v_pk_add_f32 v[42:43], v[42:43], v[82:83]
	v_pk_add_f32 v[24:25], v[24:25], v[80:81]
	v_pk_add_f32 v[26:27], v[26:27], v[82:83]
	v_pk_add_f32 v[8:9], v[8:9], v[80:81]
	v_pk_add_f32 v[10:11], v[10:11], v[82:83]
	v_pk_add_f32 v[132:133], v[132:133], v[88:89]
	v_pk_add_f32 v[134:135], v[134:135], v[90:91]
	v_pk_add_f32 v[116:117], v[116:117], v[88:89]
	v_pk_add_f32 v[118:119], v[118:119], v[90:91]
	v_pk_add_f32 v[100:101], v[100:101], v[88:89]
	v_pk_add_f32 v[102:103], v[102:103], v[90:91]
	v_pk_add_f32 v[68:69], v[68:69], v[88:89]
	v_pk_add_f32 v[70:71], v[70:71], v[90:91]
	v_pk_add_f32 v[52:53], v[52:53], v[88:89]
	v_pk_add_f32 v[54:55], v[54:55], v[90:91]
	v_pk_add_f32 v[36:37], v[36:37], v[88:89]
	v_pk_add_f32 v[38:39], v[38:39], v[90:91]
	v_pk_add_f32 v[20:21], v[20:21], v[88:89]
	v_pk_add_f32 v[22:23], v[22:23], v[90:91]
	v_pk_add_f32 v[4:5], v[4:5], v[88:89]
	v_pk_add_f32 v[6:7], v[6:7], v[90:91]
	v_pk_add_f32 v[128:129], v[128:129], v[92:93]
	v_pk_add_f32 v[130:131], v[130:131], v[94:95]
	v_pk_add_f32 v[112:113], v[112:113], v[92:93]
	v_pk_add_f32 v[114:115], v[114:115], v[94:95]
	v_pk_add_f32 v[96:97], v[96:97], v[92:93]
	v_pk_add_f32 v[98:99], v[98:99], v[94:95]
	v_pk_add_f32 v[64:65], v[64:65], v[92:93]
	v_pk_add_f32 v[66:67], v[66:67], v[94:95]
	v_pk_add_f32 v[48:49], v[48:49], v[92:93]
	v_pk_add_f32 v[50:51], v[50:51], v[94:95]
	v_pk_add_f32 v[32:33], v[32:33], v[92:93]
	v_pk_add_f32 v[34:35], v[34:35], v[94:95]
	v_pk_add_f32 v[16:17], v[16:17], v[92:93]
	v_pk_add_f32 v[18:19], v[18:19], v[94:95]
	v_pk_add_f32 v[0:1], v[0:1], v[92:93]
	v_pk_add_f32 v[2:3], v[2:3], v[94:95]
	s_add_u32 s94, s98, 0xc000
	s_addc_u32 s95, s99, 0
	global_load_dwordx4 v[240:243], v191, s[94:95] offset:0 nt
	global_load_dwordx4 v[244:247], v191, s[94:95] offset:64 nt
	s_add_u32 s94, s98, 0x12000
	s_addc_u32 s95, s99, 0
	global_load_dwordx4 v[248:251], v191, s[94:95] offset:0 nt
	global_load_dwordx4 v[252:255], v191, s[94:95] offset:64 nt
	s_add_u32 s94, s98, 0x30000
	s_addc_u32 s95, s99, 0
	global_load_dwordx4 v[136:139], v191, s[94:95] offset:0 nt
	global_load_dwordx4 v[148:151], v191, s[94:95] offset:64 nt
	s_add_u32 s94, s98, 0x36000
	s_addc_u32 s95, s99, 0
	global_load_dwordx4 v[152:155], v191, s[94:95] offset:0 nt
	global_load_dwordx4 v[156:159], v191, s[94:95] offset:64 nt
	s_waitcnt vmcnt(19)
	s_waitcnt vmcnt(11)
	v_cvt_f32_f16_e32 v72, v208
	v_cvt_f32_f16_sdwa v73, v208 dst_sel:DWORD dst_unused:UNUSED_PAD src0_sel:WORD_1
	v_cvt_f32_f16_e32 v74, v209
	v_cvt_f32_f16_sdwa v75, v209 dst_sel:DWORD dst_unused:UNUSED_PAD src0_sel:WORD_1
	v_cvt_f32_f16_e32 v80, v210
	v_cvt_f32_f16_sdwa v81, v210 dst_sel:DWORD dst_unused:UNUSED_PAD src0_sel:WORD_1
	v_cvt_f32_f16_e32 v82, v211
	v_cvt_f32_f16_sdwa v83, v211 dst_sel:DWORD dst_unused:UNUSED_PAD src0_sel:WORD_1
	v_sub_f32_e32 v72, v72, v238
	v_sub_f32_e32 v73, v73, v238
	v_sub_f32_e32 v74, v74, v238
	v_sub_f32_e32 v75, v75, v238
	v_sub_f32_e32 v80, v80, v238
	v_sub_f32_e32 v81, v81, v238
	v_sub_f32_e32 v82, v82, v238
	v_sub_f32_e32 v83, v83, v238
	v_pk_mul_f32 v[72:73], v[238:239], v[72:73] op_sel:[1,0]
	v_pk_mul_f32 v[74:75], v[238:239], v[74:75] op_sel:[1,0]
	v_pk_mul_f32 v[80:81], v[238:239], v[80:81] op_sel:[1,0]
	v_pk_mul_f32 v[82:83], v[238:239], v[82:83] op_sel:[1,0]
	v_pk_fma_f32 v[144:145], v[72:73], v[160:161], v[144:145]
	v_pk_fma_f32 v[146:147], v[74:75], v[162:163], v[146:147]
	v_pk_fma_f32 v[140:141], v[80:81], v[164:165], v[140:141]
	v_pk_fma_f32 v[142:143], v[82:83], v[166:167], v[142:143]
	v_cvt_pk_f16_f32 v144, v144, v145
	v_cvt_pk_f16_f32 v145, v146, v147
	v_cvt_pk_f16_f32 v146, v140, v141
	v_cvt_pk_f16_f32 v147, v142, v143
	ds_write_b128 v235, v[144:147]
	v_fma_mix_f32 v206, v144, 1.0, 0 op_sel_hi:[1,0,0]
	v_fma_mix_f32 v207, v144, v144, 0 op_sel_hi:[1,1,0]
	v_fma_mix_f32 v206, v144, 1.0, v206 op_sel:[1,0,0] op_sel_hi:[1,0,0]
	v_fma_mix_f32 v207, v144, v144, v207 op_sel:[1,1,0] op_sel_hi:[1,1,0]
	v_fma_mix_f32 v206, v145, 1.0, v206 op_sel_hi:[1,0,0]
	v_fma_mix_f32 v207, v145, v145, v207 op_sel_hi:[1,1,0]
	v_fma_mix_f32 v206, v145, 1.0, v206 op_sel:[1,0,0] op_sel_hi:[1,0,0]
	v_fma_mix_f32 v207, v145, v145, v207 op_sel:[1,1,0] op_sel_hi:[1,1,0]
	v_fma_mix_f32 v206, v146, 1.0, v206 op_sel_hi:[1,0,0]
	v_fma_mix_f32 v207, v146, v146, v207 op_sel_hi:[1,1,0]
	v_fma_mix_f32 v206, v146, 1.0, v206 op_sel:[1,0,0] op_sel_hi:[1,0,0]
	v_fma_mix_f32 v207, v146, v146, v207 op_sel:[1,1,0] op_sel_hi:[1,1,0]
	v_fma_mix_f32 v206, v147, 1.0, v206 op_sel_hi:[1,0,0]
	v_fma_mix_f32 v207, v147, v147, v207 op_sel_hi:[1,1,0]
	v_fma_mix_f32 v206, v147, 1.0, v206 op_sel:[1,0,0] op_sel_hi:[1,0,0]
	v_fma_mix_f32 v207, v147, v147, v207 op_sel:[1,1,0] op_sel_hi:[1,1,0]
	s_waitcnt vmcnt(10)
	v_cvt_f32_f16_e32 v72, v212
	v_cvt_f32_f16_sdwa v73, v212 dst_sel:DWORD dst_unused:UNUSED_PAD src0_sel:WORD_1
	v_cvt_f32_f16_e32 v74, v213
	v_cvt_f32_f16_sdwa v75, v213 dst_sel:DWORD dst_unused:UNUSED_PAD src0_sel:WORD_1
	v_cvt_f32_f16_e32 v80, v214
	v_cvt_f32_f16_sdwa v81, v214 dst_sel:DWORD dst_unused:UNUSED_PAD src0_sel:WORD_1
	v_cvt_f32_f16_e32 v82, v215
	v_cvt_f32_f16_sdwa v83, v215 dst_sel:DWORD dst_unused:UNUSED_PAD src0_sel:WORD_1
	v_sub_f32_e32 v72, v72, v238
	v_sub_f32_e32 v73, v73, v238
	v_sub_f32_e32 v74, v74, v238
	v_sub_f32_e32 v75, v75, v238
	v_sub_f32_e32 v80, v80, v238
	v_sub_f32_e32 v81, v81, v238
	v_sub_f32_e32 v82, v82, v238
	v_sub_f32_e32 v83, v83, v238
	v_pk_mul_f32 v[72:73], v[238:239], v[72:73] op_sel:[1,0]
	v_pk_mul_f32 v[74:75], v[238:239], v[74:75] op_sel:[1,0]
	v_pk_mul_f32 v[80:81], v[238:239], v[80:81] op_sel:[1,0]
	v_pk_mul_f32 v[82:83], v[238:239], v[82:83] op_sel:[1,0]
	v_pk_fma_f32 v[132:133], v[72:73], v[168:169], v[132:133]
	v_pk_fma_f32 v[134:135], v[74:75], v[170:171], v[134:135]
	v_pk_fma_f32 v[128:129], v[80:81], v[172:173], v[128:129]
	v_pk_fma_f32 v[130:131], v[82:83], v[174:175], v[130:131]
	v_cvt_pk_f16_f32 v132, v132, v133
	v_cvt_pk_f16_f32 v133, v134, v135
	v_cvt_pk_f16_f32 v134, v128, v129
	v_cvt_pk_f16_f32 v135, v130, v131
	ds_write_b128 v235, v[132:135] offset:64
	v_fma_mix_f32 v206, v132, 1.0, v206 op_sel_hi:[1,0,0]
	v_fma_mix_f32 v207, v132, v132, v207 op_sel_hi:[1,1,0]
	v_fma_mix_f32 v206, v132, 1.0, v206 op_sel:[1,0,0] op_sel_hi:[1,0,0]
	v_fma_mix_f32 v207, v132, v132, v207 op_sel:[1,1,0] op_sel_hi:[1,1,0]
	v_fma_mix_f32 v206, v133, 1.0, v206 op_sel_hi:[1,0,0]
	v_fma_mix_f32 v207, v133, v133, v207 op_sel_hi:[1,1,0]
	v_fma_mix_f32 v206, v133, 1.0, v206 op_sel:[1,0,0] op_sel_hi:[1,0,0]
	v_fma_mix_f32 v207, v133, v133, v207 op_sel:[1,1,0] op_sel_hi:[1,1,0]
	v_fma_mix_f32 v206, v134, 1.0, v206 op_sel_hi:[1,0,0]
	v_fma_mix_f32 v207, v134, v134, v207 op_sel_hi:[1,1,0]
	v_fma_mix_f32 v206, v134, 1.0, v206 op_sel:[1,0,0] op_sel_hi:[1,0,0]
	v_fma_mix_f32 v207, v134, v134, v207 op_sel:[1,1,0] op_sel_hi:[1,1,0]
	v_fma_mix_f32 v206, v135, 1.0, v206 op_sel_hi:[1,0,0]
	v_fma_mix_f32 v207, v135, v135, v207 op_sel_hi:[1,1,0]
	v_fma_mix_f32 v206, v135, 1.0, v206 op_sel:[1,0,0] op_sel_hi:[1,0,0]
	v_fma_mix_f32 v207, v135, v135, v207 op_sel:[1,1,0] op_sel_hi:[1,1,0]
	ds_read_b128 v[88:91], v236
	ds_read_b128 v[92:95], v236 offset:1152
	s_waitcnt vmcnt(9)
	v_cvt_f32_f16_e32 v72, v216
	v_cvt_f32_f16_sdwa v73, v216 dst_sel:DWORD dst_unused:UNUSED_PAD src0_sel:WORD_1
	v_cvt_f32_f16_e32 v74, v217
	v_cvt_f32_f16_sdwa v75, v217 dst_sel:DWORD dst_unused:UNUSED_PAD src0_sel:WORD_1
	v_cvt_f32_f16_e32 v80, v218
	v_cvt_f32_f16_sdwa v81, v218 dst_sel:DWORD dst_unused:UNUSED_PAD src0_sel:WORD_1
	v_cvt_f32_f16_e32 v82, v219
	v_cvt_f32_f16_sdwa v83, v219 dst_sel:DWORD dst_unused:UNUSED_PAD src0_sel:WORD_1
	v_sub_f32_e32 v72, v72, v192
	v_sub_f32_e32 v73, v73, v192
	v_sub_f32_e32 v74, v74, v192
	v_sub_f32_e32 v75, v75, v192
	v_sub_f32_e32 v80, v80, v192
	v_sub_f32_e32 v81, v81, v192
	v_sub_f32_e32 v82, v82, v192
	v_sub_f32_e32 v83, v83, v192
	v_pk_mul_f32 v[72:73], v[192:193], v[72:73] op_sel:[1,0]
	v_pk_mul_f32 v[74:75], v[192:193], v[74:75] op_sel:[1,0]
	v_pk_mul_f32 v[80:81], v[192:193], v[80:81] op_sel:[1,0]
	v_pk_mul_f32 v[82:83], v[192:193], v[82:83] op_sel:[1,0]
	v_pk_fma_f32 v[124:125], v[72:73], v[160:161], v[124:125]
	v_pk_fma_f32 v[126:127], v[74:75], v[162:163], v[126:127]
	v_pk_fma_f32 v[120:121], v[80:81], v[164:165], v[120:121]
	v_pk_fma_f32 v[122:123], v[82:83], v[166:167], v[122:123]
	v_cvt_pk_f16_f32 v124, v124, v125
	v_cvt_pk_f16_f32 v125, v126, v127
	v_cvt_pk_f16_f32 v126, v120, v121
	v_cvt_pk_f16_f32 v127, v122, v123
	s_waitcnt lgkmcnt(0)
	buffer_store_dwordx4 v[88:91], v225, s[24:27], 0 offen nt
	v_add_u32_e32 v82, 0x3000, v225
	buffer_store_dwordx4 v[92:95], v82, s[24:27], 0 offen nt
	ds_write_b128 v235, v[124:127]
	v_fma_mix_f32 v140, v124, 1.0, 0 op_sel_hi:[1,0,0]
	v_fma_mix_f32 v141, v124, v124, 0 op_sel_hi:[1,1,0]
	v_fma_mix_f32 v140, v124, 1.0, v140 op_sel:[1,0,0] op_sel_hi:[1,0,0]
	v_fma_mix_f32 v141, v124, v124, v141 op_sel:[1,1,0] op_sel_hi:[1,1,0]
	v_fma_mix_f32 v140, v125, 1.0, v140 op_sel_hi:[1,0,0]
	v_fma_mix_f32 v141, v125, v125, v141 op_sel_hi:[1,1,0]
	v_fma_mix_f32 v140, v125, 1.0, v140 op_sel:[1,0,0] op_sel_hi:[1,0,0]
	v_fma_mix_f32 v141, v125, v125, v141 op_sel:[1,1,0] op_sel_hi:[1,1,0]
	v_fma_mix_f32 v140, v126, 1.0, v140 op_sel_hi:[1,0,0]
	v_fma_mix_f32 v141, v126, v126, v141 op_sel_hi:[1,1,0]
	v_fma_mix_f32 v140, v126, 1.0, v140 op_sel:[1,0,0] op_sel_hi:[1,0,0]
	v_fma_mix_f32 v141, v126, v126, v141 op_sel:[1,1,0] op_sel_hi:[1,1,0]
	v_fma_mix_f32 v140, v127, 1.0, v140 op_sel_hi:[1,0,0]
	v_fma_mix_f32 v141, v127, v127, v141 op_sel_hi:[1,1,0]
	v_fma_mix_f32 v140, v127, 1.0, v140 op_sel:[1,0,0] op_sel_hi:[1,0,0]
	v_fma_mix_f32 v141, v127, v127, v141 op_sel:[1,1,0] op_sel_hi:[1,1,0]
	s_waitcnt vmcnt(10)
	v_cvt_f32_f16_e32 v72, v220
	v_cvt_f32_f16_sdwa v73, v220 dst_sel:DWORD dst_unused:UNUSED_PAD src0_sel:WORD_1
	v_cvt_f32_f16_e32 v74, v221
	v_cvt_f32_f16_sdwa v75, v221 dst_sel:DWORD dst_unused:UNUSED_PAD src0_sel:WORD_1
	v_cvt_f32_f16_e32 v80, v222
	v_cvt_f32_f16_sdwa v81, v222 dst_sel:DWORD dst_unused:UNUSED_PAD src0_sel:WORD_1
	v_cvt_f32_f16_e32 v82, v223
	v_cvt_f32_f16_sdwa v83, v223 dst_sel:DWORD dst_unused:UNUSED_PAD src0_sel:WORD_1
	v_sub_f32_e32 v72, v72, v192
	v_sub_f32_e32 v73, v73, v192
	v_sub_f32_e32 v74, v74, v192
	v_sub_f32_e32 v75, v75, v192
	v_sub_f32_e32 v80, v80, v192
	v_sub_f32_e32 v81, v81, v192
	v_sub_f32_e32 v82, v82, v192
	v_sub_f32_e32 v83, v83, v192
	v_pk_mul_f32 v[72:73], v[192:193], v[72:73] op_sel:[1,0]
	v_pk_mul_f32 v[74:75], v[192:193], v[74:75] op_sel:[1,0]
	v_pk_mul_f32 v[80:81], v[192:193], v[80:81] op_sel:[1,0]
	v_pk_mul_f32 v[82:83], v[192:193], v[82:83] op_sel:[1,0]
	v_pk_fma_f32 v[116:117], v[72:73], v[168:169], v[116:117]
	v_pk_fma_f32 v[118:119], v[74:75], v[170:171], v[118:119]
	v_pk_fma_f32 v[112:113], v[80:81], v[172:173], v[112:113]
	v_pk_fma_f32 v[114:115], v[82:83], v[174:175], v[114:115]
	v_cvt_pk_f16_f32 v116, v116, v117
	v_cvt_pk_f16_f32 v117, v118, v119
	v_cvt_pk_f16_f32 v118, v112, v113
	v_cvt_pk_f16_f32 v119, v114, v115
	ds_write_b128 v235, v[116:119] offset:64
	v_fma_mix_f32 v140, v116, 1.0, v140 op_sel_hi:[1,0,0]
	v_fma_mix_f32 v141, v116, v116, v141 op_sel_hi:[1,1,0]
	v_fma_mix_f32 v140, v116, 1.0, v140 op_sel:[1,0,0] op_sel_hi:[1,0,0]
	v_fma_mix_f32 v141, v116, v116, v141 op_sel:[1,1,0] op_sel_hi:[1,1,0]
	v_fma_mix_f32 v140, v117, 1.0, v140 op_sel_hi:[1,0,0]
	v_fma_mix_f32 v141, v117, v117, v141 op_sel_hi:[1,1,0]
	v_fma_mix_f32 v140, v117, 1.0, v140 op_sel:[1,0,0] op_sel_hi:[1,0,0]
	v_fma_mix_f32 v141, v117, v117, v141 op_sel:[1,1,0] op_sel_hi:[1,1,0]
	v_fma_mix_f32 v140, v118, 1.0, v140 op_sel_hi:[1,0,0]
	v_fma_mix_f32 v141, v118, v118, v141 op_sel_hi:[1,1,0]
	v_fma_mix_f32 v140, v118, 1.0, v140 op_sel:[1,0,0] op_sel_hi:[1,0,0]
	v_fma_mix_f32 v141, v118, v118, v141 op_sel:[1,1,0] op_sel_hi:[1,1,0]
	v_fma_mix_f32 v140, v119, 1.0, v140 op_sel_hi:[1,0,0]
	v_fma_mix_f32 v141, v119, v119, v141 op_sel_hi:[1,1,0]
	v_fma_mix_f32 v140, v119, 1.0, v140 op_sel:[1,0,0] op_sel_hi:[1,0,0]
	v_fma_mix_f32 v141, v119, v119, v141 op_sel:[1,1,0] op_sel_hi:[1,1,0]
	ds_read_b128 v[208:211], v236
	ds_read_b128 v[128:131], v236 offset:1152
	s_add_u32 s94, s98, 0x3c000
	s_addc_u32 s95, s99, 0
	global_load_dwordx4 v[212:215], v191, s[94:95] offset:0 nt
	global_load_dwordx4 v[144:147], v191, s[94:95] offset:64 nt
	s_add_u32 s94, s98, 0x42000
	s_addc_u32 s95, s99, 0
	global_load_dwordx4 v[132:135], v191, s[94:95] offset:0 nt
	global_load_dwordx4 v[88:91], v191, s[94:95] offset:64 nt
	s_waitcnt vmcnt(13)
	v_cvt_f32_f16_e32 v72, v240
	v_cvt_f32_f16_sdwa v73, v240 dst_sel:DWORD dst_unused:UNUSED_PAD src0_sel:WORD_1
	v_cvt_f32_f16_e32 v74, v241
	v_cvt_f32_f16_sdwa v75, v241 dst_sel:DWORD dst_unused:UNUSED_PAD src0_sel:WORD_1
	v_cvt_f32_f16_e32 v80, v242
	v_cvt_f32_f16_sdwa v81, v242 dst_sel:DWORD dst_unused:UNUSED_PAD src0_sel:WORD_1
	v_cvt_f32_f16_e32 v82, v243
	v_cvt_f32_f16_sdwa v83, v243 dst_sel:DWORD dst_unused:UNUSED_PAD src0_sel:WORD_1
	v_sub_f32_e32 v72, v72, v194
	v_sub_f32_e32 v73, v73, v194
	v_sub_f32_e32 v74, v74, v194
	v_sub_f32_e32 v75, v75, v194
	v_sub_f32_e32 v80, v80, v194
	v_sub_f32_e32 v81, v81, v194
	v_sub_f32_e32 v82, v82, v194
	v_sub_f32_e32 v83, v83, v194
	v_pk_mul_f32 v[72:73], v[194:195], v[72:73] op_sel:[1,0]
	v_pk_mul_f32 v[74:75], v[194:195], v[74:75] op_sel:[1,0]
	v_pk_mul_f32 v[80:81], v[194:195], v[80:81] op_sel:[1,0]
	v_pk_mul_f32 v[82:83], v[194:195], v[82:83] op_sel:[1,0]
	v_pk_fma_f32 v[108:109], v[72:73], v[160:161], v[108:109]
	v_pk_fma_f32 v[110:111], v[74:75], v[162:163], v[110:111]
	v_pk_fma_f32 v[104:105], v[80:81], v[164:165], v[104:105]
	v_pk_fma_f32 v[106:107], v[82:83], v[166:167], v[106:107]
	v_cvt_pk_f16_f32 v108, v108, v109
	v_cvt_pk_f16_f32 v109, v110, v111
	v_cvt_pk_f16_f32 v110, v104, v105
	v_cvt_pk_f16_f32 v111, v106, v107
	s_waitcnt lgkmcnt(0)
	v_add_u32_e32 v83, 0x6000, v225
	buffer_store_dwordx4 v[208:211], v83, s[24:27], 0 offen nt
	v_add_u32_e32 v82, 0x9000, v225
	buffer_store_dwordx4 v[128:131], v82, s[24:27], 0 offen nt
	ds_write_b128 v235, v[108:111]
	v_fma_mix_f32 v142, v108, 1.0, 0 op_sel_hi:[1,0,0]
	v_fma_mix_f32 v143, v108, v108, 0 op_sel_hi:[1,1,0]
	v_fma_mix_f32 v142, v108, 1.0, v142 op_sel:[1,0,0] op_sel_hi:[1,0,0]
	v_fma_mix_f32 v143, v108, v108, v143 op_sel:[1,1,0] op_sel_hi:[1,1,0]
	v_fma_mix_f32 v142, v109, 1.0, v142 op_sel_hi:[1,0,0]
	v_fma_mix_f32 v143, v109, v109, v143 op_sel_hi:[1,1,0]
	v_fma_mix_f32 v142, v109, 1.0, v142 op_sel:[1,0,0] op_sel_hi:[1,0,0]
	v_fma_mix_f32 v143, v109, v109, v143 op_sel:[1,1,0] op_sel_hi:[1,1,0]
	v_fma_mix_f32 v142, v110, 1.0, v142 op_sel_hi:[1,0,0]
	v_fma_mix_f32 v143, v110, v110, v143 op_sel_hi:[1,1,0]
	v_fma_mix_f32 v142, v110, 1.0, v142 op_sel:[1,0,0] op_sel_hi:[1,0,0]
	v_fma_mix_f32 v143, v110, v110, v143 op_sel:[1,1,0] op_sel_hi:[1,1,0]
	v_fma_mix_f32 v142, v111, 1.0, v142 op_sel_hi:[1,0,0]
	v_fma_mix_f32 v143, v111, v111, v143 op_sel_hi:[1,1,0]
	v_fma_mix_f32 v142, v111, 1.0, v142 op_sel:[1,0,0] op_sel_hi:[1,0,0]
	v_fma_mix_f32 v143, v111, v111, v143 op_sel:[1,1,0] op_sel_hi:[1,1,0]
	s_waitcnt vmcnt(14)
	v_cvt_f32_f16_e32 v72, v244
	v_cvt_f32_f16_sdwa v73, v244 dst_sel:DWORD dst_unused:UNUSED_PAD src0_sel:WORD_1
	v_cvt_f32_f16_e32 v74, v245
	v_cvt_f32_f16_sdwa v75, v245 dst_sel:DWORD dst_unused:UNUSED_PAD src0_sel:WORD_1
	v_cvt_f32_f16_e32 v80, v246
	v_cvt_f32_f16_sdwa v81, v246 dst_sel:DWORD dst_unused:UNUSED_PAD src0_sel:WORD_1
	v_cvt_f32_f16_e32 v82, v247
	v_cvt_f32_f16_sdwa v83, v247 dst_sel:DWORD dst_unused:UNUSED_PAD src0_sel:WORD_1
	v_sub_f32_e32 v72, v72, v194
	v_sub_f32_e32 v73, v73, v194
	v_sub_f32_e32 v74, v74, v194
	v_sub_f32_e32 v75, v75, v194
	v_sub_f32_e32 v80, v80, v194
	v_sub_f32_e32 v81, v81, v194
	v_sub_f32_e32 v82, v82, v194
	v_sub_f32_e32 v83, v83, v194
	v_pk_mul_f32 v[72:73], v[194:195], v[72:73] op_sel:[1,0]
	v_pk_mul_f32 v[74:75], v[194:195], v[74:75] op_sel:[1,0]
	v_pk_mul_f32 v[80:81], v[194:195], v[80:81] op_sel:[1,0]
	v_pk_mul_f32 v[82:83], v[194:195], v[82:83] op_sel:[1,0]
	v_pk_fma_f32 v[100:101], v[72:73], v[168:169], v[100:101]
	v_pk_fma_f32 v[102:103], v[74:75], v[170:171], v[102:103]
	v_pk_fma_f32 v[96:97], v[80:81], v[172:173], v[96:97]
	v_pk_fma_f32 v[98:99], v[82:83], v[174:175], v[98:99]
	v_cvt_pk_f16_f32 v100, v100, v101
	v_cvt_pk_f16_f32 v101, v102, v103
	v_cvt_pk_f16_f32 v102, v96, v97
	v_cvt_pk_f16_f32 v103, v98, v99
	ds_write_b128 v235, v[100:103] offset:64
	v_fma_mix_f32 v142, v100, 1.0, v142 op_sel_hi:[1,0,0]
	v_fma_mix_f32 v143, v100, v100, v143 op_sel_hi:[1,1,0]
	v_fma_mix_f32 v142, v100, 1.0, v142 op_sel:[1,0,0] op_sel_hi:[1,0,0]
	v_fma_mix_f32 v143, v100, v100, v143 op_sel:[1,1,0] op_sel_hi:[1,1,0]
	v_fma_mix_f32 v142, v101, 1.0, v142 op_sel_hi:[1,0,0]
	v_fma_mix_f32 v143, v101, v101, v143 op_sel_hi:[1,1,0]
	v_fma_mix_f32 v142, v101, 1.0, v142 op_sel:[1,0,0] op_sel_hi:[1,0,0]
	v_fma_mix_f32 v143, v101, v101, v143 op_sel:[1,1,0] op_sel_hi:[1,1,0]
	v_fma_mix_f32 v142, v102, 1.0, v142 op_sel_hi:[1,0,0]
	v_fma_mix_f32 v143, v102, v102, v143 op_sel_hi:[1,1,0]
	v_fma_mix_f32 v142, v102, 1.0, v142 op_sel:[1,0,0] op_sel_hi:[1,0,0]
	v_fma_mix_f32 v143, v102, v102, v143 op_sel:[1,1,0] op_sel_hi:[1,1,0]
	v_fma_mix_f32 v142, v103, 1.0, v142 op_sel_hi:[1,0,0]
	v_fma_mix_f32 v143, v103, v103, v143 op_sel_hi:[1,1,0]
	v_fma_mix_f32 v142, v103, 1.0, v142 op_sel:[1,0,0] op_sel_hi:[1,0,0]
	v_fma_mix_f32 v143, v103, v103, v143 op_sel:[1,1,0] op_sel_hi:[1,1,0]
	ds_read_b128 v[92:95], v236
	ds_read_b128 v[120:123], v236 offset:1152
	s_waitcnt vmcnt(13)
	v_cvt_f32_f16_e32 v72, v248
	v_cvt_f32_f16_sdwa v73, v248 dst_sel:DWORD dst_unused:UNUSED_PAD src0_sel:WORD_1
	v_cvt_f32_f16_e32 v74, v249
	v_cvt_f32_f16_sdwa v75, v249 dst_sel:DWORD dst_unused:UNUSED_PAD src0_sel:WORD_1
	v_cvt_f32_f16_e32 v80, v250
	v_cvt_f32_f16_sdwa v81, v250 dst_sel:DWORD dst_unused:UNUSED_PAD src0_sel:WORD_1
	v_cvt_f32_f16_e32 v82, v251
	v_cvt_f32_f16_sdwa v83, v251 dst_sel:DWORD dst_unused:UNUSED_PAD src0_sel:WORD_1
	v_sub_f32_e32 v72, v72, v196
	v_sub_f32_e32 v73, v73, v196
	v_sub_f32_e32 v74, v74, v196
	v_sub_f32_e32 v75, v75, v196
	v_sub_f32_e32 v80, v80, v196
	v_sub_f32_e32 v81, v81, v196
	v_sub_f32_e32 v82, v82, v196
	v_sub_f32_e32 v83, v83, v196
	v_pk_mul_f32 v[72:73], v[196:197], v[72:73] op_sel:[1,0]
	v_pk_mul_f32 v[74:75], v[196:197], v[74:75] op_sel:[1,0]
	v_pk_mul_f32 v[80:81], v[196:197], v[80:81] op_sel:[1,0]
	v_pk_mul_f32 v[82:83], v[196:197], v[82:83] op_sel:[1,0]
	v_pk_fma_f32 v[84:85], v[72:73], v[160:161], v[84:85]
	v_pk_fma_f32 v[86:87], v[74:75], v[162:163], v[86:87]
	v_pk_fma_f32 v[76:77], v[80:81], v[164:165], v[76:77]
	v_pk_fma_f32 v[78:79], v[82:83], v[166:167], v[78:79]
	v_cvt_pk_f16_f32 v84, v84, v85
	v_cvt_pk_f16_f32 v85, v86, v87
	v_cvt_pk_f16_f32 v86, v76, v77
	v_cvt_pk_f16_f32 v87, v78, v79
	s_waitcnt lgkmcnt(0)
	v_add_u32_e32 v83, 0xc000, v225
	buffer_store_dwordx4 v[92:95], v83, s[24:27], 0 offen nt
	v_add_u32_e32 v82, 0xf000, v225
	buffer_store_dwordx4 v[120:123], v82, s[24:27], 0 offen nt
	ds_write_b128 v235, v[84:87]
	v_fma_mix_f32 v216, v84, 1.0, 0 op_sel_hi:[1,0,0]
	v_fma_mix_f32 v217, v84, v84, 0 op_sel_hi:[1,1,0]
	v_fma_mix_f32 v216, v84, 1.0, v216 op_sel:[1,0,0] op_sel_hi:[1,0,0]
	v_fma_mix_f32 v217, v84, v84, v217 op_sel:[1,1,0] op_sel_hi:[1,1,0]
	v_fma_mix_f32 v216, v85, 1.0, v216 op_sel_hi:[1,0,0]
	v_fma_mix_f32 v217, v85, v85, v217 op_sel_hi:[1,1,0]
	v_fma_mix_f32 v216, v85, 1.0, v216 op_sel:[1,0,0] op_sel_hi:[1,0,0]
	v_fma_mix_f32 v217, v85, v85, v217 op_sel:[1,1,0] op_sel_hi:[1,1,0]
	v_fma_mix_f32 v216, v86, 1.0, v216 op_sel_hi:[1,0,0]
	v_fma_mix_f32 v217, v86, v86, v217 op_sel_hi:[1,1,0]
	v_fma_mix_f32 v216, v86, 1.0, v216 op_sel:[1,0,0] op_sel_hi:[1,0,0]
	v_fma_mix_f32 v217, v86, v86, v217 op_sel:[1,1,0] op_sel_hi:[1,1,0]
	v_fma_mix_f32 v216, v87, 1.0, v216 op_sel_hi:[1,0,0]
	v_fma_mix_f32 v217, v87, v87, v217 op_sel_hi:[1,1,0]
	v_fma_mix_f32 v216, v87, 1.0, v216 op_sel:[1,0,0] op_sel_hi:[1,0,0]
	v_fma_mix_f32 v217, v87, v87, v217 op_sel:[1,1,0] op_sel_hi:[1,1,0]
	s_waitcnt vmcnt(14)
	v_cvt_f32_f16_e32 v72, v252
	v_cvt_f32_f16_sdwa v73, v252 dst_sel:DWORD dst_unused:UNUSED_PAD src0_sel:WORD_1
	v_cvt_f32_f16_e32 v74, v253
	v_cvt_f32_f16_sdwa v75, v253 dst_sel:DWORD dst_unused:UNUSED_PAD src0_sel:WORD_1
	v_cvt_f32_f16_e32 v80, v254
	v_cvt_f32_f16_sdwa v81, v254 dst_sel:DWORD dst_unused:UNUSED_PAD src0_sel:WORD_1
	v_cvt_f32_f16_e32 v82, v255
	v_cvt_f32_f16_sdwa v83, v255 dst_sel:DWORD dst_unused:UNUSED_PAD src0_sel:WORD_1
	v_sub_f32_e32 v72, v72, v196
	v_sub_f32_e32 v73, v73, v196
	v_sub_f32_e32 v74, v74, v196
	v_sub_f32_e32 v75, v75, v196
	v_sub_f32_e32 v80, v80, v196
	v_sub_f32_e32 v81, v81, v196
	v_sub_f32_e32 v82, v82, v196
	v_sub_f32_e32 v83, v83, v196
	v_pk_mul_f32 v[72:73], v[196:197], v[72:73] op_sel:[1,0]
	v_pk_mul_f32 v[74:75], v[196:197], v[74:75] op_sel:[1,0]
	v_pk_mul_f32 v[80:81], v[196:197], v[80:81] op_sel:[1,0]
	v_pk_mul_f32 v[82:83], v[196:197], v[82:83] op_sel:[1,0]
	v_pk_fma_f32 v[68:69], v[72:73], v[168:169], v[68:69]
	v_pk_fma_f32 v[70:71], v[74:75], v[170:171], v[70:71]
	v_pk_fma_f32 v[64:65], v[80:81], v[172:173], v[64:65]
	v_pk_fma_f32 v[66:67], v[82:83], v[174:175], v[66:67]
	v_cvt_pk_f16_f32 v68, v68, v69
	v_cvt_pk_f16_f32 v69, v70, v71
	v_cvt_pk_f16_f32 v70, v64, v65
	v_cvt_pk_f16_f32 v71, v66, v67
	ds_write_b128 v235, v[68:71] offset:64
	v_fma_mix_f32 v216, v68, 1.0, v216 op_sel_hi:[1,0,0]
	v_fma_mix_f32 v217, v68, v68, v217 op_sel_hi:[1,1,0]
	v_fma_mix_f32 v216, v68, 1.0, v216 op_sel:[1,0,0] op_sel_hi:[1,0,0]
	v_fma_mix_f32 v217, v68, v68, v217 op_sel:[1,1,0] op_sel_hi:[1,1,0]
	v_fma_mix_f32 v216, v69, 1.0, v216 op_sel_hi:[1,0,0]
	v_fma_mix_f32 v217, v69, v69, v217 op_sel_hi:[1,1,0]
	v_fma_mix_f32 v216, v69, 1.0, v216 op_sel:[1,0,0] op_sel_hi:[1,0,0]
	v_fma_mix_f32 v217, v69, v69, v217 op_sel:[1,1,0] op_sel_hi:[1,1,0]
	v_fma_mix_f32 v216, v70, 1.0, v216 op_sel_hi:[1,0,0]
	v_fma_mix_f32 v217, v70, v70, v217 op_sel_hi:[1,1,0]
	v_fma_mix_f32 v216, v70, 1.0, v216 op_sel:[1,0,0] op_sel_hi:[1,0,0]
	v_fma_mix_f32 v217, v70, v70, v217 op_sel:[1,1,0] op_sel_hi:[1,1,0]
	v_fma_mix_f32 v216, v71, 1.0, v216 op_sel_hi:[1,0,0]
	v_fma_mix_f32 v217, v71, v71, v217 op_sel_hi:[1,1,0]
	v_fma_mix_f32 v216, v71, 1.0, v216 op_sel:[1,0,0] op_sel_hi:[1,0,0]
	v_fma_mix_f32 v217, v71, v71, v217 op_sel:[1,1,0] op_sel_hi:[1,1,0]
	ds_read_b128 v[112:115], v236
	ds_read_b128 v[220:223], v236 offset:1152
	s_waitcnt vmcnt(13)
	v_cvt_f32_f16_e32 v72, v136
	v_cvt_f32_f16_sdwa v73, v136 dst_sel:DWORD dst_unused:UNUSED_PAD src0_sel:WORD_1
	v_cvt_f32_f16_e32 v74, v137
	v_cvt_f32_f16_sdwa v75, v137 dst_sel:DWORD dst_unused:UNUSED_PAD src0_sel:WORD_1
	v_cvt_f32_f16_e32 v80, v138
	v_cvt_f32_f16_sdwa v81, v138 dst_sel:DWORD dst_unused:UNUSED_PAD src0_sel:WORD_1
	v_cvt_f32_f16_e32 v82, v139
	v_cvt_f32_f16_sdwa v83, v139 dst_sel:DWORD dst_unused:UNUSED_PAD src0_sel:WORD_1
	v_sub_f32_e32 v72, v72, v198
	v_sub_f32_e32 v73, v73, v198
	v_sub_f32_e32 v74, v74, v198
	v_sub_f32_e32 v75, v75, v198
	v_sub_f32_e32 v80, v80, v198
	v_sub_f32_e32 v81, v81, v198
	v_sub_f32_e32 v82, v82, v198
	v_sub_f32_e32 v83, v83, v198
	v_pk_mul_f32 v[72:73], v[198:199], v[72:73] op_sel:[1,0]
	v_pk_mul_f32 v[74:75], v[198:199], v[74:75] op_sel:[1,0]
	v_pk_mul_f32 v[80:81], v[198:199], v[80:81] op_sel:[1,0]
	v_pk_mul_f32 v[82:83], v[198:199], v[82:83] op_sel:[1,0]
	v_pk_fma_f32 v[60:61], v[72:73], v[160:161], v[60:61]
	v_pk_fma_f32 v[62:63], v[74:75], v[162:163], v[62:63]
	v_pk_fma_f32 v[56:57], v[80:81], v[164:165], v[56:57]
	v_pk_fma_f32 v[58:59], v[82:83], v[166:167], v[58:59]
	v_cvt_pk_f16_f32 v60, v60, v61
	v_cvt_pk_f16_f32 v61, v62, v63
	v_cvt_pk_f16_f32 v62, v56, v57
	v_cvt_pk_f16_f32 v63, v58, v59
	s_waitcnt lgkmcnt(0)
	v_add_u32_e32 v83, 0x12000, v225
	buffer_store_dwordx4 v[112:115], v83, s[24:27], 0 offen nt
	v_add_u32_e32 v82, 0x15000, v225
	buffer_store_dwordx4 v[220:223], v82, s[24:27], 0 offen nt
	ds_write_b128 v235, v[60:63]
	v_fma_mix_f32 v218, v60, 1.0, 0 op_sel_hi:[1,0,0]
	v_fma_mix_f32 v219, v60, v60, 0 op_sel_hi:[1,1,0]
	v_fma_mix_f32 v218, v60, 1.0, v218 op_sel:[1,0,0] op_sel_hi:[1,0,0]
	v_fma_mix_f32 v219, v60, v60, v219 op_sel:[1,1,0] op_sel_hi:[1,1,0]
	v_fma_mix_f32 v218, v61, 1.0, v218 op_sel_hi:[1,0,0]
	v_fma_mix_f32 v219, v61, v61, v219 op_sel_hi:[1,1,0]
	v_fma_mix_f32 v218, v61, 1.0, v218 op_sel:[1,0,0] op_sel_hi:[1,0,0]
	v_fma_mix_f32 v219, v61, v61, v219 op_sel:[1,1,0] op_sel_hi:[1,1,0]
	v_fma_mix_f32 v218, v62, 1.0, v218 op_sel_hi:[1,0,0]
	v_fma_mix_f32 v219, v62, v62, v219 op_sel_hi:[1,1,0]
	v_fma_mix_f32 v218, v62, 1.0, v218 op_sel:[1,0,0] op_sel_hi:[1,0,0]
	v_fma_mix_f32 v219, v62, v62, v219 op_sel:[1,1,0] op_sel_hi:[1,1,0]
	v_fma_mix_f32 v218, v63, 1.0, v218 op_sel_hi:[1,0,0]
	v_fma_mix_f32 v219, v63, v63, v219 op_sel_hi:[1,1,0]
	v_fma_mix_f32 v218, v63, 1.0, v218 op_sel:[1,0,0] op_sel_hi:[1,0,0]
	v_fma_mix_f32 v219, v63, v63, v219 op_sel:[1,1,0] op_sel_hi:[1,1,0]
	s_waitcnt vmcnt(14)
	v_cvt_f32_f16_e32 v72, v148
	v_cvt_f32_f16_sdwa v73, v148 dst_sel:DWORD dst_unused:UNUSED_PAD src0_sel:WORD_1
	v_cvt_f32_f16_e32 v74, v149
	v_cvt_f32_f16_sdwa v75, v149 dst_sel:DWORD dst_unused:UNUSED_PAD src0_sel:WORD_1
	v_cvt_f32_f16_e32 v80, v150
	v_cvt_f32_f16_sdwa v81, v150 dst_sel:DWORD dst_unused:UNUSED_PAD src0_sel:WORD_1
	v_cvt_f32_f16_e32 v82, v151
	v_cvt_f32_f16_sdwa v83, v151 dst_sel:DWORD dst_unused:UNUSED_PAD src0_sel:WORD_1
	v_sub_f32_e32 v72, v72, v198
	v_sub_f32_e32 v73, v73, v198
	v_sub_f32_e32 v74, v74, v198
	v_sub_f32_e32 v75, v75, v198
	v_sub_f32_e32 v80, v80, v198
	v_sub_f32_e32 v81, v81, v198
	v_sub_f32_e32 v82, v82, v198
	v_sub_f32_e32 v83, v83, v198
	v_pk_mul_f32 v[72:73], v[198:199], v[72:73] op_sel:[1,0]
	v_pk_mul_f32 v[74:75], v[198:199], v[74:75] op_sel:[1,0]
	v_pk_mul_f32 v[80:81], v[198:199], v[80:81] op_sel:[1,0]
	v_pk_mul_f32 v[82:83], v[198:199], v[82:83] op_sel:[1,0]
	v_pk_fma_f32 v[52:53], v[72:73], v[168:169], v[52:53]
	v_pk_fma_f32 v[54:55], v[74:75], v[170:171], v[54:55]
	v_pk_fma_f32 v[48:49], v[80:81], v[172:173], v[48:49]
	v_pk_fma_f32 v[50:51], v[82:83], v[174:175], v[50:51]
	v_cvt_pk_f16_f32 v52, v52, v53
	v_cvt_pk_f16_f32 v53, v54, v55
	v_cvt_pk_f16_f32 v54, v48, v49
	v_cvt_pk_f16_f32 v55, v50, v51
	ds_write_b128 v235, v[52:55] offset:64
	v_fma_mix_f32 v218, v52, 1.0, v218 op_sel_hi:[1,0,0]
	v_fma_mix_f32 v219, v52, v52, v219 op_sel_hi:[1,1,0]
	v_fma_mix_f32 v218, v52, 1.0, v218 op_sel:[1,0,0] op_sel_hi:[1,0,0]
	v_fma_mix_f32 v219, v52, v52, v219 op_sel:[1,1,0] op_sel_hi:[1,1,0]
	v_fma_mix_f32 v218, v53, 1.0, v218 op_sel_hi:[1,0,0]
	v_fma_mix_f32 v219, v53, v53, v219 op_sel_hi:[1,1,0]
	v_fma_mix_f32 v218, v53, 1.0, v218 op_sel:[1,0,0] op_sel_hi:[1,0,0]
	v_fma_mix_f32 v219, v53, v53, v219 op_sel:[1,1,0] op_sel_hi:[1,1,0]
	v_fma_mix_f32 v218, v54, 1.0, v218 op_sel_hi:[1,0,0]
	v_fma_mix_f32 v219, v54, v54, v219 op_sel_hi:[1,1,0]
	v_fma_mix_f32 v218, v54, 1.0, v218 op_sel:[1,0,0] op_sel_hi:[1,0,0]
	v_fma_mix_f32 v219, v54, v54, v219 op_sel:[1,1,0] op_sel_hi:[1,1,0]
	v_fma_mix_f32 v218, v55, 1.0, v218 op_sel_hi:[1,0,0]
	v_fma_mix_f32 v219, v55, v55, v219 op_sel_hi:[1,1,0]
	v_fma_mix_f32 v218, v55, 1.0, v218 op_sel:[1,0,0] op_sel_hi:[1,0,0]
	v_fma_mix_f32 v219, v55, v55, v219 op_sel:[1,1,0] op_sel_hi:[1,1,0]
	ds_read_b128 v[124:127], v236
	ds_read_b128 v[116:119], v236 offset:1152
	s_waitcnt vmcnt(13)
	v_cvt_f32_f16_e32 v72, v152
	v_cvt_f32_f16_sdwa v73, v152 dst_sel:DWORD dst_unused:UNUSED_PAD src0_sel:WORD_1
	v_cvt_f32_f16_e32 v74, v153
	v_cvt_f32_f16_sdwa v75, v153 dst_sel:DWORD dst_unused:UNUSED_PAD src0_sel:WORD_1
	v_cvt_f32_f16_e32 v80, v154
	v_cvt_f32_f16_sdwa v81, v154 dst_sel:DWORD dst_unused:UNUSED_PAD src0_sel:WORD_1
	v_cvt_f32_f16_e32 v82, v155
	v_cvt_f32_f16_sdwa v83, v155 dst_sel:DWORD dst_unused:UNUSED_PAD src0_sel:WORD_1
	v_sub_f32_e32 v72, v72, v200
	v_sub_f32_e32 v73, v73, v200
	v_sub_f32_e32 v74, v74, v200
	v_sub_f32_e32 v75, v75, v200
	v_sub_f32_e32 v80, v80, v200
	v_sub_f32_e32 v81, v81, v200
	v_sub_f32_e32 v82, v82, v200
	v_sub_f32_e32 v83, v83, v200
	v_pk_mul_f32 v[72:73], v[200:201], v[72:73] op_sel:[1,0]
	v_pk_mul_f32 v[74:75], v[200:201], v[74:75] op_sel:[1,0]
	v_pk_mul_f32 v[80:81], v[200:201], v[80:81] op_sel:[1,0]
	v_pk_mul_f32 v[82:83], v[200:201], v[82:83] op_sel:[1,0]
	v_pk_fma_f32 v[44:45], v[72:73], v[160:161], v[44:45]
	v_pk_fma_f32 v[46:47], v[74:75], v[162:163], v[46:47]
	v_pk_fma_f32 v[40:41], v[80:81], v[164:165], v[40:41]
	v_pk_fma_f32 v[42:43], v[82:83], v[166:167], v[42:43]
	v_cvt_pk_f16_f32 v44, v44, v45
	v_cvt_pk_f16_f32 v45, v46, v47
	v_cvt_pk_f16_f32 v46, v40, v41
	v_cvt_pk_f16_f32 v47, v42, v43
	s_waitcnt lgkmcnt(0)
	v_add_u32_e32 v83, 0x30000, v225
	buffer_store_dwordx4 v[124:127], v83, s[24:27], 0 offen nt
	v_add_u32_e32 v82, 0x33000, v225
	buffer_store_dwordx4 v[116:119], v82, s[24:27], 0 offen nt
	ds_write_b128 v235, v[44:47]
	v_fma_mix_f32 v208, v44, 1.0, 0 op_sel_hi:[1,0,0]
	v_fma_mix_f32 v209, v44, v44, 0 op_sel_hi:[1,1,0]
	v_fma_mix_f32 v208, v44, 1.0, v208 op_sel:[1,0,0] op_sel_hi:[1,0,0]
	v_fma_mix_f32 v209, v44, v44, v209 op_sel:[1,1,0] op_sel_hi:[1,1,0]
	v_fma_mix_f32 v208, v45, 1.0, v208 op_sel_hi:[1,0,0]
	v_fma_mix_f32 v209, v45, v45, v209 op_sel_hi:[1,1,0]
	v_fma_mix_f32 v208, v45, 1.0, v208 op_sel:[1,0,0] op_sel_hi:[1,0,0]
	v_fma_mix_f32 v209, v45, v45, v209 op_sel:[1,1,0] op_sel_hi:[1,1,0]
	v_fma_mix_f32 v208, v46, 1.0, v208 op_sel_hi:[1,0,0]
	v_fma_mix_f32 v209, v46, v46, v209 op_sel_hi:[1,1,0]
	v_fma_mix_f32 v208, v46, 1.0, v208 op_sel:[1,0,0] op_sel_hi:[1,0,0]
	v_fma_mix_f32 v209, v46, v46, v209 op_sel:[1,1,0] op_sel_hi:[1,1,0]
	v_fma_mix_f32 v208, v47, 1.0, v208 op_sel_hi:[1,0,0]
	v_fma_mix_f32 v209, v47, v47, v209 op_sel_hi:[1,1,0]
	v_fma_mix_f32 v208, v47, 1.0, v208 op_sel:[1,0,0] op_sel_hi:[1,0,0]
	v_fma_mix_f32 v209, v47, v47, v209 op_sel:[1,1,0] op_sel_hi:[1,1,0]
	s_waitcnt vmcnt(14)
	v_cvt_f32_f16_e32 v72, v156
	v_cvt_f32_f16_sdwa v73, v156 dst_sel:DWORD dst_unused:UNUSED_PAD src0_sel:WORD_1
	v_cvt_f32_f16_e32 v74, v157
	v_cvt_f32_f16_sdwa v75, v157 dst_sel:DWORD dst_unused:UNUSED_PAD src0_sel:WORD_1
	v_cvt_f32_f16_e32 v80, v158
	v_cvt_f32_f16_sdwa v81, v158 dst_sel:DWORD dst_unused:UNUSED_PAD src0_sel:WORD_1
	v_cvt_f32_f16_e32 v82, v159
	v_cvt_f32_f16_sdwa v83, v159 dst_sel:DWORD dst_unused:UNUSED_PAD src0_sel:WORD_1
	v_sub_f32_e32 v72, v72, v200
	v_sub_f32_e32 v73, v73, v200
	v_sub_f32_e32 v74, v74, v200
	v_sub_f32_e32 v75, v75, v200
	v_sub_f32_e32 v80, v80, v200
	v_sub_f32_e32 v81, v81, v200
	v_sub_f32_e32 v82, v82, v200
	v_sub_f32_e32 v83, v83, v200
	v_pk_mul_f32 v[72:73], v[200:201], v[72:73] op_sel:[1,0]
	v_pk_mul_f32 v[74:75], v[200:201], v[74:75] op_sel:[1,0]
	v_pk_mul_f32 v[80:81], v[200:201], v[80:81] op_sel:[1,0]
	v_pk_mul_f32 v[82:83], v[200:201], v[82:83] op_sel:[1,0]
	v_pk_fma_f32 v[36:37], v[72:73], v[168:169], v[36:37]
	v_pk_fma_f32 v[38:39], v[74:75], v[170:171], v[38:39]
	v_pk_fma_f32 v[32:33], v[80:81], v[172:173], v[32:33]
	v_pk_fma_f32 v[34:35], v[82:83], v[174:175], v[34:35]
	v_cvt_pk_f16_f32 v36, v36, v37
	v_cvt_pk_f16_f32 v37, v38, v39
	v_cvt_pk_f16_f32 v38, v32, v33
	v_cvt_pk_f16_f32 v39, v34, v35
	ds_write_b128 v235, v[36:39] offset:64
	v_fma_mix_f32 v208, v36, 1.0, v208 op_sel_hi:[1,0,0]
	v_fma_mix_f32 v209, v36, v36, v209 op_sel_hi:[1,1,0]
	v_fma_mix_f32 v208, v36, 1.0, v208 op_sel:[1,0,0] op_sel_hi:[1,0,0]
	v_fma_mix_f32 v209, v36, v36, v209 op_sel:[1,1,0] op_sel_hi:[1,1,0]
	v_fma_mix_f32 v208, v37, 1.0, v208 op_sel_hi:[1,0,0]
	v_fma_mix_f32 v209, v37, v37, v209 op_sel_hi:[1,1,0]
	v_fma_mix_f32 v208, v37, 1.0, v208 op_sel:[1,0,0] op_sel_hi:[1,0,0]
	v_fma_mix_f32 v209, v37, v37, v209 op_sel:[1,1,0] op_sel_hi:[1,1,0]
	v_fma_mix_f32 v208, v38, 1.0, v208 op_sel_hi:[1,0,0]
	v_fma_mix_f32 v209, v38, v38, v209 op_sel_hi:[1,1,0]
	v_fma_mix_f32 v208, v38, 1.0, v208 op_sel:[1,0,0] op_sel_hi:[1,0,0]
	v_fma_mix_f32 v209, v38, v38, v209 op_sel:[1,1,0] op_sel_hi:[1,1,0]
	v_fma_mix_f32 v208, v39, 1.0, v208 op_sel_hi:[1,0,0]
	v_fma_mix_f32 v209, v39, v39, v209 op_sel_hi:[1,1,0]
	v_fma_mix_f32 v208, v39, 1.0, v208 op_sel:[1,0,0] op_sel_hi:[1,0,0]
	v_fma_mix_f32 v209, v39, v39, v209 op_sel:[1,1,0] op_sel_hi:[1,1,0]
	ds_read_b128 v[128:131], v236
	ds_read_b128 v[104:107], v236 offset:1152
	s_waitcnt vmcnt(11)
	v_cvt_f32_f16_e32 v72, v212
	v_cvt_f32_f16_sdwa v73, v212 dst_sel:DWORD dst_unused:UNUSED_PAD src0_sel:WORD_1
	v_cvt_f32_f16_e32 v74, v213
	v_cvt_f32_f16_sdwa v75, v213 dst_sel:DWORD dst_unused:UNUSED_PAD src0_sel:WORD_1
	v_cvt_f32_f16_e32 v80, v214
	v_cvt_f32_f16_sdwa v81, v214 dst_sel:DWORD dst_unused:UNUSED_PAD src0_sel:WORD_1
	v_cvt_f32_f16_e32 v82, v215
	v_cvt_f32_f16_sdwa v83, v215 dst_sel:DWORD dst_unused:UNUSED_PAD src0_sel:WORD_1
	v_sub_f32_e32 v72, v72, v202
	v_sub_f32_e32 v73, v73, v202
	v_sub_f32_e32 v74, v74, v202
	v_sub_f32_e32 v75, v75, v202
	v_sub_f32_e32 v80, v80, v202
	v_sub_f32_e32 v81, v81, v202
	v_sub_f32_e32 v82, v82, v202
	v_sub_f32_e32 v83, v83, v202
	v_pk_mul_f32 v[72:73], v[202:203], v[72:73] op_sel:[1,0]
	v_pk_mul_f32 v[74:75], v[202:203], v[74:75] op_sel:[1,0]
	v_pk_mul_f32 v[80:81], v[202:203], v[80:81] op_sel:[1,0]
	v_pk_mul_f32 v[82:83], v[202:203], v[82:83] op_sel:[1,0]
	v_pk_fma_f32 v[28:29], v[72:73], v[160:161], v[28:29]
	v_pk_fma_f32 v[30:31], v[74:75], v[162:163], v[30:31]
	v_pk_fma_f32 v[24:25], v[80:81], v[164:165], v[24:25]
	v_pk_fma_f32 v[26:27], v[82:83], v[166:167], v[26:27]
	v_cvt_pk_f16_f32 v28, v28, v29
	v_cvt_pk_f16_f32 v29, v30, v31
	v_cvt_pk_f16_f32 v30, v24, v25
	v_cvt_pk_f16_f32 v31, v26, v27
	s_waitcnt lgkmcnt(0)
	v_add_u32_e32 v83, 0x36000, v225
	buffer_store_dwordx4 v[128:131], v83, s[24:27], 0 offen nt
	v_add_u32_e32 v82, 0x39000, v225
	buffer_store_dwordx4 v[104:107], v82, s[24:27], 0 offen nt
	ds_write_b128 v235, v[28:31]
	v_fma_mix_f32 v210, v28, 1.0, 0 op_sel_hi:[1,0,0]
	v_fma_mix_f32 v211, v28, v28, 0 op_sel_hi:[1,1,0]
	v_fma_mix_f32 v210, v28, 1.0, v210 op_sel:[1,0,0] op_sel_hi:[1,0,0]
	v_fma_mix_f32 v211, v28, v28, v211 op_sel:[1,1,0] op_sel_hi:[1,1,0]
	v_fma_mix_f32 v210, v29, 1.0, v210 op_sel_hi:[1,0,0]
	v_fma_mix_f32 v211, v29, v29, v211 op_sel_hi:[1,1,0]
	v_fma_mix_f32 v210, v29, 1.0, v210 op_sel:[1,0,0] op_sel_hi:[1,0,0]
	v_fma_mix_f32 v211, v29, v29, v211 op_sel:[1,1,0] op_sel_hi:[1,1,0]
	v_fma_mix_f32 v210, v30, 1.0, v210 op_sel_hi:[1,0,0]
	v_fma_mix_f32 v211, v30, v30, v211 op_sel_hi:[1,1,0]
	v_fma_mix_f32 v210, v30, 1.0, v210 op_sel:[1,0,0] op_sel_hi:[1,0,0]
	v_fma_mix_f32 v211, v30, v30, v211 op_sel:[1,1,0] op_sel_hi:[1,1,0]
	v_fma_mix_f32 v210, v31, 1.0, v210 op_sel_hi:[1,0,0]
	v_fma_mix_f32 v211, v31, v31, v211 op_sel_hi:[1,1,0]
	v_fma_mix_f32 v210, v31, 1.0, v210 op_sel:[1,0,0] op_sel_hi:[1,0,0]
	v_fma_mix_f32 v211, v31, v31, v211 op_sel:[1,1,0] op_sel_hi:[1,1,0]
	s_waitcnt vmcnt(12)
	v_cvt_f32_f16_e32 v72, v144
	v_cvt_f32_f16_sdwa v73, v144 dst_sel:DWORD dst_unused:UNUSED_PAD src0_sel:WORD_1
	v_cvt_f32_f16_e32 v74, v145
	v_cvt_f32_f16_sdwa v75, v145 dst_sel:DWORD dst_unused:UNUSED_PAD src0_sel:WORD_1
	v_cvt_f32_f16_e32 v80, v146
	v_cvt_f32_f16_sdwa v81, v146 dst_sel:DWORD dst_unused:UNUSED_PAD src0_sel:WORD_1
	v_cvt_f32_f16_e32 v82, v147
	v_cvt_f32_f16_sdwa v83, v147 dst_sel:DWORD dst_unused:UNUSED_PAD src0_sel:WORD_1
	v_sub_f32_e32 v72, v72, v202
	v_sub_f32_e32 v73, v73, v202
	v_sub_f32_e32 v74, v74, v202
	v_sub_f32_e32 v75, v75, v202
	v_sub_f32_e32 v80, v80, v202
	v_sub_f32_e32 v81, v81, v202
	v_sub_f32_e32 v82, v82, v202
	v_sub_f32_e32 v83, v83, v202
	v_pk_mul_f32 v[72:73], v[202:203], v[72:73] op_sel:[1,0]
	v_pk_mul_f32 v[74:75], v[202:203], v[74:75] op_sel:[1,0]
	v_pk_mul_f32 v[80:81], v[202:203], v[80:81] op_sel:[1,0]
	v_pk_mul_f32 v[82:83], v[202:203], v[82:83] op_sel:[1,0]
	v_pk_fma_f32 v[20:21], v[72:73], v[168:169], v[20:21]
	v_pk_fma_f32 v[22:23], v[74:75], v[170:171], v[22:23]
	v_pk_fma_f32 v[16:17], v[80:81], v[172:173], v[16:17]
	v_pk_fma_f32 v[18:19], v[82:83], v[174:175], v[18:19]
	v_cvt_pk_f16_f32 v20, v20, v21
	v_cvt_pk_f16_f32 v21, v22, v23
	v_cvt_pk_f16_f32 v22, v16, v17
	v_cvt_pk_f16_f32 v23, v18, v19
	ds_write_b128 v235, v[20:23] offset:64
	v_fma_mix_f32 v210, v20, 1.0, v210 op_sel_hi:[1,0,0]
	v_fma_mix_f32 v211, v20, v20, v211 op_sel_hi:[1,1,0]
	v_fma_mix_f32 v210, v20, 1.0, v210 op_sel:[1,0,0] op_sel_hi:[1,0,0]
	v_fma_mix_f32 v211, v20, v20, v211 op_sel:[1,1,0] op_sel_hi:[1,1,0]
	v_fma_mix_f32 v210, v21, 1.0, v210 op_sel_hi:[1,0,0]
	v_fma_mix_f32 v211, v21, v21, v211 op_sel_hi:[1,1,0]
	v_fma_mix_f32 v210, v21, 1.0, v210 op_sel:[1,0,0] op_sel_hi:[1,0,0]
	v_fma_mix_f32 v211, v21, v21, v211 op_sel:[1,1,0] op_sel_hi:[1,1,0]
	v_fma_mix_f32 v210, v22, 1.0, v210 op_sel_hi:[1,0,0]
	v_fma_mix_f32 v211, v22, v22, v211 op_sel_hi:[1,1,0]
	v_fma_mix_f32 v210, v22, 1.0, v210 op_sel:[1,0,0] op_sel_hi:[1,0,0]
	v_fma_mix_f32 v211, v22, v22, v211 op_sel:[1,1,0] op_sel_hi:[1,1,0]
	v_fma_mix_f32 v210, v23, 1.0, v210 op_sel_hi:[1,0,0]
	v_fma_mix_f32 v211, v23, v23, v211 op_sel_hi:[1,1,0]
	v_fma_mix_f32 v210, v23, 1.0, v210 op_sel:[1,0,0] op_sel_hi:[1,0,0]
	v_fma_mix_f32 v211, v23, v23, v211 op_sel:[1,1,0] op_sel_hi:[1,1,0]
	ds_read_b128 v[240:243], v236
	ds_read_b128 v[96:99], v236 offset:1152
	s_waitcnt vmcnt(11)
	v_cvt_f32_f16_e32 v72, v132
	v_cvt_f32_f16_sdwa v73, v132 dst_sel:DWORD dst_unused:UNUSED_PAD src0_sel:WORD_1
	v_cvt_f32_f16_e32 v74, v133
	v_cvt_f32_f16_sdwa v75, v133 dst_sel:DWORD dst_unused:UNUSED_PAD src0_sel:WORD_1
	v_cvt_f32_f16_e32 v80, v134
	v_cvt_f32_f16_sdwa v81, v134 dst_sel:DWORD dst_unused:UNUSED_PAD src0_sel:WORD_1
	v_cvt_f32_f16_e32 v82, v135
	v_cvt_f32_f16_sdwa v83, v135 dst_sel:DWORD dst_unused:UNUSED_PAD src0_sel:WORD_1
	v_sub_f32_e32 v72, v72, v204
	v_sub_f32_e32 v73, v73, v204
	v_sub_f32_e32 v74, v74, v204
	v_sub_f32_e32 v75, v75, v204
	v_sub_f32_e32 v80, v80, v204
	v_sub_f32_e32 v81, v81, v204
	v_sub_f32_e32 v82, v82, v204
	v_sub_f32_e32 v83, v83, v204
	v_pk_mul_f32 v[72:73], v[204:205], v[72:73] op_sel:[1,0]
	v_pk_mul_f32 v[74:75], v[204:205], v[74:75] op_sel:[1,0]
	v_pk_mul_f32 v[80:81], v[204:205], v[80:81] op_sel:[1,0]
	v_pk_mul_f32 v[82:83], v[204:205], v[82:83] op_sel:[1,0]
	v_pk_fma_f32 v[12:13], v[72:73], v[160:161], v[12:13]
	v_pk_fma_f32 v[14:15], v[74:75], v[162:163], v[14:15]
	v_pk_fma_f32 v[8:9], v[80:81], v[164:165], v[8:9]
	v_pk_fma_f32 v[10:11], v[82:83], v[166:167], v[10:11]
	v_cvt_pk_f16_f32 v12, v12, v13
	v_cvt_pk_f16_f32 v13, v14, v15
	v_cvt_pk_f16_f32 v14, v8, v9
	v_cvt_pk_f16_f32 v15, v10, v11
	s_waitcnt lgkmcnt(0)
	v_add_u32_e32 v83, 0x3c000, v225
	buffer_store_dwordx4 v[240:243], v83, s[24:27], 0 offen nt
	v_add_u32_e32 v82, 0x3f000, v225
	buffer_store_dwordx4 v[96:99], v82, s[24:27], 0 offen nt
	ds_write_b128 v235, v[12:15]
	v_fma_mix_f32 v244, v12, 1.0, 0 op_sel_hi:[1,0,0]
	v_fma_mix_f32 v245, v12, v12, 0 op_sel_hi:[1,1,0]
	v_fma_mix_f32 v244, v12, 1.0, v244 op_sel:[1,0,0] op_sel_hi:[1,0,0]
	v_fma_mix_f32 v245, v12, v12, v245 op_sel:[1,1,0] op_sel_hi:[1,1,0]
	v_fma_mix_f32 v244, v13, 1.0, v244 op_sel_hi:[1,0,0]
	v_fma_mix_f32 v245, v13, v13, v245 op_sel_hi:[1,1,0]
	v_fma_mix_f32 v244, v13, 1.0, v244 op_sel:[1,0,0] op_sel_hi:[1,0,0]
	v_fma_mix_f32 v245, v13, v13, v245 op_sel:[1,1,0] op_sel_hi:[1,1,0]
	v_fma_mix_f32 v244, v14, 1.0, v244 op_sel_hi:[1,0,0]
	v_fma_mix_f32 v245, v14, v14, v245 op_sel_hi:[1,1,0]
	v_fma_mix_f32 v244, v14, 1.0, v244 op_sel:[1,0,0] op_sel_hi:[1,0,0]
	v_fma_mix_f32 v245, v14, v14, v245 op_sel:[1,1,0] op_sel_hi:[1,1,0]
	v_fma_mix_f32 v244, v15, 1.0, v244 op_sel_hi:[1,0,0]
	v_fma_mix_f32 v245, v15, v15, v245 op_sel_hi:[1,1,0]
	v_fma_mix_f32 v244, v15, 1.0, v244 op_sel:[1,0,0] op_sel_hi:[1,0,0]
	v_fma_mix_f32 v245, v15, v15, v245 op_sel:[1,1,0] op_sel_hi:[1,1,0]
	s_waitcnt vmcnt(12)
	v_cvt_f32_f16_e32 v72, v88
	v_cvt_f32_f16_sdwa v73, v88 dst_sel:DWORD dst_unused:UNUSED_PAD src0_sel:WORD_1
	v_cvt_f32_f16_e32 v74, v89
	v_cvt_f32_f16_sdwa v75, v89 dst_sel:DWORD dst_unused:UNUSED_PAD src0_sel:WORD_1
	v_cvt_f32_f16_e32 v80, v90
	v_cvt_f32_f16_sdwa v81, v90 dst_sel:DWORD dst_unused:UNUSED_PAD src0_sel:WORD_1
	v_cvt_f32_f16_e32 v82, v91
	v_cvt_f32_f16_sdwa v83, v91 dst_sel:DWORD dst_unused:UNUSED_PAD src0_sel:WORD_1
	v_sub_f32_e32 v72, v72, v204
	v_sub_f32_e32 v73, v73, v204
	v_sub_f32_e32 v74, v74, v204
	v_sub_f32_e32 v75, v75, v204
	v_sub_f32_e32 v80, v80, v204
	v_sub_f32_e32 v81, v81, v204
	v_sub_f32_e32 v82, v82, v204
	v_sub_f32_e32 v83, v83, v204
	v_pk_mul_f32 v[72:73], v[204:205], v[72:73] op_sel:[1,0]
	v_pk_mul_f32 v[74:75], v[204:205], v[74:75] op_sel:[1,0]
	v_pk_mul_f32 v[80:81], v[204:205], v[80:81] op_sel:[1,0]
	v_pk_mul_f32 v[82:83], v[204:205], v[82:83] op_sel:[1,0]
	v_pk_fma_f32 v[4:5], v[72:73], v[168:169], v[4:5]
	v_pk_fma_f32 v[6:7], v[74:75], v[170:171], v[6:7]
	v_pk_fma_f32 v[0:1], v[80:81], v[172:173], v[0:1]
	v_pk_fma_f32 v[2:3], v[82:83], v[174:175], v[2:3]
	v_cvt_pk_f16_f32 v4, v4, v5
	v_cvt_pk_f16_f32 v5, v6, v7
	v_cvt_pk_f16_f32 v6, v0, v1
	v_cvt_pk_f16_f32 v7, v2, v3
	ds_write_b128 v235, v[4:7] offset:64
	v_fma_mix_f32 v244, v4, 1.0, v244 op_sel_hi:[1,0,0]
	v_fma_mix_f32 v245, v4, v4, v245 op_sel_hi:[1,1,0]
	v_fma_mix_f32 v244, v4, 1.0, v244 op_sel:[1,0,0] op_sel_hi:[1,0,0]
	v_fma_mix_f32 v245, v4, v4, v245 op_sel:[1,1,0] op_sel_hi:[1,1,0]
	v_fma_mix_f32 v244, v5, 1.0, v244 op_sel_hi:[1,0,0]
	v_fma_mix_f32 v245, v5, v5, v245 op_sel_hi:[1,1,0]
	v_fma_mix_f32 v244, v5, 1.0, v244 op_sel:[1,0,0] op_sel_hi:[1,0,0]
	v_fma_mix_f32 v245, v5, v5, v245 op_sel:[1,1,0] op_sel_hi:[1,1,0]
	v_fma_mix_f32 v244, v6, 1.0, v244 op_sel_hi:[1,0,0]
	v_fma_mix_f32 v245, v6, v6, v245 op_sel_hi:[1,1,0]
	v_fma_mix_f32 v244, v6, 1.0, v244 op_sel:[1,0,0] op_sel_hi:[1,0,0]
	v_fma_mix_f32 v245, v6, v6, v245 op_sel:[1,1,0] op_sel_hi:[1,1,0]
	v_fma_mix_f32 v244, v7, 1.0, v244 op_sel_hi:[1,0,0]
	v_fma_mix_f32 v245, v7, v7, v245 op_sel_hi:[1,1,0]
	v_fma_mix_f32 v244, v7, 1.0, v244 op_sel:[1,0,0] op_sel_hi:[1,0,0]
	v_fma_mix_f32 v245, v7, v7, v245 op_sel:[1,1,0] op_sel_hi:[1,1,0]
	ds_read_b128 v[108:111], v236
	ds_read_b128 v[100:103], v236 offset:1152
	s_waitcnt lgkmcnt(0)
	v_add_u32_e32 v83, 0x42000, v225
	buffer_store_dwordx4 v[108:111], v83, s[24:27], 0 offen nt
	v_add_u32_e32 v82, 0x45000, v225
	buffer_store_dwordx4 v[100:103], v82, s[24:27], 0 offen nt
	v_xor_b32_e32 v246, 16, v234
	v_lshlrev_b32_e32 v246, 2, v246
	v_xor_b32_e32 v247, 32, v234
	v_lshlrev_b32_e32 v247, 2, v247
	ds_bpermute_b32 v92, v246, v206
	ds_bpermute_b32 v93, v246, v207
	ds_bpermute_b32 v94, v246, v140
	ds_bpermute_b32 v95, v246, v141
	ds_bpermute_b32 v120, v246, v142
	ds_bpermute_b32 v121, v246, v143
	ds_bpermute_b32 v122, v246, v216
	ds_bpermute_b32 v123, v246, v217
	s_waitcnt lgkmcnt(0)
	v_pk_add_f32 v[206:207], v[206:207], v[92:93]
	v_pk_add_f32 v[140:141], v[140:141], v[94:95]
	v_pk_add_f32 v[142:143], v[142:143], v[120:121]
	v_pk_add_f32 v[216:217], v[216:217], v[122:123]
	ds_bpermute_b32 v92, v246, v218
	ds_bpermute_b32 v93, v246, v219
	ds_bpermute_b32 v94, v246, v208
	ds_bpermute_b32 v95, v246, v209
	ds_bpermute_b32 v120, v246, v210
	ds_bpermute_b32 v121, v246, v211
	ds_bpermute_b32 v122, v246, v244
	ds_bpermute_b32 v123, v246, v245
	s_waitcnt lgkmcnt(0)
	v_pk_add_f32 v[218:219], v[218:219], v[92:93]
	v_pk_add_f32 v[208:209], v[208:209], v[94:95]
	v_pk_add_f32 v[210:211], v[210:211], v[120:121]
	v_pk_add_f32 v[244:245], v[244:245], v[122:123]
	ds_bpermute_b32 v92, v247, v206
	ds_bpermute_b32 v93, v247, v207
	ds_bpermute_b32 v94, v247, v140
	ds_bpermute_b32 v95, v247, v141
	ds_bpermute_b32 v120, v247, v142
	ds_bpermute_b32 v121, v247, v143
	ds_bpermute_b32 v122, v247, v216
	ds_bpermute_b32 v123, v247, v217
	s_waitcnt lgkmcnt(0)
	v_pk_add_f32 v[206:207], v[206:207], v[92:93]
	v_pk_add_f32 v[140:141], v[140:141], v[94:95]
	v_pk_add_f32 v[142:143], v[142:143], v[120:121]
	v_pk_add_f32 v[216:217], v[216:217], v[122:123]
	ds_bpermute_b32 v92, v247, v218
	ds_bpermute_b32 v93, v247, v219
	ds_bpermute_b32 v94, v247, v208
	ds_bpermute_b32 v95, v247, v209
	ds_bpermute_b32 v120, v247, v210
	ds_bpermute_b32 v121, v247, v211
	ds_bpermute_b32 v122, v247, v244
	ds_bpermute_b32 v123, v247, v245
	s_waitcnt lgkmcnt(0)
	v_pk_add_f32 v[218:219], v[218:219], v[92:93]
	v_pk_add_f32 v[208:209], v[208:209], v[94:95]
	v_pk_add_f32 v[210:211], v[210:211], v[120:121]
	v_pk_add_f32 v[244:245], v[244:245], v[122:123]
	global_store_dwordx2 v224, v[206:207], s[100:101] offset:-2048
	global_store_dwordx2 v224, v[140:141], s[100:101] offset:-512
	global_store_dwordx2 v224, v[142:143], s[100:101] offset:1024
	global_store_dwordx2 v224, v[216:217], s[100:101] offset:2560
	s_add_u32 s100, s100, 0x3000
	s_addc_u32 s101, s101, 0
	global_store_dwordx2 v224, v[218:219], s[100:101] offset:-2048
	global_store_dwordx2 v224, v[208:209], s[100:101] offset:-512
	global_store_dwordx2 v224, v[210:211], s[100:101] offset:1024
	global_store_dwordx2 v224, v[244:245], s[100:101] offset:2560
	s_mov_b32 s83, s81
	s_mov_b32 s84, s82
	s_mov_b64 s[40:41], s[0:1]
	s_mov_b64 s[38:39], s[8:9]
	s_mov_b64 vcc, s[6:7]
	s_cbranch_vccz .LBB10_12
	s_waitcnt vmcnt(0)
	s_cmpk_gt_u32 s44, 0xff
	s_cbranch_scc1 .LBB10_31
	s_barrier

.LBB10_32:
	s_endpgm
	s_endpgm
	s_endpgm
	s_endpgm
	s_endpgm
	s_endpgm
	s_endpgm
	s_endpgm
	s_endpgm
	s_endpgm
	s_endpgm
	s_endpgm
	s_endpgm
	s_endpgm
	s_endpgm
	s_endpgm
	s_endpgm
	s_endpgm
	s_endpgm
	s_endpgm
	s_endpgm
	s_endpgm
	s_endpgm
	s_endpgm
	s_endpgm
	s_endpgm
	s_endpgm
	s_endpgm
	s_endpgm
	s_endpgm
	s_endpgm
	s_endpgm
	s_endpgm
	s_endpgm
	s_endpgm
	s_endpgm
	s_endpgm
	s_endpgm
	s_endpgm
	s_endpgm
	s_endpgm
	s_endpgm
	s_endpgm
	s_endpgm
	s_endpgm
	s_endpgm
	.section	.rodata,"a",@progbits
	.p2align	6, 0x0
	.amdhsa_kernel _Z6k_gemmIN2pg6EpiResELi3072EEvNS0_4GemmET_
		.amdhsa_group_segment_fixed_size 0
		.amdhsa_private_segment_fixed_size 0
		.amdhsa_kernarg_size 344
		.amdhsa_user_sgpr_count 2
		.amdhsa_user_sgpr_dispatch_ptr 0
		.amdhsa_user_sgpr_queue_ptr 0
		.amdhsa_user_sgpr_kernarg_segment_ptr 1
		.amdhsa_user_sgpr_dispatch_id 0
		.amdhsa_user_sgpr_kernarg_preload_length 0
		.amdhsa_user_sgpr_kernarg_preload_offset 0
		.amdhsa_user_sgpr_private_segment_size 0
		.amdhsa_uses_dynamic_stack 0
		.amdhsa_enable_private_segment 0
		.amdhsa_system_sgpr_workgroup_id_x 1
		.amdhsa_system_sgpr_workgroup_id_y 0
		.amdhsa_system_sgpr_workgroup_id_z 0
		.amdhsa_system_sgpr_workgroup_info 0
		.amdhsa_system_vgpr_workitem_id 0
		.amdhsa_next_free_vgpr 256
		.amdhsa_next_free_sgpr 102
		.amdhsa_accum_offset 256
		.amdhsa_reserve_vcc 1
		.amdhsa_float_round_mode_32 0
		.amdhsa_float_round_mode_16_64 0
		.amdhsa_float_denorm_mode_32 3
		.amdhsa_float_denorm_mode_16_64 3
		.amdhsa_dx10_clamp 1
		.amdhsa_ieee_mode 1
		.amdhsa_fp16_overflow 0
		.amdhsa_tg_split 0
		.amdhsa_exception_fp_ieee_invalid_op 0
		.amdhsa_exception_fp_denorm_src 0
		.amdhsa_exception_fp_ieee_div_zero 0
		.amdhsa_exception_fp_ieee_overflow 0
		.amdhsa_exception_fp_ieee_underflow 0
		.amdhsa_exception_fp_ieee_inexact 0
		.amdhsa_exception_int_div_zero 0
	.end_amdhsa_kernel

amdhsa.kernels:
  - .agpr_count:     16
    .args:
      - .actual_access:  read_only
        .address_space:  global
        .offset:         0
        .size:           8
        .value_kind:     global_buffer
      - .actual_access:  read_only
        .address_space:  global
        .offset:         8
        .size:           8
        .value_kind:     global_buffer
      - .actual_access:  write_only
        .address_space:  global
        .offset:         16
        .size:           8
        .value_kind:     global_buffer
    .group_segment_fixed_size: 45056
    .kernarg_segment_align: 8
    .kernarg_segment_size: 24
    .language:       OpenCL C
    .language_version:
      - 2
      - 0
    .max_flat_workgroup_size: 256
    .name:           _Z6k_attnPKDF16_PKfPDF16_
    .private_segment_fixed_size: 0
    .sgpr_count:     16
    .sgpr_spill_count: 0
    .symbol:         _Z6k_attnPKDF16_PKfPDF16_.kd
    .uniform_work_group_size: 1
    .uses_dynamic_stack: false
    .vgpr_count:     84
    .vgpr_spill_count: 0
    .wavefront_size: 64
  - .agpr_count:     0
    .args:
      - .actual_access:  read_only
        .address_space:  global
        .offset:         0
        .size:           8
        .value_kind:     global_buffer
      - .actual_access:  read_only
        .address_space:  global
        .offset:         8
        .size:           8
        .value_kind:     global_buffer
      - .actual_access:  write_only
        .address_space:  global
        .offset:         16
        .size:           8
        .value_kind:     global_buffer
      - .actual_access:  write_only
        .address_space:  global
        .offset:         24
        .size:           8
        .value_kind:     global_buffer
      - .actual_access:  write_only
        .address_space:  global
        .offset:         32
        .size:           8
        .value_kind:     global_buffer
      - .actual_access:  write_only
        .address_space:  global
        .offset:         40
        .size:           8
        .value_kind:     global_buffer
    .group_segment_fixed_size: 0
    .kernarg_segment_align: 8
    .kernarg_segment_size: 48
    .language:       OpenCL C
    .language_version:
      - 2
      - 0
    .max_flat_workgroup_size: 256
    .name:           _Z11k_prep_miscPKiPKfPfPDv2_fS3_S3_
    .private_segment_fixed_size: 0
    .sgpr_count:     16
    .sgpr_spill_count: 0
    .symbol:         _Z11k_prep_miscPKiPKfPfPDv2_fS3_S3_.kd
    .uniform_work_group_size: 1
    .uses_dynamic_stack: false
    .vgpr_count:     6
    .vgpr_spill_count: 0
    .wavefront_size: 64
  - .agpr_count:     0
    .args:
      - .actual_access:  read_only
        .address_space:  global
        .offset:         0
        .size:           8
        .value_kind:     global_buffer
      - .actual_access:  write_only
        .address_space:  global
        .offset:         8
        .size:           8
        .value_kind:     global_buffer
    .group_segment_fixed_size: 0
    .kernarg_segment_align: 8
    .kernarg_segment_size: 16
    .language:       OpenCL C
    .language_version:
      - 2
      - 0
    .max_flat_workgroup_size: 256
    .name:           _Z7k_cvt_xPKfPDF16_
    .private_segment_fixed_size: 0
    .sgpr_count:     14
    .sgpr_spill_count: 0
    .symbol:         _Z7k_cvt_xPKfPDF16_.kd
    .uniform_work_group_size: 1
    .uses_dynamic_stack: false
    .vgpr_count:     12
    .vgpr_spill_count: 0
    .wavefront_size: 64
  - .agpr_count:     0
    .args:
      - .offset:         0
        .size:           176
        .value_kind:     by_value
    .group_segment_fixed_size: 9216
    .kernarg_segment_align: 8
    .kernarg_segment_size: 176
    .language:       OpenCL C
    .language_version:
      - 2
      - 0
    .max_flat_workgroup_size: 256
    .name:           _Z8k_wtrans8PrepArgs
    .private_segment_fixed_size: 0
    .sgpr_count:     44
    .sgpr_spill_count: 0
    .symbol:         _Z8k_wtrans8PrepArgs.kd
    .uniform_work_group_size: 1
    .uses_dynamic_stack: false
    .vgpr_count:     18
    .vgpr_spill_count: 0
    .wavefront_size: 64
  - .agpr_count:     0
    .args:
      - .offset:         0
        .size:           176
        .value_kind:     by_value
      - .actual_access:  read_only
        .address_space:  global
        .offset:         176
        .size:           8
        .value_kind:     global_buffer
      - .actual_access:  read_only
        .address_space:  global
        .offset:         184
        .size:           8
        .value_kind:     global_buffer
    .group_segment_fixed_size: 2048
    .kernarg_segment_align: 8
    .kernarg_segment_size: 192
    .language:       OpenCL C
    .language_version:
      - 2
      - 0
    .max_flat_workgroup_size: 256
    .name:           _Z8k_colvec8PrepArgsPKfS1_
    .private_segment_fixed_size: 0
    .sgpr_count:     38
    .sgpr_spill_count: 0
    .symbol:         _Z8k_colvec8PrepArgsPKfS1_.kd
    .uniform_work_group_size: 1
    .uses_dynamic_stack: false
    .vgpr_count:     114
    .vgpr_spill_count: 0
    .wavefront_size: 64
  - .agpr_count:     0
    .args:
      - .actual_access:  read_only
        .address_space:  global
        .offset:         0
        .size:           8
        .value_kind:     global_buffer
      - .actual_access:  write_only
        .address_space:  global
        .offset:         8
        .size:           8
        .value_kind:     global_buffer
    .group_segment_fixed_size: 0
    .kernarg_segment_align: 8
    .kernarg_segment_size: 16
    .language:       OpenCL C
    .language_version:
      - 2
      - 0
    .max_flat_workgroup_size: 256
    .name:           _Z9k_rowstatPKDv2_fPS_
    .private_segment_fixed_size: 0
    .sgpr_count:     14
    .sgpr_spill_count: 0
    .symbol:         _Z9k_rowstatPKDv2_fPS_.kd
    .uniform_work_group_size: 1
    .uses_dynamic_stack: false
    .vgpr_count:     28
    .vgpr_spill_count: 0
    .wavefront_size: 64
  - .agpr_count:     0
    .args:
      - .actual_access:  read_only
        .address_space:  global
        .offset:         0
        .size:           8
        .value_kind:     global_buffer
      - .actual_access:  read_only
        .address_space:  global
        .offset:         8
        .size:           8
        .value_kind:     global_buffer
      - .actual_access:  read_only
        .address_space:  global
        .offset:         16
        .size:           8
        .value_kind:     global_buffer
      - .actual_access:  read_only
        .address_space:  global
        .offset:         24
        .size:           8
        .value_kind:     global_buffer
      - .actual_access:  write_only
        .address_space:  global
        .offset:         32
        .size:           8
        .value_kind:     global_buffer
    .group_segment_fixed_size: 0
    .kernarg_segment_align: 8
    .kernarg_segment_size: 40
    .language:       OpenCL C
    .language_version:
      - 2
      - 0
    .max_flat_workgroup_size: 256
    .name:           _Z10k_final_lnPKDF16_PKDv2_fPKfS5_Pf
    .private_segment_fixed_size: 0
    .sgpr_count:     19
    .sgpr_spill_count: 0
    .symbol:         _Z10k_final_lnPKDF16_PKDv2_fPKfS5_Pf.kd
    .uniform_work_group_size: 1
    .uses_dynamic_stack: false
    .vgpr_count:     19
    .vgpr_spill_count: 0
    .wavefront_size: 64
  - .agpr_count:     0
    .args:
      - .offset:         0
        .size:           32
        .value_kind:     by_value
      - .offset:         32
        .size:           32
        .value_kind:     by_value
      - .offset:         64
        .size:           4
        .value_kind:     hidden_block_count_x
      - .offset:         68
        .size:           4
        .value_kind:     hidden_block_count_y
      - .offset:         72
        .size:           4
        .value_kind:     hidden_block_count_z
      - .offset:         76
        .size:           2
        .value_kind:     hidden_group_size_x
      - .offset:         78
        .size:           2
        .value_kind:     hidden_group_size_y
      - .offset:         80
        .size:           2
        .value_kind:     hidden_group_size_z
      - .offset:         82
        .size:           2
        .value_kind:     hidden_remainder_x
      - .offset:         84
        .size:           2
        .value_kind:     hidden_remainder_y
      - .offset:         86
        .size:           2
        .value_kind:     hidden_remainder_z
      - .offset:         104
        .size:           8
        .value_kind:     hidden_global_offset_x
      - .offset:         112
        .size:           8
        .value_kind:     hidden_global_offset_y
      - .offset:         120
        .size:           8
        .value_kind:     hidden_global_offset_z
      - .offset:         128
        .size:           2
        .value_kind:     hidden_grid_dims
      - .offset:         184
        .size:           4
        .value_kind:     hidden_dynamic_lds_size
    .group_segment_fixed_size: 0
    .kernarg_segment_align: 8
    .kernarg_segment_size: 320
    .language:       OpenCL C
    .language_version:
      - 2
      - 0
    .max_flat_workgroup_size: 512
    .name:           _Z6k_gemmIN2pg6EpiLinILi0EEELi768EEvNS0_4GemmET_
    .private_segment_fixed_size: 0
    .sgpr_count:     83
    .sgpr_spill_count: 0
    .symbol:         _Z6k_gemmIN2pg6EpiLinILi0EEELi768EEvNS0_4GemmET_.kd
    .uniform_work_group_size: 1
    .uses_dynamic_stack: false
    .vgpr_count:     254
    .vgpr_spill_count: 0
    .wavefront_size: 64
  - .agpr_count:     0
    .args:
      - .offset:         0
        .size:           32
        .value_kind:     by_value
      - .offset:         32
        .size:           56
        .value_kind:     by_value
      - .offset:         88
        .size:           4
        .value_kind:     hidden_block_count_x
      - .offset:         92
        .size:           4
        .value_kind:     hidden_block_count_y
      - .offset:         96
        .size:           4
        .value_kind:     hidden_block_count_z
      - .offset:         100
        .size:           2
        .value_kind:     hidden_group_size_x
      - .offset:         102
        .size:           2
        .value_kind:     hidden_group_size_y
      - .offset:         104
        .size:           2
        .value_kind:     hidden_group_size_z
      - .offset:         106
        .size:           2
        .value_kind:     hidden_remainder_x
      - .offset:         108
        .size:           2
        .value_kind:     hidden_remainder_y
      - .offset:         110
        .size:           2
        .value_kind:     hidden_remainder_z
      - .offset:         128
        .size:           8
        .value_kind:     hidden_global_offset_x
      - .offset:         136
        .size:           8
        .value_kind:     hidden_global_offset_y
      - .offset:         144
        .size:           8
        .value_kind:     hidden_global_offset_z
      - .offset:         152
        .size:           2
        .value_kind:     hidden_grid_dims
      - .offset:         208
        .size:           4
        .value_kind:     hidden_dynamic_lds_size
    .group_segment_fixed_size: 0
    .kernarg_segment_align: 8
    .kernarg_segment_size: 344
    .language:       OpenCL C
    .language_version:
      - 2
      - 0
    .max_flat_workgroup_size: 512
    .name:           _Z6k_gemmIN2pg6EpiResELi768EEvNS0_4GemmET_
    .private_segment_fixed_size: 0
    .sgpr_count:     108
    .sgpr_spill_count: 0
    .symbol:         _Z6k_gemmIN2pg6EpiResELi768EEvNS0_4GemmET_.kd
    .uniform_work_group_size: 1
    .uses_dynamic_stack: false
    .vgpr_count:     256
    .vgpr_spill_count: 0
    .wavefront_size: 64
  - .agpr_count:     0
    .args:
      - .offset:         0
        .size:           32
        .value_kind:     by_value
      - .offset:         32
        .size:           32
        .value_kind:     by_value
      - .offset:         64
        .size:           4
        .value_kind:     hidden_block_count_x
      - .offset:         68
        .size:           4
        .value_kind:     hidden_block_count_y
      - .offset:         72
        .size:           4
        .value_kind:     hidden_block_count_z
      - .offset:         76
        .size:           2
        .value_kind:     hidden_group_size_x
      - .offset:         78
        .size:           2
        .value_kind:     hidden_group_size_y
      - .offset:         80
        .size:           2
        .value_kind:     hidden_group_size_z
      - .offset:         82
        .size:           2
        .value_kind:     hidden_remainder_x
      - .offset:         84
        .size:           2
        .value_kind:     hidden_remainder_y
      - .offset:         86
        .size:           2
        .value_kind:     hidden_remainder_z
      - .offset:         104
        .size:           8
        .value_kind:     hidden_global_offset_x
      - .offset:         112
        .size:           8
        .value_kind:     hidden_global_offset_y
      - .offset:         120
        .size:           8
        .value_kind:     hidden_global_offset_z
      - .offset:         128
        .size:           2
        .value_kind:     hidden_grid_dims
      - .offset:         184
        .size:           4
        .value_kind:     hidden_dynamic_lds_size
    .group_segment_fixed_size: 0
    .kernarg_segment_align: 8
    .kernarg_segment_size: 320
    .language:       OpenCL C
    .language_version:
      - 2
      - 0
    .max_flat_workgroup_size: 512
    .name:           _Z6k_gemmIN2pg6EpiLinILi1EEELi768EEvNS0_4GemmET_
    .private_segment_fixed_size: 0
    .sgpr_count:     83
    .sgpr_spill_count: 0
    .symbol:         _Z6k_gemmIN2pg6EpiLinILi1EEELi768EEvNS0_4GemmET_.kd
    .uniform_work_group_size: 1
    .uses_dynamic_stack: false
    .vgpr_count:     254
    .vgpr_spill_count: 0
    .wavefront_size: 64
  - .agpr_count:     0
    .args:
      - .offset:         0
        .size:           32
        .value_kind:     by_value
      - .offset:         32
        .size:           56
        .value_kind:     by_value
      - .offset:         88
        .size:           4
        .value_kind:     hidden_block_count_x
      - .offset:         92
        .size:           4
        .value_kind:     hidden_block_count_y
      - .offset:         96
        .size:           4
        .value_kind:     hidden_block_count_z
      - .offset:         100
        .size:           2
        .value_kind:     hidden_group_size_x
      - .offset:         102
        .size:           2
        .value_kind:     hidden_group_size_y
      - .offset:         104
        .size:           2
        .value_kind:     hidden_group_size_z
      - .offset:         106
        .size:           2
        .value_kind:     hidden_remainder_x
      - .offset:         108
        .size:           2
        .value_kind:     hidden_remainder_y
      - .offset:         110
        .size:           2
        .value_kind:     hidden_remainder_z
      - .offset:         128
        .size:           8
        .value_kind:     hidden_global_offset_x
      - .offset:         136
        .size:           8
        .value_kind:     hidden_global_offset_y
      - .offset:         144
        .size:           8
        .value_kind:     hidden_global_offset_z
      - .offset:         152
        .size:           2
        .value_kind:     hidden_grid_dims
      - .offset:         208
        .size:           4
        .value_kind:     hidden_dynamic_lds_size
    .group_segment_fixed_size: 0
    .kernarg_segment_align: 8
    .kernarg_segment_size: 344
    .language:       OpenCL C
    .language_version:
      - 2
      - 0
    .max_flat_workgroup_size: 512
    .name:           _Z6k_gemmIN2pg6EpiResELi3072EEvNS0_4GemmET_
    .private_segment_fixed_size: 0
    .sgpr_count:     108
    .sgpr_spill_count: 0
    .symbol:         _Z6k_gemmIN2pg6EpiResELi3072EEvNS0_4GemmET_.kd
    .uniform_work_group_size: 1
    .uses_dynamic_stack: false
    .vgpr_count:     256
    .vgpr_spill_count: 0
    .wavefront_size: 64
